# v80 with the odd-chunk placeholder scale loads removed and the counted vmcnt waits of both loop bodies recomputed
# speedup vs baseline: 1.0339x; 1.0019x over previous
; #define P12_ISSUE(c_, i_, h_, CW_, SC_) do { _Pragma("unroll") for (int bb = 0; bb < 8; ++bb) { const unsigned ro = (unsigned)(c_) * 16384u + (unsigned)EL[(i_) * 128 + ((h_) * 8 + bb) * 8 + g8]; \
;         CW_[bb] = *(const v4u*)(U4 + (size_t)(ro * 128u + 16u * (unsigned)k8)); SC_[bb] = USS[(size_t)(ro * 8u + (unsigned)k8)]; } } while (0)
; #define P12_COMP(i_, h_, CW_, SC_) do { _Pragma("unroll") for (int bb = 0; bb < 8; ++bb) { int a0 = 0, a1 = 0; P12_U4(CW_[bb].x, xa.x, xa.y, a0); P12_U4(CW_[bb].y, xa.z, xa.w, a1); P12_U4(CW_[bb].z, xb.x, xb.y, a0); P12_U4(CW_[bb].w, xb.z, xb.w, a1); \
;         psum[(i_)][(h_) * 8 + bb] += __uint_as_float(SC_[bb] << 16) * (float)((a0 + a1) - xo); } } while (0)
; #define P12_BAR() asm volatile("" ::: "memory")
; __device__ __forceinline__ void p12_peer(Frame& F) {
;     ...
;     { v4u cwA[8], cwB[8]; unsigned scA[8], scB[8]; v4u xa, xb; int xo;
;       P12_ISSUE(0, 0, 0, cwA, scA);
; _Pragma("nounroll")
;       for (int c = 0; c < 16; ++c) { const int cn = c + 1 < 16 ? c + 1 : 15;
;           P12_XQ(c, 0); P12_ISSUE(c, 0, 1, cwB, scB); P12_BAR(); P12_COMP(0, 0, cwA, scA); P12_ISSUE(c, 1, 0, cwA, scA); P12_BAR(); P12_COMP(0, 1, cwB, scB);
;           P12_XQ(c, 1); P12_ISSUE(c, 1, 1, cwB, scB); P12_BAR(); P12_COMP(1, 0, cwA, scA); P12_ISSUE(c, 2, 0, cwA, scA); P12_BAR(); P12_COMP(1, 1, cwB, scB);
;           P12_XQ(c, 2); P12_ISSUE(c, 2, 1, cwB, scB); P12_BAR(); P12_COMP(2, 0, cwA, scA); P12_ISSUE(c, 3, 0, cwA, scA); P12_BAR(); P12_COMP(2, 1, cwB, scB);
;           P12_XQ(c, 3); P12_ISSUE(c, 3, 1, cwB, scB); P12_BAR(); P12_COMP(3, 0, cwA, scA); P12_ISSUE(cn, 0, 0, cwA, scA); P12_BAR(); P12_COMP(3, 1, cwB, scB);
.LBB0_3272:
	s_lshl_b32 s49, s44, 4
	s_sub_u32 s46, s18, s49
	s_subb_u32 s47, s19, 0
	ds_read_b128 v[36:39], v166
	ds_read_b128 v[32:35], v166 offset:16
	ds_read_u16 v44, v93 offset:16512
	ds_read_u16 v45, v93 offset:16528
	ds_read_u16 v46, v93 offset:16544
	ds_read_u16 v47, v93 offset:16560
	v_mov_b32_e32 v48, 0
	s_waitcnt lgkmcnt(3)
	v_add_u32_e32 v44, s44, v44
	v_lshl_or_b32 v49, v44, 7, v165
	global_load_dwordx4 v[88:91], v49, s[0:1]
	v_lshl_or_b32 v49, v44, 5, v248
	s_waitcnt lgkmcnt(2)
	v_add_u32_e32 v44, s44, v45
	v_lshl_or_b32 v45, v44, 7, v165
	v_lshl_or_b32 v50, v44, 5, v248
	s_waitcnt lgkmcnt(1)
	v_add_u32_e32 v44, s44, v46
	global_load_dwordx4 v[84:87], v45, s[0:1]
	v_lshl_or_b32 v45, v44, 7, v165
	v_lshl_or_b32 v51, v44, 5, v248
	s_waitcnt lgkmcnt(0)
	v_add_u32_e32 v44, s44, v47
	global_load_dwordx4 v[80:83], v45, s[0:1]
	v_lshl_or_b32 v45, v44, 7, v165
	v_lshl_or_b32 v56, v44, 5, v248
	ds_read_u16 v44, v93 offset:16576
	global_load_dwordx4 v[76:79], v45, s[0:1]
	v_dot4c_i32_i8_e32 v48, 0x1010101, v36
	v_dot4c_i32_i8_e32 v48, 0x1010101, v37
	v_dot4c_i32_i8_e32 v48, 0x1010101, v38
	s_waitcnt lgkmcnt(0)
	v_add_u32_e32 v44, s44, v44
	v_lshl_or_b32 v45, v44, 7, v165
	v_lshl_or_b32 v57, v44, 5, v248
	ds_read_u16 v44, v93 offset:16592
	global_load_dwordx4 v[68:71], v45, s[0:1]
	v_dot4c_i32_i8_e32 v48, 0x1010101, v39
	v_dot4c_i32_i8_e32 v48, 0x1010101, v32
	v_dot4c_i32_i8_e32 v48, 0x1010101, v33
	s_waitcnt lgkmcnt(0)
	v_add_u32_e32 v44, s44, v44
	v_lshl_or_b32 v45, v44, 7, v165
	v_lshl_or_b32 v58, v44, 5, v248
	ds_read_u16 v44, v93 offset:16608
	global_load_dwordx4 v[60:63], v45, s[0:1]
	v_dot4c_i32_i8_e32 v48, 0x1010101, v34
	v_dot4c_i32_i8_e32 v48, 0x1010101, v35
	s_add_i32 s45, s44, 0x4000
	s_waitcnt lgkmcnt(0)
	v_add_u32_e32 v44, s44, v44
	v_lshl_or_b32 v45, v44, 7, v165
	v_lshl_or_b32 v59, v44, 5, v248
	ds_read_u16 v44, v93 offset:16624
	global_load_dwordx4 v[52:55], v45, s[0:1]
	v_lshlrev_b32_e32 v171, 3, v48
	s_waitcnt vmcnt(14)
	v_and_b32_e32 v48, 0xf0f0f0f, v28
	v_lshrrev_b32_e32 v28, 4, v28
	s_waitcnt lgkmcnt(0)
	v_add_u32_e32 v64, s44, v44
	v_lshl_or_b32 v44, v64, 7, v165
	global_load_dwordx4 v[44:47], v44, s[0:1]
	v_lshl_or_b32 v64, v64, 5, v248
	global_load_dword v193, v50, s[46:47]
	global_load_dword v192, v49, s[46:47]
	global_load_dword v195, v56, s[46:47]
	global_load_dword v194, v51, s[46:47]
	global_load_dword v197, v58, s[46:47]
	global_load_dword v196, v57, s[46:47]
	global_load_dword v199, v64, s[46:47]
	global_load_dword v198, v59, s[46:47]
	v_mov_b32_e32 v49, 0
	v_dot4c_i32_i8_e32 v49, v48, v36
	v_and_b32_e32 v28, 0xf0f0f0f, v28
	v_dot4c_i32_i8_e32 v49, v28, v37
	v_and_b32_e32 v28, 0xf0f0f0f, v29
	v_mov_b32_e32 v48, 0
	v_dot4c_i32_i8_e32 v48, v28, v38
	v_lshrrev_b32_e32 v28, 4, v29
	v_and_b32_e32 v28, 0xf0f0f0f, v28
	v_dot4c_i32_i8_e32 v48, v28, v39
	v_and_b32_e32 v28, 0xf0f0f0f, v30
	v_dot4c_i32_i8_e32 v49, v28, v32
	v_lshrrev_b32_e32 v28, 4, v30
	v_and_b32_e32 v28, 0xf0f0f0f, v28
	v_dot4c_i32_i8_e32 v49, v28, v33
	v_and_b32_e32 v28, 0xf0f0f0f, v31
	v_dot4c_i32_i8_e32 v48, v28, v34
	v_lshrrev_b32_e32 v28, 4, v31
	v_and_b32_e32 v28, 0xf0f0f0f, v28
	v_dot4c_i32_i8_e32 v48, v28, v35
	s_waitcnt vmcnt(22)
	v_and_b32_e32 v28, 0xf0f0f0f, v24
	v_mov_b32_e32 v29, 0
	v_lshrrev_b32_e32 v24, 4, v24
	v_dot4c_i32_i8_e32 v29, v28, v36
	v_and_b32_e32 v24, 0xf0f0f0f, v24
	v_dot4c_i32_i8_e32 v29, v24, v37
	v_and_b32_e32 v24, 0xf0f0f0f, v25
	v_mov_b32_e32 v28, 0
	v_dot4c_i32_i8_e32 v28, v24, v38
	v_lshrrev_b32_e32 v24, 4, v25
	v_and_b32_e32 v24, 0xf0f0f0f, v24
	v_dot4c_i32_i8_e32 v28, v24, v39
	v_and_b32_e32 v24, 0xf0f0f0f, v26
	v_dot4c_i32_i8_e32 v29, v24, v32
	v_lshrrev_b32_e32 v24, 4, v26
	v_and_b32_e32 v24, 0xf0f0f0f, v24
	v_dot4c_i32_i8_e32 v29, v24, v33
	v_and_b32_e32 v24, 0xf0f0f0f, v27
	v_dot4c_i32_i8_e32 v28, v24, v34
	v_lshrrev_b32_e32 v24, 4, v27
	v_and_b32_e32 v24, 0xf0f0f0f, v24
	v_dot4c_i32_i8_e32 v28, v24, v35
	v_add_u32_e32 v26, v49, v48
	v_sub_u32_e32 v26, v26, v171
	v_and_b32_e32 v25, 0xffff0000, v43
	v_add_u32_e32 v27, v29, v28
	v_sub_u32_e32 v28, v27, v171
	v_cvt_f32_i32_e32 v27, v26
	v_cvt_f32_i32_e32 v26, v28
	v_lshlrev_b32_e32 v24, 16, v43
	s_cmp_eq_u32 s44, 0x3c000
	v_pk_fma_f32 v[158:159], v[24:25], v[26:27], v[158:159]
	s_waitcnt vmcnt(21)
	v_and_b32_e32 v24, 0xf0f0f0f, v20
	v_mov_b32_e32 v25, 0
	v_lshrrev_b32_e32 v20, 4, v20
	v_dot4c_i32_i8_e32 v25, v24, v36
	v_and_b32_e32 v20, 0xf0f0f0f, v20
	v_dot4c_i32_i8_e32 v25, v20, v37
	v_and_b32_e32 v20, 0xf0f0f0f, v21
	v_mov_b32_e32 v24, 0
	v_dot4c_i32_i8_e32 v24, v20, v38
	v_lshrrev_b32_e32 v20, 4, v21
	v_and_b32_e32 v20, 0xf0f0f0f, v20
	v_dot4c_i32_i8_e32 v24, v20, v39
	v_and_b32_e32 v20, 0xf0f0f0f, v22
	v_dot4c_i32_i8_e32 v25, v20, v32
	v_lshrrev_b32_e32 v20, 4, v22
	v_and_b32_e32 v20, 0xf0f0f0f, v20
	v_dot4c_i32_i8_e32 v25, v20, v33
	v_and_b32_e32 v20, 0xf0f0f0f, v23
	v_dot4c_i32_i8_e32 v24, v20, v34
	v_lshrrev_b32_e32 v20, 4, v23
	v_and_b32_e32 v20, 0xf0f0f0f, v20
	v_dot4c_i32_i8_e32 v24, v20, v35
	s_waitcnt vmcnt(20)
	v_and_b32_e32 v20, 0xf0f0f0f, v16
	v_mov_b32_e32 v21, 0
	v_lshrrev_b32_e32 v16, 4, v16
	v_dot4c_i32_i8_e32 v21, v20, v36
	v_and_b32_e32 v16, 0xf0f0f0f, v16
	v_dot4c_i32_i8_e32 v21, v16, v37
	v_and_b32_e32 v16, 0xf0f0f0f, v17
	v_mov_b32_e32 v20, 0
	v_dot4c_i32_i8_e32 v20, v16, v38
	v_lshrrev_b32_e32 v16, 4, v17
	v_and_b32_e32 v16, 0xf0f0f0f, v16
	v_dot4c_i32_i8_e32 v20, v16, v39
	v_and_b32_e32 v16, 0xf0f0f0f, v18
	v_dot4c_i32_i8_e32 v21, v16, v32
	v_lshrrev_b32_e32 v16, 4, v18
	v_and_b32_e32 v16, 0xf0f0f0f, v16
	v_dot4c_i32_i8_e32 v21, v16, v33
	v_and_b32_e32 v16, 0xf0f0f0f, v19
	v_dot4c_i32_i8_e32 v20, v16, v34
	v_lshrrev_b32_e32 v16, 4, v19
	v_and_b32_e32 v16, 0xf0f0f0f, v16
	v_dot4c_i32_i8_e32 v20, v16, v35
	v_add_u32_e32 v18, v25, v24
	v_sub_u32_e32 v18, v18, v171
	v_and_b32_e32 v17, 0xffff0000, v42
	v_add_u32_e32 v19, v21, v20
	v_sub_u32_e32 v20, v19, v171
	v_cvt_f32_i32_e32 v19, v18
	v_cvt_f32_i32_e32 v18, v20
	v_lshlrev_b32_e32 v16, 16, v42
	v_pk_fma_f32 v[156:157], v[16:17], v[18:19], v[156:157]
	s_waitcnt vmcnt(19)
; #define P12_ISSUE(c_, i_, h_, CW_, SC_) do { _Pragma("unroll") for (int bb = 0; bb < 8; ++bb) { const unsigned ro = (unsigned)(c_) * 16384u + (unsigned)EL[(i_) * 128 + ((h_) * 8 + bb) * 8 + g8]; \
;         CW_[bb] = *(const v4u*)(U4 + (size_t)(ro * 128u + 16u * (unsigned)k8)); SC_[bb] = USS[(size_t)(ro * 8u + (unsigned)k8)]; } } while (0)
; #define P12_COMP(i_, h_, CW_, SC_) do { _Pragma("unroll") for (int bb = 0; bb < 8; ++bb) { int a0 = 0, a1 = 0; P12_U4(CW_[bb].x, xa.x, xa.y, a0); P12_U4(CW_[bb].y, xa.z, xa.w, a1); P12_U4(CW_[bb].z, xb.x, xb.y, a0); P12_U4(CW_[bb].w, xb.z, xb.w, a1); \
;         psum[(i_)][(h_) * 8 + bb] += __uint_as_float(SC_[bb] << 16) * (float)((a0 + a1) - xo); } } while (0)
; #define P12_BAR() asm volatile("" ::: "memory")
; __device__ __forceinline__ void p12_peer(Frame& F) {
;     ...
;     { v4u cwA[8], cwB[8]; unsigned scA[8], scB[8]; v4u xa, xb; int xo;
;       P12_ISSUE(0, 0, 0, cwA, scA);
; _Pragma("nounroll")
;       for (int c = 0; c < 16; ++c) { const int cn = c + 1 < 16 ? c + 1 : 15;
;           P12_XQ(c, 0); P12_ISSUE(c, 0, 1, cwB, scB); P12_BAR(); P12_COMP(0, 0, cwA, scA); P12_ISSUE(c, 1, 0, cwA, scA); P12_BAR(); P12_COMP(0, 1, cwB, scB);
;           P12_XQ(c, 1); P12_ISSUE(c, 1, 1, cwB, scB); P12_BAR(); P12_COMP(1, 0, cwA, scA); P12_ISSUE(c, 2, 0, cwA, scA); P12_BAR(); P12_COMP(1, 1, cwB, scB);
;           P12_XQ(c, 2); P12_ISSUE(c, 2, 1, cwB, scB); P12_BAR(); P12_COMP(2, 0, cwA, scA); P12_ISSUE(c, 3, 0, cwA, scA); P12_BAR(); P12_COMP(2, 1, cwB, scB);
;           P12_XQ(c, 3); P12_ISSUE(c, 3, 1, cwB, scB); P12_BAR(); P12_COMP(3, 0, cwA, scA); P12_ISSUE(cn, 0, 0, cwA, scA); P12_BAR(); P12_COMP(3, 1, cwB, scB);
	v_and_b32_e32 v16, 0xf0f0f0f, v12
	v_mov_b32_e32 v17, 0
	v_lshrrev_b32_e32 v12, 4, v12
	v_dot4c_i32_i8_e32 v17, v16, v36
	v_and_b32_e32 v12, 0xf0f0f0f, v12
	v_dot4c_i32_i8_e32 v17, v12, v37
	v_and_b32_e32 v12, 0xf0f0f0f, v13
	v_mov_b32_e32 v16, 0
	v_dot4c_i32_i8_e32 v16, v12, v38
	v_lshrrev_b32_e32 v12, 4, v13
	v_and_b32_e32 v12, 0xf0f0f0f, v12
	v_dot4c_i32_i8_e32 v16, v12, v39
	v_and_b32_e32 v12, 0xf0f0f0f, v14
	v_dot4c_i32_i8_e32 v17, v12, v32
	v_lshrrev_b32_e32 v12, 4, v14
	v_and_b32_e32 v12, 0xf0f0f0f, v12
	v_dot4c_i32_i8_e32 v17, v12, v33
	v_and_b32_e32 v12, 0xf0f0f0f, v15
	v_dot4c_i32_i8_e32 v16, v12, v34
	v_lshrrev_b32_e32 v12, 4, v15
	v_and_b32_e32 v12, 0xf0f0f0f, v12
	v_dot4c_i32_i8_e32 v16, v12, v35
	s_waitcnt vmcnt(18)
	v_and_b32_e32 v12, 0xf0f0f0f, v8
	v_mov_b32_e32 v13, 0
	v_lshrrev_b32_e32 v8, 4, v8
	v_dot4c_i32_i8_e32 v13, v12, v36
	v_and_b32_e32 v8, 0xf0f0f0f, v8
	v_dot4c_i32_i8_e32 v13, v8, v37
	v_and_b32_e32 v8, 0xf0f0f0f, v9
	v_mov_b32_e32 v12, 0
	v_dot4c_i32_i8_e32 v12, v8, v38
	v_lshrrev_b32_e32 v8, 4, v9
	v_and_b32_e32 v8, 0xf0f0f0f, v8
	v_dot4c_i32_i8_e32 v12, v8, v39
	v_and_b32_e32 v8, 0xf0f0f0f, v10
	v_dot4c_i32_i8_e32 v13, v8, v32
	v_lshrrev_b32_e32 v8, 4, v10
	v_and_b32_e32 v8, 0xf0f0f0f, v8
	v_dot4c_i32_i8_e32 v13, v8, v33
	v_and_b32_e32 v8, 0xf0f0f0f, v11
	v_dot4c_i32_i8_e32 v12, v8, v34
	v_lshrrev_b32_e32 v8, 4, v11
	v_and_b32_e32 v8, 0xf0f0f0f, v8
	v_dot4c_i32_i8_e32 v12, v8, v35
	v_add_u32_e32 v10, v17, v16
	v_sub_u32_e32 v10, v10, v171
	v_and_b32_e32 v9, 0xffff0000, v41
	v_add_u32_e32 v11, v13, v12
	v_sub_u32_e32 v12, v11, v171
	v_cvt_f32_i32_e32 v11, v10
	v_cvt_f32_i32_e32 v10, v12
	v_lshlrev_b32_e32 v8, 16, v41
	v_pk_fma_f32 v[154:155], v[8:9], v[10:11], v[154:155]
	s_waitcnt vmcnt(17)
	v_and_b32_e32 v8, 0xf0f0f0f, v4
	v_mov_b32_e32 v9, 0
	v_lshrrev_b32_e32 v4, 4, v4
	v_dot4c_i32_i8_e32 v9, v8, v36
	v_and_b32_e32 v4, 0xf0f0f0f, v4
	v_dot4c_i32_i8_e32 v9, v4, v37
	v_and_b32_e32 v4, 0xf0f0f0f, v5
	v_mov_b32_e32 v8, 0
	v_dot4c_i32_i8_e32 v8, v4, v38
	v_lshrrev_b32_e32 v4, 4, v5
	v_and_b32_e32 v4, 0xf0f0f0f, v4
	v_dot4c_i32_i8_e32 v8, v4, v39
	v_and_b32_e32 v4, 0xf0f0f0f, v6
	v_dot4c_i32_i8_e32 v9, v4, v32
	v_lshrrev_b32_e32 v4, 4, v6
	v_and_b32_e32 v4, 0xf0f0f0f, v4
	v_dot4c_i32_i8_e32 v9, v4, v33
	v_and_b32_e32 v4, 0xf0f0f0f, v7
	v_dot4c_i32_i8_e32 v8, v4, v34
	v_lshrrev_b32_e32 v4, 4, v7
	v_and_b32_e32 v4, 0xf0f0f0f, v4
	v_dot4c_i32_i8_e32 v8, v4, v35
	s_waitcnt vmcnt(16)
	v_and_b32_e32 v4, 0xf0f0f0f, v0
	v_mov_b32_e32 v5, 0
	v_lshrrev_b32_e32 v0, 4, v0
	v_dot4c_i32_i8_e32 v5, v4, v36
	v_and_b32_e32 v0, 0xf0f0f0f, v0
	v_dot4c_i32_i8_e32 v5, v0, v37
	v_and_b32_e32 v0, 0xf0f0f0f, v1
	v_mov_b32_e32 v4, 0
	v_dot4c_i32_i8_e32 v4, v0, v38
	v_lshrrev_b32_e32 v0, 4, v1
	v_and_b32_e32 v0, 0xf0f0f0f, v0
	v_dot4c_i32_i8_e32 v4, v0, v39
	v_and_b32_e32 v0, 0xf0f0f0f, v2
	v_dot4c_i32_i8_e32 v5, v0, v32
	v_lshrrev_b32_e32 v0, 4, v2
	v_and_b32_e32 v0, 0xf0f0f0f, v0
	v_dot4c_i32_i8_e32 v5, v0, v33
	v_and_b32_e32 v0, 0xf0f0f0f, v3
	v_dot4c_i32_i8_e32 v4, v0, v34
	v_lshrrev_b32_e32 v0, 4, v3
	v_and_b32_e32 v0, 0xf0f0f0f, v0
	v_dot4c_i32_i8_e32 v4, v0, v35
	v_add_u32_e32 v2, v9, v8
	v_sub_u32_e32 v2, v2, v171
	v_and_b32_e32 v1, 0xffff0000, v40
	v_add_u32_e32 v3, v5, v4
	v_sub_u32_e32 v4, v3, v171
	v_cvt_f32_i32_e32 v3, v2
	v_cvt_f32_i32_e32 v2, v4
	v_lshlrev_b32_e32 v0, 16, v40
	v_pk_fma_f32 v[152:153], v[0:1], v[2:3], v[152:153]
	ds_read_u16 v0, v93 offset:16640
	ds_read_u16 v1, v93 offset:16656
	ds_read_u16 v2, v93 offset:16672
	ds_read_u16 v3, v93 offset:16688
	s_waitcnt lgkmcnt(3)
	v_add_u32_e32 v0, s44, v0
	v_lshl_or_b32 v4, v0, 7, v165
	s_waitcnt lgkmcnt(2)
	v_add_u32_e32 v1, s44, v1
	global_load_dwordx4 v[72:75], v4, s[0:1]
	v_lshl_or_b32 v4, v1, 7, v165
	s_waitcnt lgkmcnt(1)
	v_add_u32_e32 v2, s44, v2
	global_load_dwordx4 v[64:67], v4, s[0:1]
	v_lshl_or_b32 v4, v2, 7, v165
	s_waitcnt lgkmcnt(0)
	v_add_u32_e32 v3, s44, v3
	global_load_dwordx4 v[56:59], v4, s[0:1]
	v_lshl_or_b32 v4, v3, 7, v165
	global_load_dwordx4 v[48:51], v4, s[0:1]
	ds_read_u16 v4, v93 offset:16704
	v_lshl_or_b32 v0, v0, 5, v248
	v_lshl_or_b32 v1, v1, 5, v248
	v_lshl_or_b32 v2, v2, 5, v248
	v_lshl_or_b32 v3, v3, 5, v248
	s_waitcnt lgkmcnt(0)
	v_add_u32_e32 v4, s44, v4
	v_lshl_or_b32 v5, v4, 7, v165
	global_load_dwordx4 v[40:43], v5, s[0:1]
	ds_read_u16 v5, v93 offset:16720
	v_lshl_or_b32 v4, v4, 5, v248
	s_waitcnt lgkmcnt(0)
	v_add_u32_e32 v5, s44, v5
	v_lshl_or_b32 v6, v5, 7, v165
	global_load_dwordx4 v[24:27], v6, s[0:1]
	ds_read_u16 v6, v93 offset:16736
	v_lshl_or_b32 v5, v5, 5, v248
	s_waitcnt lgkmcnt(0)
	v_add_u32_e32 v6, s44, v6
	v_lshl_or_b32 v7, v6, 7, v165
	global_load_dwordx4 v[12:15], v7, s[0:1]
	ds_read_u16 v7, v93 offset:16752
	v_lshl_or_b32 v6, v6, 5, v248
	s_waitcnt lgkmcnt(0)
	v_add_u32_e32 v7, s44, v7
	v_lshl_or_b32 v8, v7, 7, v165
	global_load_dwordx4 v[8:11], v8, s[0:1]
	v_lshl_or_b32 v7, v7, 5, v248
	global_load_dword v201, v1, s[46:47]
	global_load_dword v200, v0, s[46:47]
	global_load_dword v203, v3, s[46:47]
	global_load_dword v202, v2, s[46:47]
	global_load_dword v205, v5, s[46:47]
	global_load_dword v204, v4, s[46:47]
	global_load_dword v207, v7, s[46:47]
	global_load_dword v206, v6, s[46:47]
	s_waitcnt vmcnt(31)
	v_and_b32_e32 v0, 0xf0f0f0f, v88
	v_mov_b32_e32 v2, 0
	v_dot4c_i32_i8_e32 v2, v0, v36
	v_lshrrev_b32_e32 v0, 4, v88
	v_and_b32_e32 v0, 0xf0f0f0f, v0
	v_dot4c_i32_i8_e32 v2, v0, v37
	v_and_b32_e32 v0, 0xf0f0f0f, v89
	v_mov_b32_e32 v3, 0
	v_dot4c_i32_i8_e32 v3, v0, v38
	v_lshrrev_b32_e32 v0, 4, v89
	v_and_b32_e32 v0, 0xf0f0f0f, v0
	v_dot4c_i32_i8_e32 v3, v0, v39
	v_and_b32_e32 v0, 0xf0f0f0f, v90
	v_dot4c_i32_i8_e32 v2, v0, v32
	v_lshrrev_b32_e32 v0, 4, v90
	v_and_b32_e32 v0, 0xf0f0f0f, v0
	v_dot4c_i32_i8_e32 v2, v0, v33
	v_and_b32_e32 v0, 0xf0f0f0f, v91
	v_dot4c_i32_i8_e32 v3, v0, v34
	v_lshrrev_b32_e32 v0, 4, v91
	v_and_b32_e32 v0, 0xf0f0f0f, v0
	v_dot4c_i32_i8_e32 v3, v0, v35
	s_waitcnt vmcnt(30)
; #define P12_ISSUE(c_, i_, h_, CW_, SC_) do { _Pragma("unroll") for (int bb = 0; bb < 8; ++bb) { const unsigned ro = (unsigned)(c_) * 16384u + (unsigned)EL[(i_) * 128 + ((h_) * 8 + bb) * 8 + g8]; \
;         CW_[bb] = *(const v4u*)(U4 + (size_t)(ro * 128u + 16u * (unsigned)k8)); SC_[bb] = USS[(size_t)(ro * 8u + (unsigned)k8)]; } } while (0)
; #define P12_COMP(i_, h_, CW_, SC_) do { _Pragma("unroll") for (int bb = 0; bb < 8; ++bb) { int a0 = 0, a1 = 0; P12_U4(CW_[bb].x, xa.x, xa.y, a0); P12_U4(CW_[bb].y, xa.z, xa.w, a1); P12_U4(CW_[bb].z, xb.x, xb.y, a0); P12_U4(CW_[bb].w, xb.z, xb.w, a1); \
;         psum[(i_)][(h_) * 8 + bb] += __uint_as_float(SC_[bb] << 16) * (float)((a0 + a1) - xo); } } while (0)
; #define P12_BAR() asm volatile("" ::: "memory")
; __device__ __forceinline__ void p12_peer(Frame& F) {
;     ...
;     { v4u cwA[8], cwB[8]; unsigned scA[8], scB[8]; v4u xa, xb; int xo;
;       P12_ISSUE(0, 0, 0, cwA, scA);
; _Pragma("nounroll")
;       for (int c = 0; c < 16; ++c) { const int cn = c + 1 < 16 ? c + 1 : 15;
;           P12_XQ(c, 0); P12_ISSUE(c, 0, 1, cwB, scB); P12_BAR(); P12_COMP(0, 0, cwA, scA); P12_ISSUE(c, 1, 0, cwA, scA); P12_BAR(); P12_COMP(0, 1, cwB, scB);
;           P12_XQ(c, 1); P12_ISSUE(c, 1, 1, cwB, scB); P12_BAR(); P12_COMP(1, 0, cwA, scA); P12_ISSUE(c, 2, 0, cwA, scA); P12_BAR(); P12_COMP(1, 1, cwB, scB);
;           P12_XQ(c, 2); P12_ISSUE(c, 2, 1, cwB, scB); P12_BAR(); P12_COMP(2, 0, cwA, scA); P12_ISSUE(c, 3, 0, cwA, scA); P12_BAR(); P12_COMP(2, 1, cwB, scB);
;           P12_XQ(c, 3); P12_ISSUE(c, 3, 1, cwB, scB); P12_BAR(); P12_COMP(3, 0, cwA, scA); P12_ISSUE(cn, 0, 0, cwA, scA); P12_BAR(); P12_COMP(3, 1, cwB, scB);
	v_and_b32_e32 v0, 0xf0f0f0f, v84
	v_mov_b32_e32 v4, 0
	v_dot4c_i32_i8_e32 v4, v0, v36
	v_lshrrev_b32_e32 v0, 4, v84
	v_and_b32_e32 v0, 0xf0f0f0f, v0
	v_dot4c_i32_i8_e32 v4, v0, v37
	v_and_b32_e32 v0, 0xf0f0f0f, v85
	v_mov_b32_e32 v5, 0
	v_dot4c_i32_i8_e32 v5, v0, v38
	v_lshrrev_b32_e32 v0, 4, v85
	v_and_b32_e32 v0, 0xf0f0f0f, v0
	v_dot4c_i32_i8_e32 v5, v0, v39
	v_and_b32_e32 v0, 0xf0f0f0f, v86
	v_dot4c_i32_i8_e32 v4, v0, v32
	v_lshrrev_b32_e32 v0, 4, v86
	v_and_b32_e32 v0, 0xf0f0f0f, v0
	v_dot4c_i32_i8_e32 v4, v0, v33
	v_and_b32_e32 v0, 0xf0f0f0f, v87
	v_dot4c_i32_i8_e32 v5, v0, v34
	v_lshrrev_b32_e32 v0, 4, v87
	v_and_b32_e32 v0, 0xf0f0f0f, v0
	v_dot4c_i32_i8_e32 v5, v0, v35
	v_add_u32_e32 v2, v2, v3
	v_sub_u32_e32 v2, v2, v171
	s_waitcnt vmcnt(22)
	v_lshlrev_b32_e32 v1, 16, v192
	v_sub_u32_e32 v3, v5, v171
	v_add_u32_e32 v4, v3, v4
	v_cvt_f32_i32_e32 v3, v2
	v_cvt_f32_i32_e32 v2, v4
	v_lshlrev_b32_e32 v0, 16, v193
	v_mov_b32_e32 v4, 0
	v_mov_b32_e32 v5, 0
	v_pk_fma_f32 v[150:151], v[0:1], v[2:3], v[150:151]
	v_and_b32_e32 v0, 0xf0f0f0f, v80
	v_mov_b32_e32 v2, 0
	v_dot4c_i32_i8_e32 v2, v0, v36
	v_lshrrev_b32_e32 v0, 4, v80
	v_and_b32_e32 v0, 0xf0f0f0f, v0
	v_dot4c_i32_i8_e32 v2, v0, v37
	v_and_b32_e32 v0, 0xf0f0f0f, v81
	v_mov_b32_e32 v3, 0
	v_dot4c_i32_i8_e32 v3, v0, v38
	v_lshrrev_b32_e32 v0, 4, v81
	v_and_b32_e32 v0, 0xf0f0f0f, v0
	v_dot4c_i32_i8_e32 v3, v0, v39
	v_and_b32_e32 v0, 0xf0f0f0f, v82
	v_dot4c_i32_i8_e32 v2, v0, v32
	v_lshrrev_b32_e32 v0, 4, v82
	v_and_b32_e32 v0, 0xf0f0f0f, v0
	v_dot4c_i32_i8_e32 v2, v0, v33
	v_and_b32_e32 v0, 0xf0f0f0f, v83
	v_dot4c_i32_i8_e32 v3, v0, v34
	v_lshrrev_b32_e32 v0, 4, v83
	v_and_b32_e32 v0, 0xf0f0f0f, v0
	v_dot4c_i32_i8_e32 v3, v0, v35
	v_and_b32_e32 v0, 0xf0f0f0f, v76
	v_dot4c_i32_i8_e32 v4, v0, v36
	v_lshrrev_b32_e32 v0, 4, v76
	v_and_b32_e32 v0, 0xf0f0f0f, v0
	v_dot4c_i32_i8_e32 v4, v0, v37
	v_and_b32_e32 v0, 0xf0f0f0f, v77
	v_dot4c_i32_i8_e32 v5, v0, v38
	v_lshrrev_b32_e32 v0, 4, v77
	v_and_b32_e32 v0, 0xf0f0f0f, v0
	v_dot4c_i32_i8_e32 v5, v0, v39
	v_and_b32_e32 v0, 0xf0f0f0f, v78
	v_dot4c_i32_i8_e32 v4, v0, v32
	v_lshrrev_b32_e32 v0, 4, v78
	v_and_b32_e32 v0, 0xf0f0f0f, v0
	v_dot4c_i32_i8_e32 v4, v0, v33
	v_and_b32_e32 v0, 0xf0f0f0f, v79
	v_dot4c_i32_i8_e32 v5, v0, v34
	v_lshrrev_b32_e32 v0, 4, v79
	v_and_b32_e32 v0, 0xf0f0f0f, v0
	v_dot4c_i32_i8_e32 v5, v0, v35
	v_sub_u32_e32 v3, v3, v171
	v_add_u32_e32 v2, v3, v2
	v_cvt_f32_i32_e32 v3, v2
	v_sub_u32_e32 v5, v5, v171
	v_add_u32_e32 v4, v5, v4
	v_cvt_f32_i32_e32 v2, v4
	s_waitcnt vmcnt(20)
	v_lshlrev_b32_e32 v1, 16, v194
	v_lshlrev_b32_e32 v0, 16, v195
	v_mov_b32_e32 v4, 0
	v_pk_fma_f32 v[148:149], v[0:1], v[2:3], v[148:149]
	v_and_b32_e32 v0, 0xf0f0f0f, v68
	v_mov_b32_e32 v2, 0
	v_dot4c_i32_i8_e32 v2, v0, v36
	v_lshrrev_b32_e32 v0, 4, v68
	v_and_b32_e32 v0, 0xf0f0f0f, v0
	v_dot4c_i32_i8_e32 v2, v0, v37
	v_and_b32_e32 v0, 0xf0f0f0f, v69
	v_mov_b32_e32 v3, 0
	v_dot4c_i32_i8_e32 v3, v0, v38
	v_lshrrev_b32_e32 v0, 4, v69
	v_and_b32_e32 v0, 0xf0f0f0f, v0
	v_dot4c_i32_i8_e32 v3, v0, v39
	v_and_b32_e32 v0, 0xf0f0f0f, v70
	v_dot4c_i32_i8_e32 v2, v0, v32
	v_lshrrev_b32_e32 v0, 4, v70
	v_and_b32_e32 v0, 0xf0f0f0f, v0
	v_dot4c_i32_i8_e32 v2, v0, v33
	v_and_b32_e32 v0, 0xf0f0f0f, v71
	v_dot4c_i32_i8_e32 v3, v0, v34
	v_lshrrev_b32_e32 v0, 4, v71
	v_and_b32_e32 v0, 0xf0f0f0f, v0
	v_dot4c_i32_i8_e32 v3, v0, v35
	v_and_b32_e32 v0, 0xf0f0f0f, v60
	v_dot4c_i32_i8_e32 v4, v0, v36
	v_lshrrev_b32_e32 v0, 4, v60
	v_and_b32_e32 v0, 0xf0f0f0f, v0
	v_dot4c_i32_i8_e32 v4, v0, v37
	v_and_b32_e32 v0, 0xf0f0f0f, v61
	v_mov_b32_e32 v5, 0
	v_dot4c_i32_i8_e32 v5, v0, v38
	v_lshrrev_b32_e32 v0, 4, v61
	v_and_b32_e32 v0, 0xf0f0f0f, v0
	v_dot4c_i32_i8_e32 v5, v0, v39
	v_and_b32_e32 v0, 0xf0f0f0f, v62
	v_dot4c_i32_i8_e32 v4, v0, v32
	v_lshrrev_b32_e32 v0, 4, v62
	v_and_b32_e32 v0, 0xf0f0f0f, v0
	v_dot4c_i32_i8_e32 v4, v0, v33
	v_and_b32_e32 v0, 0xf0f0f0f, v63
	v_dot4c_i32_i8_e32 v5, v0, v34
	v_lshrrev_b32_e32 v0, 4, v63
	v_and_b32_e32 v0, 0xf0f0f0f, v0
	v_dot4c_i32_i8_e32 v5, v0, v35
	v_sub_u32_e32 v3, v3, v171
	v_add_u32_e32 v2, v3, v2
	v_cvt_f32_i32_e32 v3, v2
	v_sub_u32_e32 v5, v5, v171
	v_add_u32_e32 v4, v5, v4
	v_cvt_f32_i32_e32 v2, v4
	s_waitcnt vmcnt(18)
	v_lshlrev_b32_e32 v1, 16, v196
	v_lshlrev_b32_e32 v0, 16, v197
	v_mov_b32_e32 v4, 0
	v_pk_fma_f32 v[146:147], v[0:1], v[2:3], v[146:147]
	v_and_b32_e32 v0, 0xf0f0f0f, v52
	v_mov_b32_e32 v2, 0
	v_dot4c_i32_i8_e32 v2, v0, v36
	v_lshrrev_b32_e32 v0, 4, v52
	v_and_b32_e32 v0, 0xf0f0f0f, v0
	v_dot4c_i32_i8_e32 v2, v0, v37
	v_and_b32_e32 v0, 0xf0f0f0f, v53
	v_mov_b32_e32 v3, 0
	v_dot4c_i32_i8_e32 v3, v0, v38
	v_lshrrev_b32_e32 v0, 4, v53
	v_and_b32_e32 v0, 0xf0f0f0f, v0
	v_dot4c_i32_i8_e32 v3, v0, v39
	v_and_b32_e32 v0, 0xf0f0f0f, v54
	v_dot4c_i32_i8_e32 v2, v0, v32
	v_lshrrev_b32_e32 v0, 4, v54
	v_and_b32_e32 v0, 0xf0f0f0f, v0
	v_dot4c_i32_i8_e32 v2, v0, v33
	v_and_b32_e32 v0, 0xf0f0f0f, v55
	v_dot4c_i32_i8_e32 v3, v0, v34
	v_lshrrev_b32_e32 v0, 4, v55
	v_and_b32_e32 v0, 0xf0f0f0f, v0
	v_dot4c_i32_i8_e32 v3, v0, v35
	v_and_b32_e32 v0, 0xf0f0f0f, v44
	v_dot4c_i32_i8_e32 v4, v0, v36
	v_lshrrev_b32_e32 v0, 4, v44
	v_and_b32_e32 v0, 0xf0f0f0f, v0
	v_dot4c_i32_i8_e32 v4, v0, v37
	v_and_b32_e32 v0, 0xf0f0f0f, v45
	v_mov_b32_e32 v5, 0
	v_dot4c_i32_i8_e32 v5, v0, v38
	v_lshrrev_b32_e32 v0, 4, v45
	v_and_b32_e32 v0, 0xf0f0f0f, v0
	v_dot4c_i32_i8_e32 v5, v0, v39
	v_and_b32_e32 v0, 0xf0f0f0f, v46
	v_dot4c_i32_i8_e32 v4, v0, v32
	v_lshrrev_b32_e32 v0, 4, v46
	v_and_b32_e32 v0, 0xf0f0f0f, v0
	v_dot4c_i32_i8_e32 v4, v0, v33
	v_and_b32_e32 v0, 0xf0f0f0f, v47
	v_dot4c_i32_i8_e32 v5, v0, v34
	v_lshrrev_b32_e32 v0, 4, v47
	v_and_b32_e32 v0, 0xf0f0f0f, v0
	v_dot4c_i32_i8_e32 v5, v0, v35
	v_sub_u32_e32 v3, v3, v171
	v_add_u32_e32 v2, v3, v2
	v_cvt_f32_i32_e32 v3, v2
	v_sub_u32_e32 v5, v5, v171
	v_add_u32_e32 v4, v5, v4
	v_cvt_f32_i32_e32 v2, v4
	s_waitcnt vmcnt(16)
; #define P12_ISSUE(c_, i_, h_, CW_, SC_) do { _Pragma("unroll") for (int bb = 0; bb < 8; ++bb) { const unsigned ro = (unsigned)(c_) * 16384u + (unsigned)EL[(i_) * 128 + ((h_) * 8 + bb) * 8 + g8]; \
;         CW_[bb] = *(const v4u*)(U4 + (size_t)(ro * 128u + 16u * (unsigned)k8)); SC_[bb] = USS[(size_t)(ro * 8u + (unsigned)k8)]; } } while (0)
; #define P12_COMP(i_, h_, CW_, SC_) do { _Pragma("unroll") for (int bb = 0; bb < 8; ++bb) { int a0 = 0, a1 = 0; P12_U4(CW_[bb].x, xa.x, xa.y, a0); P12_U4(CW_[bb].y, xa.z, xa.w, a1); P12_U4(CW_[bb].z, xb.x, xb.y, a0); P12_U4(CW_[bb].w, xb.z, xb.w, a1); \
;         psum[(i_)][(h_) * 8 + bb] += __uint_as_float(SC_[bb] << 16) * (float)((a0 + a1) - xo); } } while (0)
; #define P12_BAR() asm volatile("" ::: "memory")
; __device__ __forceinline__ void p12_peer(Frame& F) {
;     ...
;     { v4u cwA[8], cwB[8]; unsigned scA[8], scB[8]; v4u xa, xb; int xo;
;       P12_ISSUE(0, 0, 0, cwA, scA);
; _Pragma("nounroll")
;       for (int c = 0; c < 16; ++c) { const int cn = c + 1 < 16 ? c + 1 : 15;
;           P12_XQ(c, 0); P12_ISSUE(c, 0, 1, cwB, scB); P12_BAR(); P12_COMP(0, 0, cwA, scA); P12_ISSUE(c, 1, 0, cwA, scA); P12_BAR(); P12_COMP(0, 1, cwB, scB);
;           P12_XQ(c, 1); P12_ISSUE(c, 1, 1, cwB, scB); P12_BAR(); P12_COMP(1, 0, cwA, scA); P12_ISSUE(c, 2, 0, cwA, scA); P12_BAR(); P12_COMP(1, 1, cwB, scB);
;           P12_XQ(c, 2); P12_ISSUE(c, 2, 1, cwB, scB); P12_BAR(); P12_COMP(2, 0, cwA, scA); P12_ISSUE(c, 3, 0, cwA, scA); P12_BAR(); P12_COMP(2, 1, cwB, scB);
;           P12_XQ(c, 3); P12_ISSUE(c, 3, 1, cwB, scB); P12_BAR(); P12_COMP(3, 0, cwA, scA); P12_ISSUE(cn, 0, 0, cwA, scA); P12_BAR(); P12_COMP(3, 1, cwB, scB);
	v_lshlrev_b32_e32 v1, 16, v198
	v_lshlrev_b32_e32 v0, 16, v199
	v_pk_fma_f32 v[144:145], v[0:1], v[2:3], v[144:145]
	ds_read_b128 v[4:7], v166 offset:4096
	ds_read_b128 v[0:3], v166 offset:4112
	ds_read_u16 v16, v93 offset:16768
	ds_read_u16 v17, v93 offset:16784
	ds_read_u16 v18, v93 offset:16800
	ds_read_u16 v19, v93 offset:16816
	v_mov_b32_e32 v44, 0
	s_waitcnt lgkmcnt(3)
	v_add_u32_e32 v16, s44, v16
	v_lshl_or_b32 v20, v16, 7, v165
	v_lshl_or_b32 v45, v16, 5, v248
	s_waitcnt lgkmcnt(2)
	v_add_u32_e32 v16, s44, v17
	v_lshl_or_b32 v17, v16, 7, v165
	v_lshl_or_b32 v46, v16, 5, v248
	s_waitcnt lgkmcnt(1)
	v_add_u32_e32 v16, s44, v18
	global_load_dwordx4 v[80:83], v20, s[0:1]
	global_load_dwordx4 v[68:71], v17, s[0:1]
	v_lshl_or_b32 v17, v16, 7, v165
	v_lshl_or_b32 v47, v16, 5, v248
	s_waitcnt lgkmcnt(0)
	v_add_u32_e32 v16, s44, v19
	global_load_dwordx4 v[52:55], v17, s[0:1]
	v_lshl_or_b32 v17, v16, 7, v165
	v_lshl_or_b32 v60, v16, 5, v248
	ds_read_u16 v16, v93 offset:16832
	global_load_dwordx4 v[36:39], v17, s[0:1]
	v_dot4c_i32_i8_e32 v44, 0x1010101, v4
	v_dot4c_i32_i8_e32 v44, 0x1010101, v5
	v_dot4c_i32_i8_e32 v44, 0x1010101, v6
	s_waitcnt lgkmcnt(0)
	v_add_u32_e32 v16, s44, v16
	v_lshl_or_b32 v17, v16, 7, v165
	v_lshl_or_b32 v61, v16, 5, v248
	ds_read_u16 v16, v93 offset:16848
	global_load_dwordx4 v[32:35], v17, s[0:1]
	v_dot4c_i32_i8_e32 v44, 0x1010101, v7
	v_dot4c_i32_i8_e32 v44, 0x1010101, v0
	v_dot4c_i32_i8_e32 v44, 0x1010101, v1
	s_waitcnt lgkmcnt(0)
	v_add_u32_e32 v16, s44, v16
	v_lshl_or_b32 v17, v16, 7, v165
	v_lshl_or_b32 v62, v16, 5, v248
	ds_read_u16 v16, v93 offset:16864
	global_load_dwordx4 v[28:31], v17, s[0:1]
	v_dot4c_i32_i8_e32 v44, 0x1010101, v2
	v_dot4c_i32_i8_e32 v44, 0x1010101, v3
	s_waitcnt lgkmcnt(0)
	v_add_u32_e32 v16, s44, v16
	v_lshl_or_b32 v17, v16, 7, v165
	v_lshl_or_b32 v63, v16, 5, v248
	ds_read_u16 v16, v93 offset:16880
	global_load_dwordx4 v[20:23], v17, s[0:1]
	v_lshlrev_b32_e32 v84, 3, v44
	s_waitcnt vmcnt(22)
	v_and_b32_e32 v44, 0xf0f0f0f, v72
	s_waitcnt lgkmcnt(0)
	v_add_u32_e32 v76, s44, v16
	v_lshl_or_b32 v16, v76, 7, v165
	global_load_dwordx4 v[16:19], v16, s[0:1]
	v_lshl_or_b32 v76, v76, 5, v248
	global_load_dword v209, v46, s[46:47]
	global_load_dword v208, v45, s[46:47]
	global_load_dword v211, v60, s[46:47]
	global_load_dword v210, v47, s[46:47]
	global_load_dword v213, v62, s[46:47]
	global_load_dword v212, v61, s[46:47]
	global_load_dword v215, v76, s[46:47]
	global_load_dword v214, v63, s[46:47]
	v_mov_b32_e32 v46, 0
	v_dot4c_i32_i8_e32 v46, v44, v4
	v_lshrrev_b32_e32 v44, 4, v72
	v_and_b32_e32 v44, 0xf0f0f0f, v44
	v_dot4c_i32_i8_e32 v46, v44, v5
	v_and_b32_e32 v44, 0xf0f0f0f, v73
	v_mov_b32_e32 v47, 0
	v_dot4c_i32_i8_e32 v47, v44, v6
	v_lshrrev_b32_e32 v44, 4, v73
	v_and_b32_e32 v44, 0xf0f0f0f, v44
	v_dot4c_i32_i8_e32 v47, v44, v7
	v_and_b32_e32 v44, 0xf0f0f0f, v74
	v_dot4c_i32_i8_e32 v46, v44, v0
	v_lshrrev_b32_e32 v44, 4, v74
	v_and_b32_e32 v44, 0xf0f0f0f, v44
	v_dot4c_i32_i8_e32 v46, v44, v1
	v_and_b32_e32 v44, 0xf0f0f0f, v75
	v_dot4c_i32_i8_e32 v47, v44, v2
	v_lshrrev_b32_e32 v44, 4, v75
	v_and_b32_e32 v44, 0xf0f0f0f, v44
	v_dot4c_i32_i8_e32 v47, v44, v3
	s_waitcnt vmcnt(30)
	v_and_b32_e32 v44, 0xf0f0f0f, v64
	v_mov_b32_e32 v60, 0
	v_dot4c_i32_i8_e32 v60, v44, v4
	v_lshrrev_b32_e32 v44, 4, v64
	v_and_b32_e32 v44, 0xf0f0f0f, v44
	v_dot4c_i32_i8_e32 v60, v44, v5
	v_and_b32_e32 v44, 0xf0f0f0f, v65
	v_mov_b32_e32 v61, 0
	v_dot4c_i32_i8_e32 v61, v44, v6
	v_lshrrev_b32_e32 v44, 4, v65
	v_and_b32_e32 v44, 0xf0f0f0f, v44
	v_dot4c_i32_i8_e32 v61, v44, v7
	v_and_b32_e32 v44, 0xf0f0f0f, v66
	v_dot4c_i32_i8_e32 v60, v44, v0
	v_lshrrev_b32_e32 v44, 4, v66
	v_and_b32_e32 v44, 0xf0f0f0f, v44
	v_dot4c_i32_i8_e32 v60, v44, v1
	v_and_b32_e32 v44, 0xf0f0f0f, v67
	v_dot4c_i32_i8_e32 v61, v44, v2
	v_lshrrev_b32_e32 v44, 4, v67
	v_and_b32_e32 v44, 0xf0f0f0f, v44
	v_dot4c_i32_i8_e32 v61, v44, v3
	v_add_u32_e32 v46, v46, v47
	v_sub_u32_e32 v46, v46, v84
	s_waitcnt vmcnt(22)
	v_lshlrev_b32_e32 v45, 16, v200
	v_add_u32_e32 v47, v60, v61
	v_sub_u32_e32 v60, v47, v84
	v_cvt_f32_i32_e32 v47, v46
	v_cvt_f32_i32_e32 v46, v60
	v_lshlrev_b32_e32 v44, 16, v201
	v_pk_fma_f32 v[142:143], v[44:45], v[46:47], v[142:143]
	v_and_b32_e32 v44, 0xf0f0f0f, v56
	v_mov_b32_e32 v46, 0
	v_dot4c_i32_i8_e32 v46, v44, v4
	v_lshrrev_b32_e32 v44, 4, v56
	v_and_b32_e32 v44, 0xf0f0f0f, v44
	v_dot4c_i32_i8_e32 v46, v44, v5
	v_and_b32_e32 v44, 0xf0f0f0f, v57
	v_mov_b32_e32 v47, 0
	v_dot4c_i32_i8_e32 v47, v44, v6
	v_lshrrev_b32_e32 v44, 4, v57
	v_and_b32_e32 v44, 0xf0f0f0f, v44
	v_dot4c_i32_i8_e32 v47, v44, v7
	v_and_b32_e32 v44, 0xf0f0f0f, v58
	v_dot4c_i32_i8_e32 v46, v44, v0
	v_lshrrev_b32_e32 v44, 4, v58
	v_and_b32_e32 v44, 0xf0f0f0f, v44
	v_dot4c_i32_i8_e32 v46, v44, v1
	v_and_b32_e32 v44, 0xf0f0f0f, v59
	v_dot4c_i32_i8_e32 v47, v44, v2
	v_lshrrev_b32_e32 v44, 4, v59
	v_and_b32_e32 v44, 0xf0f0f0f, v44
	v_dot4c_i32_i8_e32 v47, v44, v3
	v_and_b32_e32 v44, 0xf0f0f0f, v48
	v_mov_b32_e32 v56, 0
	v_dot4c_i32_i8_e32 v56, v44, v4
	v_lshrrev_b32_e32 v44, 4, v48
	v_and_b32_e32 v44, 0xf0f0f0f, v44
	v_dot4c_i32_i8_e32 v56, v44, v5
	v_and_b32_e32 v44, 0xf0f0f0f, v49
	v_mov_b32_e32 v48, 0
	v_dot4c_i32_i8_e32 v48, v44, v6
	v_lshrrev_b32_e32 v44, 4, v49
	v_and_b32_e32 v44, 0xf0f0f0f, v44
	v_dot4c_i32_i8_e32 v48, v44, v7
	v_and_b32_e32 v44, 0xf0f0f0f, v50
	v_dot4c_i32_i8_e32 v56, v44, v0
	v_lshrrev_b32_e32 v44, 4, v50
	v_and_b32_e32 v44, 0xf0f0f0f, v44
	v_dot4c_i32_i8_e32 v56, v44, v1
	v_and_b32_e32 v44, 0xf0f0f0f, v51
	v_dot4c_i32_i8_e32 v48, v44, v2
	v_lshrrev_b32_e32 v44, 4, v51
	v_and_b32_e32 v44, 0xf0f0f0f, v44
	v_dot4c_i32_i8_e32 v48, v44, v3
	v_add_u32_e32 v46, v46, v47
	v_sub_u32_e32 v46, v46, v84
	s_waitcnt vmcnt(20)
; #define P12_ISSUE(c_, i_, h_, CW_, SC_) do { _Pragma("unroll") for (int bb = 0; bb < 8; ++bb) { const unsigned ro = (unsigned)(c_) * 16384u + (unsigned)EL[(i_) * 128 + ((h_) * 8 + bb) * 8 + g8]; \
;         CW_[bb] = *(const v4u*)(U4 + (size_t)(ro * 128u + 16u * (unsigned)k8)); SC_[bb] = USS[(size_t)(ro * 8u + (unsigned)k8)]; } } while (0)
; #define P12_COMP(i_, h_, CW_, SC_) do { _Pragma("unroll") for (int bb = 0; bb < 8; ++bb) { int a0 = 0, a1 = 0; P12_U4(CW_[bb].x, xa.x, xa.y, a0); P12_U4(CW_[bb].y, xa.z, xa.w, a1); P12_U4(CW_[bb].z, xb.x, xb.y, a0); P12_U4(CW_[bb].w, xb.z, xb.w, a1); \
;         psum[(i_)][(h_) * 8 + bb] += __uint_as_float(SC_[bb] << 16) * (float)((a0 + a1) - xo); } } while (0)
; #define P12_BAR() asm volatile("" ::: "memory")
; __device__ __forceinline__ void p12_peer(Frame& F) {
;     ...
;     { v4u cwA[8], cwB[8]; unsigned scA[8], scB[8]; v4u xa, xb; int xo;
;       P12_ISSUE(0, 0, 0, cwA, scA);
; _Pragma("nounroll")
;       for (int c = 0; c < 16; ++c) { const int cn = c + 1 < 16 ? c + 1 : 15;
;           P12_XQ(c, 0); P12_ISSUE(c, 0, 1, cwB, scB); P12_BAR(); P12_COMP(0, 0, cwA, scA); P12_ISSUE(c, 1, 0, cwA, scA); P12_BAR(); P12_COMP(0, 1, cwB, scB);
;           P12_XQ(c, 1); P12_ISSUE(c, 1, 1, cwB, scB); P12_BAR(); P12_COMP(1, 0, cwA, scA); P12_ISSUE(c, 2, 0, cwA, scA); P12_BAR(); P12_COMP(1, 1, cwB, scB);
;           P12_XQ(c, 2); P12_ISSUE(c, 2, 1, cwB, scB); P12_BAR(); P12_COMP(2, 0, cwA, scA); P12_ISSUE(c, 3, 0, cwA, scA); P12_BAR(); P12_COMP(2, 1, cwB, scB);
;           P12_XQ(c, 3); P12_ISSUE(c, 3, 1, cwB, scB); P12_BAR(); P12_COMP(3, 0, cwA, scA); P12_ISSUE(cn, 0, 0, cwA, scA); P12_BAR(); P12_COMP(3, 1, cwB, scB);
	v_lshlrev_b32_e32 v45, 16, v202
	v_add_u32_e32 v47, v56, v48
	v_sub_u32_e32 v48, v47, v84
	v_cvt_f32_i32_e32 v47, v46
	v_cvt_f32_i32_e32 v46, v48
	v_lshlrev_b32_e32 v44, 16, v203
	v_pk_fma_f32 v[140:141], v[44:45], v[46:47], v[140:141]
	v_and_b32_e32 v44, 0xf0f0f0f, v40
	v_mov_b32_e32 v45, 0
	v_lshrrev_b32_e32 v40, 4, v40
	v_dot4c_i32_i8_e32 v45, v44, v4
	v_and_b32_e32 v40, 0xf0f0f0f, v40
	v_dot4c_i32_i8_e32 v45, v40, v5
	v_and_b32_e32 v40, 0xf0f0f0f, v41
	v_mov_b32_e32 v44, 0
	v_dot4c_i32_i8_e32 v44, v40, v6
	v_lshrrev_b32_e32 v40, 4, v41
	v_and_b32_e32 v40, 0xf0f0f0f, v40
	v_dot4c_i32_i8_e32 v44, v40, v7
	v_and_b32_e32 v40, 0xf0f0f0f, v42
	v_dot4c_i32_i8_e32 v45, v40, v0
	v_lshrrev_b32_e32 v40, 4, v42
	v_and_b32_e32 v40, 0xf0f0f0f, v40
	v_dot4c_i32_i8_e32 v45, v40, v1
	v_and_b32_e32 v40, 0xf0f0f0f, v43
	v_dot4c_i32_i8_e32 v44, v40, v2
	v_lshrrev_b32_e32 v40, 4, v43
	v_and_b32_e32 v40, 0xf0f0f0f, v40
	v_dot4c_i32_i8_e32 v44, v40, v3
	v_and_b32_e32 v40, 0xf0f0f0f, v24
	v_mov_b32_e32 v41, 0
	v_lshrrev_b32_e32 v24, 4, v24
	v_dot4c_i32_i8_e32 v41, v40, v4
	v_and_b32_e32 v24, 0xf0f0f0f, v24
	v_dot4c_i32_i8_e32 v41, v24, v5
	v_and_b32_e32 v24, 0xf0f0f0f, v25
	v_mov_b32_e32 v40, 0
	v_dot4c_i32_i8_e32 v40, v24, v6
	v_lshrrev_b32_e32 v24, 4, v25
	v_and_b32_e32 v24, 0xf0f0f0f, v24
	v_dot4c_i32_i8_e32 v40, v24, v7
	v_and_b32_e32 v24, 0xf0f0f0f, v26
	v_dot4c_i32_i8_e32 v41, v24, v0
	v_lshrrev_b32_e32 v24, 4, v26
	v_and_b32_e32 v24, 0xf0f0f0f, v24
	v_dot4c_i32_i8_e32 v41, v24, v1
	v_and_b32_e32 v24, 0xf0f0f0f, v27
	v_dot4c_i32_i8_e32 v40, v24, v2
	v_lshrrev_b32_e32 v24, 4, v27
	v_and_b32_e32 v24, 0xf0f0f0f, v24
	v_dot4c_i32_i8_e32 v40, v24, v3
	v_add_u32_e32 v26, v45, v44
	v_sub_u32_e32 v26, v26, v84
	s_waitcnt vmcnt(18)
	v_lshlrev_b32_e32 v25, 16, v204
	v_add_u32_e32 v27, v41, v40
	v_sub_u32_e32 v40, v27, v84
	v_cvt_f32_i32_e32 v27, v26
	v_cvt_f32_i32_e32 v26, v40
	v_lshlrev_b32_e32 v24, 16, v205
	v_pk_fma_f32 v[138:139], v[24:25], v[26:27], v[138:139]
	v_and_b32_e32 v24, 0xf0f0f0f, v12
	v_mov_b32_e32 v25, 0
	v_lshrrev_b32_e32 v12, 4, v12
	v_dot4c_i32_i8_e32 v25, v24, v4
	v_and_b32_e32 v12, 0xf0f0f0f, v12
	v_dot4c_i32_i8_e32 v25, v12, v5
	v_and_b32_e32 v12, 0xf0f0f0f, v13
	v_mov_b32_e32 v24, 0
	v_dot4c_i32_i8_e32 v24, v12, v6
	v_lshrrev_b32_e32 v12, 4, v13
	v_and_b32_e32 v12, 0xf0f0f0f, v12
	v_dot4c_i32_i8_e32 v24, v12, v7
	v_and_b32_e32 v12, 0xf0f0f0f, v14
	v_dot4c_i32_i8_e32 v25, v12, v0
	v_lshrrev_b32_e32 v12, 4, v14
	v_and_b32_e32 v12, 0xf0f0f0f, v12
	v_dot4c_i32_i8_e32 v25, v12, v1
	v_and_b32_e32 v12, 0xf0f0f0f, v15
	v_dot4c_i32_i8_e32 v24, v12, v2
	v_lshrrev_b32_e32 v12, 4, v15
	v_and_b32_e32 v12, 0xf0f0f0f, v12
	v_dot4c_i32_i8_e32 v24, v12, v3
	v_and_b32_e32 v12, 0xf0f0f0f, v8
	v_mov_b32_e32 v13, 0
	v_lshrrev_b32_e32 v8, 4, v8
	v_dot4c_i32_i8_e32 v13, v12, v4
	v_and_b32_e32 v8, 0xf0f0f0f, v8
	v_dot4c_i32_i8_e32 v13, v8, v5
	v_and_b32_e32 v8, 0xf0f0f0f, v9
	v_mov_b32_e32 v12, 0
	v_dot4c_i32_i8_e32 v12, v8, v6
	v_lshrrev_b32_e32 v8, 4, v9
	v_and_b32_e32 v8, 0xf0f0f0f, v8
	v_dot4c_i32_i8_e32 v12, v8, v7
	v_and_b32_e32 v8, 0xf0f0f0f, v10
	v_dot4c_i32_i8_e32 v13, v8, v0
	v_lshrrev_b32_e32 v8, 4, v10
	v_and_b32_e32 v8, 0xf0f0f0f, v8
	v_dot4c_i32_i8_e32 v13, v8, v1
	v_and_b32_e32 v8, 0xf0f0f0f, v11
	v_dot4c_i32_i8_e32 v12, v8, v2
	v_lshrrev_b32_e32 v8, 4, v11
	v_and_b32_e32 v8, 0xf0f0f0f, v8
	v_dot4c_i32_i8_e32 v12, v8, v3
	v_add_u32_e32 v10, v25, v24
	v_sub_u32_e32 v10, v10, v84
	s_waitcnt vmcnt(16)
	v_lshlrev_b32_e32 v9, 16, v206
	v_add_u32_e32 v11, v13, v12
	v_sub_u32_e32 v12, v11, v84
	v_cvt_f32_i32_e32 v11, v10
	v_cvt_f32_i32_e32 v10, v12
	v_lshlrev_b32_e32 v8, 16, v207
	v_pk_fma_f32 v[136:137], v[8:9], v[10:11], v[136:137]
	ds_read_u16 v8, v93 offset:16896
	ds_read_u16 v9, v93 offset:16912
	ds_read_u16 v10, v93 offset:16928
	ds_read_u16 v11, v93 offset:16944
	s_waitcnt lgkmcnt(3)
	v_add_u32_e32 v8, s44, v8
	v_lshl_or_b32 v12, v8, 7, v165
	v_lshl_or_b32 v40, v8, 5, v248
	s_waitcnt lgkmcnt(2)
	v_add_u32_e32 v8, s44, v9
	v_lshl_or_b32 v9, v8, 7, v165
	v_lshl_or_b32 v41, v8, 5, v248
	s_waitcnt lgkmcnt(1)
	v_add_u32_e32 v8, s44, v10
	global_load_dwordx4 v[76:79], v12, s[0:1]
	global_load_dwordx4 v[72:75], v9, s[0:1]
	v_lshl_or_b32 v9, v8, 7, v165
	v_lshl_or_b32 v42, v8, 5, v248
	s_waitcnt lgkmcnt(0)
	v_add_u32_e32 v8, s44, v11
	global_load_dwordx4 v[60:63], v9, s[0:1]
	v_lshl_or_b32 v9, v8, 7, v165
	v_lshl_or_b32 v43, v8, 5, v248
	ds_read_u16 v8, v93 offset:16960
	global_load_dwordx4 v[56:59], v9, s[0:1]
	s_waitcnt lgkmcnt(0)
	v_add_u32_e32 v8, s44, v8
	v_lshl_or_b32 v9, v8, 7, v165
	v_lshl_or_b32 v48, v8, 5, v248
	ds_read_u16 v8, v93 offset:16976
	global_load_dwordx4 v[44:47], v9, s[0:1]
	s_waitcnt lgkmcnt(0)
	v_add_u32_e32 v8, s44, v8
	v_lshl_or_b32 v9, v8, 7, v165
	v_lshl_or_b32 v49, v8, 5, v248
	ds_read_u16 v8, v93 offset:16992
	global_load_dwordx4 v[24:27], v9, s[0:1]
	s_waitcnt lgkmcnt(0)
	v_add_u32_e32 v8, s44, v8
	v_lshl_or_b32 v9, v8, 7, v165
	v_lshl_or_b32 v50, v8, 5, v248
	ds_read_u16 v8, v93 offset:17008
	global_load_dwordx4 v[12:15], v9, s[0:1]
	s_waitcnt lgkmcnt(0)
	v_add_u32_e32 v51, s44, v8
	v_lshl_or_b32 v8, v51, 7, v165
	global_load_dwordx4 v[8:11], v8, s[0:1]
	v_lshl_or_b32 v51, v51, 5, v248
	global_load_dword v217, v41, s[46:47]
	global_load_dword v216, v40, s[46:47]
	global_load_dword v219, v43, s[46:47]
	global_load_dword v218, v42, s[46:47]
	global_load_dword v221, v49, s[46:47]
	global_load_dword v220, v48, s[46:47]
	global_load_dword v223, v51, s[46:47]
	global_load_dword v222, v50, s[46:47]
	s_waitcnt vmcnt(31)
; #define P12_ISSUE(c_, i_, h_, CW_, SC_) do { _Pragma("unroll") for (int bb = 0; bb < 8; ++bb) { const unsigned ro = (unsigned)(c_) * 16384u + (unsigned)EL[(i_) * 128 + ((h_) * 8 + bb) * 8 + g8]; \
;         CW_[bb] = *(const v4u*)(U4 + (size_t)(ro * 128u + 16u * (unsigned)k8)); SC_[bb] = USS[(size_t)(ro * 8u + (unsigned)k8)]; } } while (0)
; #define P12_COMP(i_, h_, CW_, SC_) do { _Pragma("unroll") for (int bb = 0; bb < 8; ++bb) { int a0 = 0, a1 = 0; P12_U4(CW_[bb].x, xa.x, xa.y, a0); P12_U4(CW_[bb].y, xa.z, xa.w, a1); P12_U4(CW_[bb].z, xb.x, xb.y, a0); P12_U4(CW_[bb].w, xb.z, xb.w, a1); \
;         psum[(i_)][(h_) * 8 + bb] += __uint_as_float(SC_[bb] << 16) * (float)((a0 + a1) - xo); } } while (0)
; #define P12_BAR() asm volatile("" ::: "memory")
; __device__ __forceinline__ void p12_peer(Frame& F) {
;     ...
;     { v4u cwA[8], cwB[8]; unsigned scA[8], scB[8]; v4u xa, xb; int xo;
;       P12_ISSUE(0, 0, 0, cwA, scA);
; _Pragma("nounroll")
;       for (int c = 0; c < 16; ++c) { const int cn = c + 1 < 16 ? c + 1 : 15;
;           P12_XQ(c, 0); P12_ISSUE(c, 0, 1, cwB, scB); P12_BAR(); P12_COMP(0, 0, cwA, scA); P12_ISSUE(c, 1, 0, cwA, scA); P12_BAR(); P12_COMP(0, 1, cwB, scB);
;           P12_XQ(c, 1); P12_ISSUE(c, 1, 1, cwB, scB); P12_BAR(); P12_COMP(1, 0, cwA, scA); P12_ISSUE(c, 2, 0, cwA, scA); P12_BAR(); P12_COMP(1, 1, cwB, scB);
;           P12_XQ(c, 2); P12_ISSUE(c, 2, 1, cwB, scB); P12_BAR(); P12_COMP(2, 0, cwA, scA); P12_ISSUE(c, 3, 0, cwA, scA); P12_BAR(); P12_COMP(2, 1, cwB, scB);
;           P12_XQ(c, 3); P12_ISSUE(c, 3, 1, cwB, scB); P12_BAR(); P12_COMP(3, 0, cwA, scA); P12_ISSUE(cn, 0, 0, cwA, scA); P12_BAR(); P12_COMP(3, 1, cwB, scB);
	v_and_b32_e32 v40, 0xf0f0f0f, v80
	v_mov_b32_e32 v42, 0
	v_dot4c_i32_i8_e32 v42, v40, v4
	v_lshrrev_b32_e32 v40, 4, v80
	v_and_b32_e32 v40, 0xf0f0f0f, v40
	v_dot4c_i32_i8_e32 v42, v40, v5
	v_and_b32_e32 v40, 0xf0f0f0f, v81
	v_mov_b32_e32 v43, 0
	v_dot4c_i32_i8_e32 v43, v40, v6
	v_lshrrev_b32_e32 v40, 4, v81
	v_and_b32_e32 v40, 0xf0f0f0f, v40
	v_dot4c_i32_i8_e32 v43, v40, v7
	v_and_b32_e32 v40, 0xf0f0f0f, v82
	v_dot4c_i32_i8_e32 v42, v40, v0
	v_lshrrev_b32_e32 v40, 4, v82
	v_and_b32_e32 v40, 0xf0f0f0f, v40
	v_dot4c_i32_i8_e32 v42, v40, v1
	v_and_b32_e32 v40, 0xf0f0f0f, v83
	v_dot4c_i32_i8_e32 v43, v40, v2
	v_lshrrev_b32_e32 v40, 4, v83
	v_and_b32_e32 v40, 0xf0f0f0f, v40
	v_dot4c_i32_i8_e32 v43, v40, v3
	s_waitcnt vmcnt(30)
	v_and_b32_e32 v40, 0xf0f0f0f, v68
	v_mov_b32_e32 v48, 0
	v_dot4c_i32_i8_e32 v48, v40, v4
	v_lshrrev_b32_e32 v40, 4, v68
	v_and_b32_e32 v40, 0xf0f0f0f, v40
	v_dot4c_i32_i8_e32 v48, v40, v5
	v_and_b32_e32 v40, 0xf0f0f0f, v69
	v_mov_b32_e32 v49, 0
	v_dot4c_i32_i8_e32 v49, v40, v6
	v_lshrrev_b32_e32 v40, 4, v69
	v_and_b32_e32 v40, 0xf0f0f0f, v40
	v_dot4c_i32_i8_e32 v49, v40, v7
	v_and_b32_e32 v40, 0xf0f0f0f, v70
	v_dot4c_i32_i8_e32 v48, v40, v0
	v_lshrrev_b32_e32 v40, 4, v70
	v_and_b32_e32 v40, 0xf0f0f0f, v40
	v_dot4c_i32_i8_e32 v48, v40, v1
	v_and_b32_e32 v40, 0xf0f0f0f, v71
	v_dot4c_i32_i8_e32 v49, v40, v2
	v_lshrrev_b32_e32 v40, 4, v71
	v_and_b32_e32 v40, 0xf0f0f0f, v40
	v_dot4c_i32_i8_e32 v49, v40, v3
	v_add_u32_e32 v42, v42, v43
	v_sub_u32_e32 v42, v42, v84
	s_waitcnt vmcnt(22)
	v_lshlrev_b32_e32 v41, 16, v208
	v_sub_u32_e32 v43, v49, v84
	v_add_u32_e32 v48, v43, v48
	v_cvt_f32_i32_e32 v43, v42
	v_cvt_f32_i32_e32 v42, v48
	v_lshlrev_b32_e32 v40, 16, v209
	v_pk_fma_f32 v[134:135], v[40:41], v[42:43], v[134:135]
	v_and_b32_e32 v40, 0xf0f0f0f, v52
	v_mov_b32_e32 v41, 0
	v_dot4c_i32_i8_e32 v41, v40, v4
	v_lshrrev_b32_e32 v40, 4, v52
	v_and_b32_e32 v40, 0xf0f0f0f, v40
	v_dot4c_i32_i8_e32 v41, v40, v5
	v_and_b32_e32 v40, 0xf0f0f0f, v53
	v_mov_b32_e32 v42, 0
	v_dot4c_i32_i8_e32 v42, v40, v6
	v_lshrrev_b32_e32 v40, 4, v53
	v_and_b32_e32 v40, 0xf0f0f0f, v40
	v_dot4c_i32_i8_e32 v42, v40, v7
	v_and_b32_e32 v40, 0xf0f0f0f, v54
	v_dot4c_i32_i8_e32 v41, v40, v0
	v_lshrrev_b32_e32 v40, 4, v54
	v_and_b32_e32 v40, 0xf0f0f0f, v40
	v_dot4c_i32_i8_e32 v41, v40, v1
	v_and_b32_e32 v40, 0xf0f0f0f, v55
	v_dot4c_i32_i8_e32 v42, v40, v2
	v_lshrrev_b32_e32 v40, 4, v55
	v_and_b32_e32 v40, 0xf0f0f0f, v40
	v_dot4c_i32_i8_e32 v42, v40, v3
	v_and_b32_e32 v40, 0xf0f0f0f, v36
	v_mov_b32_e32 v43, 0
	v_lshrrev_b32_e32 v36, 4, v36
	v_dot4c_i32_i8_e32 v43, v40, v4
	v_and_b32_e32 v36, 0xf0f0f0f, v36
	v_dot4c_i32_i8_e32 v43, v36, v5
	v_and_b32_e32 v36, 0xf0f0f0f, v37
	v_mov_b32_e32 v40, 0
	v_dot4c_i32_i8_e32 v40, v36, v6
	v_lshrrev_b32_e32 v36, 4, v37
	v_and_b32_e32 v36, 0xf0f0f0f, v36
	v_dot4c_i32_i8_e32 v40, v36, v7
	v_and_b32_e32 v36, 0xf0f0f0f, v38
	v_dot4c_i32_i8_e32 v43, v36, v0
	v_lshrrev_b32_e32 v36, 4, v38
	v_and_b32_e32 v36, 0xf0f0f0f, v36
	v_dot4c_i32_i8_e32 v43, v36, v1
	v_and_b32_e32 v36, 0xf0f0f0f, v39
	v_dot4c_i32_i8_e32 v40, v36, v2
	v_lshrrev_b32_e32 v36, 4, v39
	v_and_b32_e32 v36, 0xf0f0f0f, v36
	v_dot4c_i32_i8_e32 v40, v36, v3
	v_sub_u32_e32 v38, v42, v84
	v_add_u32_e32 v38, v38, v41
	s_waitcnt vmcnt(20)
	v_lshlrev_b32_e32 v37, 16, v210
	v_sub_u32_e32 v39, v40, v84
	v_add_u32_e32 v40, v39, v43
	v_cvt_f32_i32_e32 v39, v38
	v_cvt_f32_i32_e32 v38, v40
	v_lshlrev_b32_e32 v36, 16, v211
	v_pk_fma_f32 v[132:133], v[36:37], v[38:39], v[132:133]
	v_and_b32_e32 v36, 0xf0f0f0f, v32
	v_mov_b32_e32 v37, 0
	v_lshrrev_b32_e32 v32, 4, v32
	v_dot4c_i32_i8_e32 v37, v36, v4
	v_and_b32_e32 v32, 0xf0f0f0f, v32
	v_dot4c_i32_i8_e32 v37, v32, v5
	v_and_b32_e32 v32, 0xf0f0f0f, v33
	v_mov_b32_e32 v36, 0
	v_dot4c_i32_i8_e32 v36, v32, v6
	v_lshrrev_b32_e32 v32, 4, v33
	v_and_b32_e32 v32, 0xf0f0f0f, v32
	v_dot4c_i32_i8_e32 v36, v32, v7
	v_and_b32_e32 v32, 0xf0f0f0f, v34
	v_dot4c_i32_i8_e32 v37, v32, v0
	v_lshrrev_b32_e32 v32, 4, v34
	v_and_b32_e32 v32, 0xf0f0f0f, v32
	v_dot4c_i32_i8_e32 v37, v32, v1
	v_and_b32_e32 v32, 0xf0f0f0f, v35
	v_dot4c_i32_i8_e32 v36, v32, v2
	v_lshrrev_b32_e32 v32, 4, v35
	v_and_b32_e32 v32, 0xf0f0f0f, v32
	v_dot4c_i32_i8_e32 v36, v32, v3
	v_and_b32_e32 v32, 0xf0f0f0f, v28
	v_mov_b32_e32 v33, 0
	v_lshrrev_b32_e32 v28, 4, v28
	v_dot4c_i32_i8_e32 v33, v32, v4
	v_and_b32_e32 v28, 0xf0f0f0f, v28
	v_dot4c_i32_i8_e32 v33, v28, v5
	v_and_b32_e32 v28, 0xf0f0f0f, v29
	v_mov_b32_e32 v32, 0
	v_dot4c_i32_i8_e32 v32, v28, v6
	v_lshrrev_b32_e32 v28, 4, v29
	v_and_b32_e32 v28, 0xf0f0f0f, v28
	v_dot4c_i32_i8_e32 v32, v28, v7
	v_and_b32_e32 v28, 0xf0f0f0f, v30
	v_dot4c_i32_i8_e32 v33, v28, v0
	v_lshrrev_b32_e32 v28, 4, v30
	v_and_b32_e32 v28, 0xf0f0f0f, v28
	v_dot4c_i32_i8_e32 v33, v28, v1
	v_and_b32_e32 v28, 0xf0f0f0f, v31
	v_dot4c_i32_i8_e32 v32, v28, v2
	v_lshrrev_b32_e32 v28, 4, v31
	v_and_b32_e32 v28, 0xf0f0f0f, v28
	v_dot4c_i32_i8_e32 v32, v28, v3
	v_sub_u32_e32 v30, v36, v84
	v_add_u32_e32 v30, v30, v37
	s_waitcnt vmcnt(18)
; #define P12_ISSUE(c_, i_, h_, CW_, SC_) do { _Pragma("unroll") for (int bb = 0; bb < 8; ++bb) { const unsigned ro = (unsigned)(c_) * 16384u + (unsigned)EL[(i_) * 128 + ((h_) * 8 + bb) * 8 + g8]; \
;         CW_[bb] = *(const v4u*)(U4 + (size_t)(ro * 128u + 16u * (unsigned)k8)); SC_[bb] = USS[(size_t)(ro * 8u + (unsigned)k8)]; } } while (0)
; #define P12_COMP(i_, h_, CW_, SC_) do { _Pragma("unroll") for (int bb = 0; bb < 8; ++bb) { int a0 = 0, a1 = 0; P12_U4(CW_[bb].x, xa.x, xa.y, a0); P12_U4(CW_[bb].y, xa.z, xa.w, a1); P12_U4(CW_[bb].z, xb.x, xb.y, a0); P12_U4(CW_[bb].w, xb.z, xb.w, a1); \
;         psum[(i_)][(h_) * 8 + bb] += __uint_as_float(SC_[bb] << 16) * (float)((a0 + a1) - xo); } } while (0)
; #define P12_BAR() asm volatile("" ::: "memory")
; __device__ __forceinline__ void p12_peer(Frame& F) {
;     ...
;     { v4u cwA[8], cwB[8]; unsigned scA[8], scB[8]; v4u xa, xb; int xo;
;       P12_ISSUE(0, 0, 0, cwA, scA);
; _Pragma("nounroll")
;       for (int c = 0; c < 16; ++c) { const int cn = c + 1 < 16 ? c + 1 : 15;
;           P12_XQ(c, 0); P12_ISSUE(c, 0, 1, cwB, scB); P12_BAR(); P12_COMP(0, 0, cwA, scA); P12_ISSUE(c, 1, 0, cwA, scA); P12_BAR(); P12_COMP(0, 1, cwB, scB);
;           P12_XQ(c, 1); P12_ISSUE(c, 1, 1, cwB, scB); P12_BAR(); P12_COMP(1, 0, cwA, scA); P12_ISSUE(c, 2, 0, cwA, scA); P12_BAR(); P12_COMP(1, 1, cwB, scB);
;           P12_XQ(c, 2); P12_ISSUE(c, 2, 1, cwB, scB); P12_BAR(); P12_COMP(2, 0, cwA, scA); P12_ISSUE(c, 3, 0, cwA, scA); P12_BAR(); P12_COMP(2, 1, cwB, scB);
;           P12_XQ(c, 3); P12_ISSUE(c, 3, 1, cwB, scB); P12_BAR(); P12_COMP(3, 0, cwA, scA); P12_ISSUE(cn, 0, 0, cwA, scA); P12_BAR(); P12_COMP(3, 1, cwB, scB);
	v_lshlrev_b32_e32 v29, 16, v212
	v_sub_u32_e32 v31, v32, v84
	v_add_u32_e32 v32, v31, v33
	v_cvt_f32_i32_e32 v31, v30
	v_cvt_f32_i32_e32 v30, v32
	v_lshlrev_b32_e32 v28, 16, v213
	v_pk_fma_f32 v[130:131], v[28:29], v[30:31], v[130:131]
	v_and_b32_e32 v28, 0xf0f0f0f, v20
	v_mov_b32_e32 v29, 0
	v_lshrrev_b32_e32 v20, 4, v20
	v_dot4c_i32_i8_e32 v29, v28, v4
	v_and_b32_e32 v20, 0xf0f0f0f, v20
	v_dot4c_i32_i8_e32 v29, v20, v5
	v_and_b32_e32 v20, 0xf0f0f0f, v21
	v_mov_b32_e32 v28, 0
	v_dot4c_i32_i8_e32 v28, v20, v6
	v_lshrrev_b32_e32 v20, 4, v21
	v_and_b32_e32 v20, 0xf0f0f0f, v20
	v_dot4c_i32_i8_e32 v28, v20, v7
	v_and_b32_e32 v20, 0xf0f0f0f, v22
	v_dot4c_i32_i8_e32 v29, v20, v0
	v_lshrrev_b32_e32 v20, 4, v22
	v_and_b32_e32 v20, 0xf0f0f0f, v20
	v_dot4c_i32_i8_e32 v29, v20, v1
	v_and_b32_e32 v20, 0xf0f0f0f, v23
	v_dot4c_i32_i8_e32 v28, v20, v2
	v_lshrrev_b32_e32 v20, 4, v23
	v_and_b32_e32 v20, 0xf0f0f0f, v20
	v_dot4c_i32_i8_e32 v28, v20, v3
	v_and_b32_e32 v20, 0xf0f0f0f, v16
	v_mov_b32_e32 v21, 0
	v_dot4c_i32_i8_e32 v21, v20, v4
	v_lshrrev_b32_e32 v4, 4, v16
	v_and_b32_e32 v4, 0xf0f0f0f, v4
	v_dot4c_i32_i8_e32 v21, v4, v5
	v_and_b32_e32 v4, 0xf0f0f0f, v17
	v_mov_b32_e32 v5, 0
	v_dot4c_i32_i8_e32 v5, v4, v6
	v_lshrrev_b32_e32 v4, 4, v17
	v_and_b32_e32 v4, 0xf0f0f0f, v4
	v_dot4c_i32_i8_e32 v5, v4, v7
	v_and_b32_e32 v4, 0xf0f0f0f, v18
	v_dot4c_i32_i8_e32 v21, v4, v0
	v_lshrrev_b32_e32 v0, 4, v18
	v_and_b32_e32 v0, 0xf0f0f0f, v0
	v_dot4c_i32_i8_e32 v21, v0, v1
	v_and_b32_e32 v0, 0xf0f0f0f, v19
	v_dot4c_i32_i8_e32 v5, v0, v2
	v_lshrrev_b32_e32 v0, 4, v19
	v_and_b32_e32 v0, 0xf0f0f0f, v0
	v_dot4c_i32_i8_e32 v5, v0, v3
	v_sub_u32_e32 v2, v28, v84
	v_add_u32_e32 v2, v2, v29
	s_waitcnt vmcnt(16)
	v_lshlrev_b32_e32 v1, 16, v214
	v_sub_u32_e32 v3, v5, v84
	v_add_u32_e32 v4, v3, v21
	v_cvt_f32_i32_e32 v3, v2
	v_cvt_f32_i32_e32 v2, v4
	v_lshlrev_b32_e32 v0, 16, v215
	ds_read_b128 v[32:35], v166 offset:8192
	ds_read_b128 v[28:31], v166 offset:8208
	v_pk_fma_f32 v[128:129], v[0:1], v[2:3], v[128:129]
	ds_read_u16 v1, v93 offset:17024
	ds_read_u16 v2, v93 offset:17040
	ds_read_u16 v3, v93 offset:17056
	ds_read_u16 v4, v93 offset:17072
	v_mov_b32_e32 v0, 0
	s_waitcnt lgkmcnt(3)
	v_add_u32_e32 v1, s44, v1
	v_lshl_or_b32 v5, v1, 7, v165
	s_waitcnt lgkmcnt(2)
	v_add_u32_e32 v2, s44, v2
	global_load_dwordx4 v[84:87], v5, s[0:1]
	v_lshl_or_b32 v5, v2, 7, v165
	s_waitcnt lgkmcnt(1)
	v_add_u32_e32 v3, s44, v3
	global_load_dwordx4 v[80:83], v5, s[0:1]
	v_lshl_or_b32 v5, v3, 7, v165
	s_waitcnt lgkmcnt(0)
	v_add_u32_e32 v4, s44, v4
	global_load_dwordx4 v[68:71], v5, s[0:1]
	v_lshl_or_b32 v5, v4, 7, v165
	global_load_dwordx4 v[64:67], v5, s[0:1]
	ds_read_u16 v5, v93 offset:17088
	v_dot4c_i32_i8_e32 v0, 0x1010101, v32
	v_dot4c_i32_i8_e32 v0, 0x1010101, v33
	v_dot4c_i32_i8_e32 v0, 0x1010101, v34
	v_dot4c_i32_i8_e32 v0, 0x1010101, v35
	s_waitcnt lgkmcnt(0)
	v_add_u32_e32 v5, s44, v5
	v_lshl_or_b32 v6, v5, 7, v165
	global_load_dwordx4 v[52:55], v6, s[0:1]
	ds_read_u16 v6, v93 offset:17104
	v_dot4c_i32_i8_e32 v0, 0x1010101, v28
	v_dot4c_i32_i8_e32 v0, 0x1010101, v29
	v_dot4c_i32_i8_e32 v0, 0x1010101, v30
	v_dot4c_i32_i8_e32 v0, 0x1010101, v31
	s_waitcnt lgkmcnt(0)
	v_add_u32_e32 v6, s44, v6
	v_lshl_or_b32 v7, v6, 7, v165
	global_load_dwordx4 v[48:51], v7, s[0:1]
	ds_read_u16 v7, v93 offset:17120
	v_lshl_or_b32 v2, v2, 5, v248
	v_lshl_or_b32 v1, v1, 5, v248
	v_lshl_or_b32 v3, v3, 5, v248
	v_lshl_or_b32 v4, v4, 5, v248
	s_waitcnt lgkmcnt(0)
	v_add_u32_e32 v7, s44, v7
	v_lshl_or_b32 v16, v7, 7, v165
	global_load_dwordx4 v[40:43], v16, s[0:1]
	ds_read_u16 v16, v93 offset:17136
	v_lshl_or_b32 v5, v5, 5, v248
	v_lshl_or_b32 v6, v6, 5, v248
	v_lshl_or_b32 v7, v7, 5, v248
	v_lshlrev_b32_e32 v169, 3, v0
	s_waitcnt lgkmcnt(0)
	v_add_u32_e32 v16, s44, v16
	v_lshl_or_b32 v17, v16, 7, v165
	global_load_dwordx4 v[36:39], v17, s[0:1]
	v_lshl_or_b32 v16, v16, 5, v248
	global_load_dword v225, v2, s[46:47]
	global_load_dword v224, v1, s[46:47]
	global_load_dword v227, v4, s[46:47]
	global_load_dword v226, v3, s[46:47]
	global_load_dword v229, v6, s[46:47]
	global_load_dword v228, v5, s[46:47]
	global_load_dword v231, v16, s[46:47]
	global_load_dword v230, v7, s[46:47]
	s_waitcnt vmcnt(31)
	v_and_b32_e32 v0, 0xf0f0f0f, v76
	v_mov_b32_e32 v2, 0
	v_dot4c_i32_i8_e32 v2, v0, v32
	v_lshrrev_b32_e32 v0, 4, v76
	v_and_b32_e32 v0, 0xf0f0f0f, v0
	v_dot4c_i32_i8_e32 v2, v0, v33
	v_and_b32_e32 v0, 0xf0f0f0f, v77
	v_mov_b32_e32 v3, 0
	v_dot4c_i32_i8_e32 v3, v0, v34
	v_lshrrev_b32_e32 v0, 4, v77
	v_and_b32_e32 v0, 0xf0f0f0f, v0
	v_dot4c_i32_i8_e32 v3, v0, v35
	v_and_b32_e32 v0, 0xf0f0f0f, v78
	v_dot4c_i32_i8_e32 v2, v0, v28
	v_lshrrev_b32_e32 v0, 4, v78
	v_and_b32_e32 v0, 0xf0f0f0f, v0
	v_dot4c_i32_i8_e32 v2, v0, v29
	v_and_b32_e32 v0, 0xf0f0f0f, v79
	v_dot4c_i32_i8_e32 v3, v0, v30
	v_lshrrev_b32_e32 v0, 4, v79
	v_and_b32_e32 v0, 0xf0f0f0f, v0
	v_dot4c_i32_i8_e32 v3, v0, v31
	s_waitcnt vmcnt(30)
	v_and_b32_e32 v0, 0xf0f0f0f, v72
	v_mov_b32_e32 v4, 0
	v_dot4c_i32_i8_e32 v4, v0, v32
	v_lshrrev_b32_e32 v0, 4, v72
	v_and_b32_e32 v0, 0xf0f0f0f, v0
	v_dot4c_i32_i8_e32 v4, v0, v33
	v_and_b32_e32 v0, 0xf0f0f0f, v73
	v_mov_b32_e32 v5, 0
	v_dot4c_i32_i8_e32 v5, v0, v34
	v_lshrrev_b32_e32 v0, 4, v73
	v_and_b32_e32 v0, 0xf0f0f0f, v0
	v_dot4c_i32_i8_e32 v5, v0, v35
	v_and_b32_e32 v0, 0xf0f0f0f, v74
	v_dot4c_i32_i8_e32 v4, v0, v28
	v_lshrrev_b32_e32 v0, 4, v74
	v_and_b32_e32 v0, 0xf0f0f0f, v0
	v_dot4c_i32_i8_e32 v4, v0, v29
	v_and_b32_e32 v0, 0xf0f0f0f, v75
	v_dot4c_i32_i8_e32 v5, v0, v30
	v_lshrrev_b32_e32 v0, 4, v75
	v_and_b32_e32 v0, 0xf0f0f0f, v0
	v_dot4c_i32_i8_e32 v5, v0, v31
	v_add_u32_e32 v2, v2, v3
	v_sub_u32_e32 v2, v2, v169
	s_waitcnt vmcnt(22)
; #define P12_ISSUE(c_, i_, h_, CW_, SC_) do { _Pragma("unroll") for (int bb = 0; bb < 8; ++bb) { const unsigned ro = (unsigned)(c_) * 16384u + (unsigned)EL[(i_) * 128 + ((h_) * 8 + bb) * 8 + g8]; \
;         CW_[bb] = *(const v4u*)(U4 + (size_t)(ro * 128u + 16u * (unsigned)k8)); SC_[bb] = USS[(size_t)(ro * 8u + (unsigned)k8)]; } } while (0)
; #define P12_COMP(i_, h_, CW_, SC_) do { _Pragma("unroll") for (int bb = 0; bb < 8; ++bb) { int a0 = 0, a1 = 0; P12_U4(CW_[bb].x, xa.x, xa.y, a0); P12_U4(CW_[bb].y, xa.z, xa.w, a1); P12_U4(CW_[bb].z, xb.x, xb.y, a0); P12_U4(CW_[bb].w, xb.z, xb.w, a1); \
;         psum[(i_)][(h_) * 8 + bb] += __uint_as_float(SC_[bb] << 16) * (float)((a0 + a1) - xo); } } while (0)
; #define P12_BAR() asm volatile("" ::: "memory")
; __device__ __forceinline__ void p12_peer(Frame& F) {
;     ...
;     { v4u cwA[8], cwB[8]; unsigned scA[8], scB[8]; v4u xa, xb; int xo;
;       P12_ISSUE(0, 0, 0, cwA, scA);
; _Pragma("nounroll")
;       for (int c = 0; c < 16; ++c) { const int cn = c + 1 < 16 ? c + 1 : 15;
;           P12_XQ(c, 0); P12_ISSUE(c, 0, 1, cwB, scB); P12_BAR(); P12_COMP(0, 0, cwA, scA); P12_ISSUE(c, 1, 0, cwA, scA); P12_BAR(); P12_COMP(0, 1, cwB, scB);
;           P12_XQ(c, 1); P12_ISSUE(c, 1, 1, cwB, scB); P12_BAR(); P12_COMP(1, 0, cwA, scA); P12_ISSUE(c, 2, 0, cwA, scA); P12_BAR(); P12_COMP(1, 1, cwB, scB);
;           P12_XQ(c, 2); P12_ISSUE(c, 2, 1, cwB, scB); P12_BAR(); P12_COMP(2, 0, cwA, scA); P12_ISSUE(c, 3, 0, cwA, scA); P12_BAR(); P12_COMP(2, 1, cwB, scB);
;           P12_XQ(c, 3); P12_ISSUE(c, 3, 1, cwB, scB); P12_BAR(); P12_COMP(3, 0, cwA, scA); P12_ISSUE(cn, 0, 0, cwA, scA); P12_BAR(); P12_COMP(3, 1, cwB, scB);
	v_lshlrev_b32_e32 v1, 16, v216
	v_add_u32_e32 v3, v4, v5
	v_sub_u32_e32 v4, v3, v169
	v_cvt_f32_i32_e32 v3, v2
	v_cvt_f32_i32_e32 v2, v4
	v_lshlrev_b32_e32 v0, 16, v217
	v_mov_b32_e32 v4, 0
	v_mov_b32_e32 v5, 0
	v_pk_fma_f32 v[126:127], v[0:1], v[2:3], v[126:127]
	v_and_b32_e32 v0, 0xf0f0f0f, v60
	v_mov_b32_e32 v2, 0
	v_dot4c_i32_i8_e32 v2, v0, v32
	v_lshrrev_b32_e32 v0, 4, v60
	v_and_b32_e32 v0, 0xf0f0f0f, v0
	v_dot4c_i32_i8_e32 v2, v0, v33
	v_and_b32_e32 v0, 0xf0f0f0f, v61
	v_mov_b32_e32 v3, 0
	v_dot4c_i32_i8_e32 v3, v0, v34
	v_lshrrev_b32_e32 v0, 4, v61
	v_and_b32_e32 v0, 0xf0f0f0f, v0
	v_dot4c_i32_i8_e32 v3, v0, v35
	v_and_b32_e32 v0, 0xf0f0f0f, v62
	v_dot4c_i32_i8_e32 v2, v0, v28
	v_lshrrev_b32_e32 v0, 4, v62
	v_and_b32_e32 v0, 0xf0f0f0f, v0
	v_dot4c_i32_i8_e32 v2, v0, v29
	v_and_b32_e32 v0, 0xf0f0f0f, v63
	v_dot4c_i32_i8_e32 v3, v0, v30
	v_lshrrev_b32_e32 v0, 4, v63
	v_and_b32_e32 v0, 0xf0f0f0f, v0
	v_dot4c_i32_i8_e32 v3, v0, v31
	v_and_b32_e32 v0, 0xf0f0f0f, v56
	v_dot4c_i32_i8_e32 v4, v0, v32
	v_lshrrev_b32_e32 v0, 4, v56
	v_and_b32_e32 v0, 0xf0f0f0f, v0
	v_dot4c_i32_i8_e32 v4, v0, v33
	v_and_b32_e32 v0, 0xf0f0f0f, v57
	v_dot4c_i32_i8_e32 v5, v0, v34
	v_lshrrev_b32_e32 v0, 4, v57
	v_and_b32_e32 v0, 0xf0f0f0f, v0
	v_dot4c_i32_i8_e32 v5, v0, v35
	v_and_b32_e32 v0, 0xf0f0f0f, v58
	v_dot4c_i32_i8_e32 v4, v0, v28
	v_lshrrev_b32_e32 v0, 4, v58
	v_and_b32_e32 v0, 0xf0f0f0f, v0
	v_dot4c_i32_i8_e32 v4, v0, v29
	v_and_b32_e32 v0, 0xf0f0f0f, v59
	v_dot4c_i32_i8_e32 v5, v0, v30
	v_lshrrev_b32_e32 v0, 4, v59
	v_and_b32_e32 v0, 0xf0f0f0f, v0
	v_dot4c_i32_i8_e32 v5, v0, v31
	v_add_u32_e32 v2, v2, v3
	v_sub_u32_e32 v2, v2, v169
	s_waitcnt vmcnt(20)
	v_lshlrev_b32_e32 v1, 16, v218
	v_add_u32_e32 v3, v4, v5
	v_sub_u32_e32 v4, v3, v169
	v_cvt_f32_i32_e32 v3, v2
	v_cvt_f32_i32_e32 v2, v4
	v_lshlrev_b32_e32 v0, 16, v219
	v_mov_b32_e32 v4, 0
	v_mov_b32_e32 v5, 0
	v_pk_fma_f32 v[124:125], v[0:1], v[2:3], v[124:125]
	v_and_b32_e32 v0, 0xf0f0f0f, v44
	v_mov_b32_e32 v2, 0
	v_dot4c_i32_i8_e32 v2, v0, v32
	v_lshrrev_b32_e32 v0, 4, v44
	v_and_b32_e32 v0, 0xf0f0f0f, v0
	v_dot4c_i32_i8_e32 v2, v0, v33
	v_and_b32_e32 v0, 0xf0f0f0f, v45
	v_mov_b32_e32 v3, 0
	v_dot4c_i32_i8_e32 v3, v0, v34
	v_lshrrev_b32_e32 v0, 4, v45
	v_and_b32_e32 v0, 0xf0f0f0f, v0
	v_dot4c_i32_i8_e32 v3, v0, v35
	v_and_b32_e32 v0, 0xf0f0f0f, v46
	v_dot4c_i32_i8_e32 v2, v0, v28
	v_lshrrev_b32_e32 v0, 4, v46
	v_and_b32_e32 v0, 0xf0f0f0f, v0
	v_dot4c_i32_i8_e32 v2, v0, v29
	v_and_b32_e32 v0, 0xf0f0f0f, v47
	v_dot4c_i32_i8_e32 v3, v0, v30
	v_lshrrev_b32_e32 v0, 4, v47
	v_and_b32_e32 v0, 0xf0f0f0f, v0
	v_dot4c_i32_i8_e32 v3, v0, v31
	v_and_b32_e32 v0, 0xf0f0f0f, v24
	v_dot4c_i32_i8_e32 v4, v0, v32
	v_lshrrev_b32_e32 v0, 4, v24
	v_and_b32_e32 v0, 0xf0f0f0f, v0
	v_dot4c_i32_i8_e32 v4, v0, v33
	v_and_b32_e32 v0, 0xf0f0f0f, v25
	v_dot4c_i32_i8_e32 v5, v0, v34
	v_lshrrev_b32_e32 v0, 4, v25
	v_and_b32_e32 v0, 0xf0f0f0f, v0
	v_dot4c_i32_i8_e32 v5, v0, v35
	v_and_b32_e32 v0, 0xf0f0f0f, v26
	v_dot4c_i32_i8_e32 v4, v0, v28
	v_lshrrev_b32_e32 v0, 4, v26
	v_and_b32_e32 v0, 0xf0f0f0f, v0
	v_dot4c_i32_i8_e32 v4, v0, v29
	v_and_b32_e32 v0, 0xf0f0f0f, v27
	v_dot4c_i32_i8_e32 v5, v0, v30
	v_lshrrev_b32_e32 v0, 4, v27
	v_and_b32_e32 v0, 0xf0f0f0f, v0
	v_dot4c_i32_i8_e32 v5, v0, v31
	v_add_u32_e32 v2, v2, v3
	v_sub_u32_e32 v2, v2, v169
	s_waitcnt vmcnt(18)
	v_lshlrev_b32_e32 v1, 16, v220
	v_add_u32_e32 v3, v4, v5
	v_sub_u32_e32 v4, v3, v169
	v_cvt_f32_i32_e32 v3, v2
	v_cvt_f32_i32_e32 v2, v4
	v_lshlrev_b32_e32 v0, 16, v221
	v_mov_b32_e32 v4, 0
	v_mov_b32_e32 v5, 0
	v_pk_fma_f32 v[122:123], v[0:1], v[2:3], v[122:123]
	v_and_b32_e32 v0, 0xf0f0f0f, v12
	v_mov_b32_e32 v2, 0
	v_dot4c_i32_i8_e32 v2, v0, v32
	v_lshrrev_b32_e32 v0, 4, v12
	v_and_b32_e32 v0, 0xf0f0f0f, v0
	v_dot4c_i32_i8_e32 v2, v0, v33
	v_and_b32_e32 v0, 0xf0f0f0f, v13
	v_mov_b32_e32 v3, 0
	v_dot4c_i32_i8_e32 v3, v0, v34
	v_lshrrev_b32_e32 v0, 4, v13
	v_and_b32_e32 v0, 0xf0f0f0f, v0
	v_dot4c_i32_i8_e32 v3, v0, v35
	v_and_b32_e32 v0, 0xf0f0f0f, v14
	v_dot4c_i32_i8_e32 v2, v0, v28
	v_lshrrev_b32_e32 v0, 4, v14
	v_and_b32_e32 v0, 0xf0f0f0f, v0
	v_dot4c_i32_i8_e32 v2, v0, v29
	v_and_b32_e32 v0, 0xf0f0f0f, v15
	v_dot4c_i32_i8_e32 v3, v0, v30
	v_lshrrev_b32_e32 v0, 4, v15
	v_and_b32_e32 v0, 0xf0f0f0f, v0
	v_dot4c_i32_i8_e32 v3, v0, v31
	v_and_b32_e32 v0, 0xf0f0f0f, v8
	v_dot4c_i32_i8_e32 v4, v0, v32
	v_lshrrev_b32_e32 v0, 4, v8
	v_and_b32_e32 v0, 0xf0f0f0f, v0
	v_dot4c_i32_i8_e32 v4, v0, v33
	v_and_b32_e32 v0, 0xf0f0f0f, v9
	v_dot4c_i32_i8_e32 v5, v0, v34
	v_lshrrev_b32_e32 v0, 4, v9
	v_and_b32_e32 v0, 0xf0f0f0f, v0
	v_dot4c_i32_i8_e32 v5, v0, v35
	v_and_b32_e32 v0, 0xf0f0f0f, v10
	v_dot4c_i32_i8_e32 v4, v0, v28
	v_lshrrev_b32_e32 v0, 4, v10
	v_and_b32_e32 v0, 0xf0f0f0f, v0
	v_dot4c_i32_i8_e32 v4, v0, v29
	v_and_b32_e32 v0, 0xf0f0f0f, v11
	v_dot4c_i32_i8_e32 v5, v0, v30
	v_lshrrev_b32_e32 v0, 4, v11
	v_and_b32_e32 v0, 0xf0f0f0f, v0
	v_dot4c_i32_i8_e32 v5, v0, v31
	v_add_u32_e32 v2, v2, v3
	v_sub_u32_e32 v2, v2, v169
	s_waitcnt vmcnt(16)
	v_lshlrev_b32_e32 v1, 16, v222
	v_add_u32_e32 v3, v4, v5
	v_sub_u32_e32 v4, v3, v169
	v_cvt_f32_i32_e32 v3, v2
	v_cvt_f32_i32_e32 v2, v4
	v_lshlrev_b32_e32 v0, 16, v223
	v_pk_fma_f32 v[120:121], v[0:1], v[2:3], v[120:121]
	ds_read_u16 v0, v93 offset:17152
	ds_read_u16 v1, v93 offset:17168
	ds_read_u16 v2, v93 offset:17184
	ds_read_u16 v3, v93 offset:17200
	s_waitcnt lgkmcnt(3)
	v_add_u32_e32 v0, s44, v0
	v_lshl_or_b32 v4, v0, 7, v165
	v_lshl_or_b32 v44, v0, 5, v248
	s_waitcnt lgkmcnt(2)
	v_add_u32_e32 v0, s44, v1
	v_lshl_or_b32 v1, v0, 7, v165
	v_lshl_or_b32 v45, v0, 5, v248
	s_waitcnt lgkmcnt(1)
; #define P12_ISSUE(c_, i_, h_, CW_, SC_) do { _Pragma("unroll") for (int bb = 0; bb < 8; ++bb) { const unsigned ro = (unsigned)(c_) * 16384u + (unsigned)EL[(i_) * 128 + ((h_) * 8 + bb) * 8 + g8]; \
;         CW_[bb] = *(const v4u*)(U4 + (size_t)(ro * 128u + 16u * (unsigned)k8)); SC_[bb] = USS[(size_t)(ro * 8u + (unsigned)k8)]; } } while (0)
; #define P12_COMP(i_, h_, CW_, SC_) do { _Pragma("unroll") for (int bb = 0; bb < 8; ++bb) { int a0 = 0, a1 = 0; P12_U4(CW_[bb].x, xa.x, xa.y, a0); P12_U4(CW_[bb].y, xa.z, xa.w, a1); P12_U4(CW_[bb].z, xb.x, xb.y, a0); P12_U4(CW_[bb].w, xb.z, xb.w, a1); \
;         psum[(i_)][(h_) * 8 + bb] += __uint_as_float(SC_[bb] << 16) * (float)((a0 + a1) - xo); } } while (0)
; #define P12_BAR() asm volatile("" ::: "memory")
; __device__ __forceinline__ void p12_peer(Frame& F) {
;     ...
;     { v4u cwA[8], cwB[8]; unsigned scA[8], scB[8]; v4u xa, xb; int xo;
;       P12_ISSUE(0, 0, 0, cwA, scA);
; _Pragma("nounroll")
;       for (int c = 0; c < 16; ++c) { const int cn = c + 1 < 16 ? c + 1 : 15;
;           P12_XQ(c, 0); P12_ISSUE(c, 0, 1, cwB, scB); P12_BAR(); P12_COMP(0, 0, cwA, scA); P12_ISSUE(c, 1, 0, cwA, scA); P12_BAR(); P12_COMP(0, 1, cwB, scB);
;           P12_XQ(c, 1); P12_ISSUE(c, 1, 1, cwB, scB); P12_BAR(); P12_COMP(1, 0, cwA, scA); P12_ISSUE(c, 2, 0, cwA, scA); P12_BAR(); P12_COMP(1, 1, cwB, scB);
;           P12_XQ(c, 2); P12_ISSUE(c, 2, 1, cwB, scB); P12_BAR(); P12_COMP(2, 0, cwA, scA); P12_ISSUE(c, 3, 0, cwA, scA); P12_BAR(); P12_COMP(2, 1, cwB, scB);
;           P12_XQ(c, 3); P12_ISSUE(c, 3, 1, cwB, scB); P12_BAR(); P12_COMP(3, 0, cwA, scA); P12_ISSUE(cn, 0, 0, cwA, scA); P12_BAR(); P12_COMP(3, 1, cwB, scB);
	v_add_u32_e32 v0, s44, v2
	global_load_dwordx4 v[72:75], v4, s[0:1]
	global_load_dwordx4 v[24:27], v1, s[0:1]
	v_lshl_or_b32 v1, v0, 7, v165
	v_lshl_or_b32 v46, v0, 5, v248
	s_waitcnt lgkmcnt(0)
	v_add_u32_e32 v0, s44, v3
	global_load_dwordx4 v[20:23], v1, s[0:1]
	v_lshl_or_b32 v1, v0, 7, v165
	v_lshl_or_b32 v47, v0, 5, v248
	ds_read_u16 v0, v93 offset:17216
	global_load_dwordx4 v[16:19], v1, s[0:1]
	s_waitcnt lgkmcnt(0)
	v_add_u32_e32 v0, s44, v0
	v_lshl_or_b32 v1, v0, 7, v165
	v_lshl_or_b32 v56, v0, 5, v248
	ds_read_u16 v0, v93 offset:17232
	global_load_dwordx4 v[12:15], v1, s[0:1]
	s_waitcnt lgkmcnt(0)
	v_add_u32_e32 v0, s44, v0
	v_lshl_or_b32 v1, v0, 7, v165
	v_lshl_or_b32 v57, v0, 5, v248
	ds_read_u16 v0, v93 offset:17248
	global_load_dwordx4 v[8:11], v1, s[0:1]
	s_waitcnt lgkmcnt(0)
	v_add_u32_e32 v0, s44, v0
	v_lshl_or_b32 v1, v0, 7, v165
	v_lshl_or_b32 v58, v0, 5, v248
	ds_read_u16 v0, v93 offset:17264
	global_load_dwordx4 v[4:7], v1, s[0:1]
	s_waitcnt lgkmcnt(0)
	v_add_u32_e32 v59, s44, v0
	v_lshl_or_b32 v0, v59, 7, v165
	global_load_dwordx4 v[0:3], v0, s[0:1]
	v_lshl_or_b32 v59, v59, 5, v248
	global_load_dword v233, v45, s[46:47]
	global_load_dword v232, v44, s[46:47]
	global_load_dword v235, v47, s[46:47]
	global_load_dword v234, v46, s[46:47]
	global_load_dword v236, v56, s[46:47]
	global_load_dword v237, v57, s[46:47]
	global_load_dword v238, v58, s[46:47]
	global_load_dword v239, v59, s[46:47]
	s_waitcnt vmcnt(31)
	v_and_b32_e32 v44, 0xf0f0f0f, v84
	v_mov_b32_e32 v46, 0
	v_dot4c_i32_i8_e32 v46, v44, v32
	v_lshrrev_b32_e32 v44, 4, v84
	v_and_b32_e32 v44, 0xf0f0f0f, v44
	v_dot4c_i32_i8_e32 v46, v44, v33
	v_and_b32_e32 v44, 0xf0f0f0f, v85
	v_mov_b32_e32 v47, 0
	v_dot4c_i32_i8_e32 v47, v44, v34
	v_lshrrev_b32_e32 v44, 4, v85
	v_and_b32_e32 v44, 0xf0f0f0f, v44
	v_dot4c_i32_i8_e32 v47, v44, v35
	v_and_b32_e32 v44, 0xf0f0f0f, v86
	v_dot4c_i32_i8_e32 v46, v44, v28
	v_lshrrev_b32_e32 v44, 4, v86
	v_and_b32_e32 v44, 0xf0f0f0f, v44
	v_dot4c_i32_i8_e32 v46, v44, v29
	v_and_b32_e32 v44, 0xf0f0f0f, v87
	v_dot4c_i32_i8_e32 v47, v44, v30
	v_lshrrev_b32_e32 v44, 4, v87
	v_and_b32_e32 v44, 0xf0f0f0f, v44
	v_dot4c_i32_i8_e32 v47, v44, v31
	s_waitcnt vmcnt(30)
	v_and_b32_e32 v44, 0xf0f0f0f, v80
	v_mov_b32_e32 v56, 0
	v_dot4c_i32_i8_e32 v56, v44, v32
	v_lshrrev_b32_e32 v44, 4, v80
	v_and_b32_e32 v44, 0xf0f0f0f, v44
	v_dot4c_i32_i8_e32 v56, v44, v33
	v_and_b32_e32 v44, 0xf0f0f0f, v81
	v_mov_b32_e32 v57, 0
	v_dot4c_i32_i8_e32 v57, v44, v34
	v_lshrrev_b32_e32 v44, 4, v81
	v_and_b32_e32 v44, 0xf0f0f0f, v44
	v_dot4c_i32_i8_e32 v57, v44, v35
	v_and_b32_e32 v44, 0xf0f0f0f, v82
	v_dot4c_i32_i8_e32 v56, v44, v28
	v_lshrrev_b32_e32 v44, 4, v82
	v_and_b32_e32 v44, 0xf0f0f0f, v44
	v_dot4c_i32_i8_e32 v56, v44, v29
	v_and_b32_e32 v44, 0xf0f0f0f, v83
	v_dot4c_i32_i8_e32 v57, v44, v30
	v_lshrrev_b32_e32 v44, 4, v83
	v_and_b32_e32 v44, 0xf0f0f0f, v44
	v_dot4c_i32_i8_e32 v57, v44, v31
	v_add_u32_e32 v46, v46, v47
	v_sub_u32_e32 v46, v46, v169
	s_waitcnt vmcnt(22)
	v_lshlrev_b32_e32 v45, 16, v224
	v_sub_u32_e32 v47, v57, v169
	v_add_u32_e32 v56, v47, v56
	v_cvt_f32_i32_e32 v47, v46
	v_cvt_f32_i32_e32 v46, v56
	v_lshlrev_b32_e32 v44, 16, v225
	v_mov_b32_e32 v56, 0
	v_mov_b32_e32 v57, 0
	v_pk_fma_f32 v[118:119], v[44:45], v[46:47], v[118:119]
	v_and_b32_e32 v44, 0xf0f0f0f, v68
	v_mov_b32_e32 v46, 0
	v_dot4c_i32_i8_e32 v46, v44, v32
	v_lshrrev_b32_e32 v44, 4, v68
	v_and_b32_e32 v44, 0xf0f0f0f, v44
	v_dot4c_i32_i8_e32 v46, v44, v33
	v_and_b32_e32 v44, 0xf0f0f0f, v69
	v_mov_b32_e32 v47, 0
	v_dot4c_i32_i8_e32 v47, v44, v34
	v_lshrrev_b32_e32 v44, 4, v69
	v_and_b32_e32 v44, 0xf0f0f0f, v44
	v_dot4c_i32_i8_e32 v47, v44, v35
	v_and_b32_e32 v44, 0xf0f0f0f, v70
	v_dot4c_i32_i8_e32 v46, v44, v28
	v_lshrrev_b32_e32 v44, 4, v70
	v_and_b32_e32 v44, 0xf0f0f0f, v44
	v_dot4c_i32_i8_e32 v46, v44, v29
	v_and_b32_e32 v44, 0xf0f0f0f, v71
	v_dot4c_i32_i8_e32 v47, v44, v30
	v_lshrrev_b32_e32 v44, 4, v71
	v_and_b32_e32 v44, 0xf0f0f0f, v44
	v_dot4c_i32_i8_e32 v47, v44, v31
	v_and_b32_e32 v44, 0xf0f0f0f, v64
	v_dot4c_i32_i8_e32 v56, v44, v32
	v_lshrrev_b32_e32 v44, 4, v64
	v_and_b32_e32 v44, 0xf0f0f0f, v44
	v_dot4c_i32_i8_e32 v56, v44, v33
	v_and_b32_e32 v44, 0xf0f0f0f, v65
	v_dot4c_i32_i8_e32 v57, v44, v34
	v_lshrrev_b32_e32 v44, 4, v65
	v_and_b32_e32 v44, 0xf0f0f0f, v44
	v_dot4c_i32_i8_e32 v57, v44, v35
	v_and_b32_e32 v44, 0xf0f0f0f, v66
	v_dot4c_i32_i8_e32 v56, v44, v28
	v_lshrrev_b32_e32 v44, 4, v66
	v_and_b32_e32 v44, 0xf0f0f0f, v44
	v_dot4c_i32_i8_e32 v56, v44, v29
	v_and_b32_e32 v44, 0xf0f0f0f, v67
	v_dot4c_i32_i8_e32 v57, v44, v30
	v_lshrrev_b32_e32 v44, 4, v67
	v_and_b32_e32 v44, 0xf0f0f0f, v44
	v_dot4c_i32_i8_e32 v57, v44, v31
	v_sub_u32_e32 v47, v47, v169
	v_add_u32_e32 v46, v47, v46
	v_cvt_f32_i32_e32 v47, v46
	v_sub_u32_e32 v57, v57, v169
	v_add_u32_e32 v56, v57, v56
	v_cvt_f32_i32_e32 v46, v56
	s_waitcnt vmcnt(20)
; #define P12_ISSUE(c_, i_, h_, CW_, SC_) do { _Pragma("unroll") for (int bb = 0; bb < 8; ++bb) { const unsigned ro = (unsigned)(c_) * 16384u + (unsigned)EL[(i_) * 128 + ((h_) * 8 + bb) * 8 + g8]; \
;         CW_[bb] = *(const v4u*)(U4 + (size_t)(ro * 128u + 16u * (unsigned)k8)); SC_[bb] = USS[(size_t)(ro * 8u + (unsigned)k8)]; } } while (0)
; #define P12_COMP(i_, h_, CW_, SC_) do { _Pragma("unroll") for (int bb = 0; bb < 8; ++bb) { int a0 = 0, a1 = 0; P12_U4(CW_[bb].x, xa.x, xa.y, a0); P12_U4(CW_[bb].y, xa.z, xa.w, a1); P12_U4(CW_[bb].z, xb.x, xb.y, a0); P12_U4(CW_[bb].w, xb.z, xb.w, a1); \
;         psum[(i_)][(h_) * 8 + bb] += __uint_as_float(SC_[bb] << 16) * (float)((a0 + a1) - xo); } } while (0)
; #define P12_BAR() asm volatile("" ::: "memory")
; __device__ __forceinline__ void p12_peer(Frame& F) {
;     ...
;     { v4u cwA[8], cwB[8]; unsigned scA[8], scB[8]; v4u xa, xb; int xo;
;       P12_ISSUE(0, 0, 0, cwA, scA);
; _Pragma("nounroll")
;       for (int c = 0; c < 16; ++c) { const int cn = c + 1 < 16 ? c + 1 : 15;
;           P12_XQ(c, 0); P12_ISSUE(c, 0, 1, cwB, scB); P12_BAR(); P12_COMP(0, 0, cwA, scA); P12_ISSUE(c, 1, 0, cwA, scA); P12_BAR(); P12_COMP(0, 1, cwB, scB);
;           P12_XQ(c, 1); P12_ISSUE(c, 1, 1, cwB, scB); P12_BAR(); P12_COMP(1, 0, cwA, scA); P12_ISSUE(c, 2, 0, cwA, scA); P12_BAR(); P12_COMP(1, 1, cwB, scB);
;           P12_XQ(c, 2); P12_ISSUE(c, 2, 1, cwB, scB); P12_BAR(); P12_COMP(2, 0, cwA, scA); P12_ISSUE(c, 3, 0, cwA, scA); P12_BAR(); P12_COMP(2, 1, cwB, scB);
;           P12_XQ(c, 3); P12_ISSUE(c, 3, 1, cwB, scB); P12_BAR(); P12_COMP(3, 0, cwA, scA); P12_ISSUE(cn, 0, 0, cwA, scA); P12_BAR(); P12_COMP(3, 1, cwB, scB);
	v_lshlrev_b32_e32 v45, 16, v226
	v_lshlrev_b32_e32 v44, 16, v227
	v_pk_fma_f32 v[116:117], v[44:45], v[46:47], v[116:117]
	v_and_b32_e32 v44, 0xf0f0f0f, v52
	v_mov_b32_e32 v46, 0
	v_dot4c_i32_i8_e32 v46, v44, v32
	v_lshrrev_b32_e32 v44, 4, v52
	v_and_b32_e32 v44, 0xf0f0f0f, v44
	v_dot4c_i32_i8_e32 v46, v44, v33
	v_and_b32_e32 v44, 0xf0f0f0f, v53
	v_mov_b32_e32 v47, 0
	v_dot4c_i32_i8_e32 v47, v44, v34
	v_lshrrev_b32_e32 v44, 4, v53
	v_and_b32_e32 v44, 0xf0f0f0f, v44
	v_dot4c_i32_i8_e32 v47, v44, v35
	v_and_b32_e32 v44, 0xf0f0f0f, v54
	v_dot4c_i32_i8_e32 v46, v44, v28
	v_lshrrev_b32_e32 v44, 4, v54
	v_and_b32_e32 v44, 0xf0f0f0f, v44
	v_dot4c_i32_i8_e32 v46, v44, v29
	v_and_b32_e32 v44, 0xf0f0f0f, v55
	v_dot4c_i32_i8_e32 v47, v44, v30
	v_lshrrev_b32_e32 v44, 4, v55
	v_and_b32_e32 v44, 0xf0f0f0f, v44
	v_dot4c_i32_i8_e32 v47, v44, v31
	v_and_b32_e32 v44, 0xf0f0f0f, v48
	v_mov_b32_e32 v52, 0
	v_dot4c_i32_i8_e32 v52, v44, v32
	v_lshrrev_b32_e32 v44, 4, v48
	v_and_b32_e32 v44, 0xf0f0f0f, v44
	v_dot4c_i32_i8_e32 v52, v44, v33
	v_and_b32_e32 v44, 0xf0f0f0f, v49
	v_mov_b32_e32 v48, 0
	v_dot4c_i32_i8_e32 v48, v44, v34
	v_lshrrev_b32_e32 v44, 4, v49
	v_and_b32_e32 v44, 0xf0f0f0f, v44
	v_dot4c_i32_i8_e32 v48, v44, v35
	v_and_b32_e32 v44, 0xf0f0f0f, v50
	v_dot4c_i32_i8_e32 v52, v44, v28
	v_lshrrev_b32_e32 v44, 4, v50
	v_and_b32_e32 v44, 0xf0f0f0f, v44
	v_dot4c_i32_i8_e32 v52, v44, v29
	v_and_b32_e32 v44, 0xf0f0f0f, v51
	v_dot4c_i32_i8_e32 v48, v44, v30
	v_lshrrev_b32_e32 v44, 4, v51
	v_and_b32_e32 v44, 0xf0f0f0f, v44
	v_dot4c_i32_i8_e32 v48, v44, v31
	v_sub_u32_e32 v47, v47, v169
	v_add_u32_e32 v46, v47, v46
	v_cvt_f32_i32_e32 v47, v46
	v_sub_u32_e32 v48, v48, v169
	v_add_u32_e32 v48, v48, v52
	v_cvt_f32_i32_e32 v46, v48
	s_waitcnt vmcnt(18)
	v_lshlrev_b32_e32 v45, 16, v228
	v_lshlrev_b32_e32 v44, 16, v229
	v_pk_fma_f32 v[114:115], v[44:45], v[46:47], v[114:115]
	v_and_b32_e32 v44, 0xf0f0f0f, v40
	v_mov_b32_e32 v45, 0
	v_lshrrev_b32_e32 v40, 4, v40
	v_dot4c_i32_i8_e32 v45, v44, v32
	v_and_b32_e32 v40, 0xf0f0f0f, v40
	v_dot4c_i32_i8_e32 v45, v40, v33
	v_and_b32_e32 v40, 0xf0f0f0f, v41
	v_mov_b32_e32 v44, 0
	v_dot4c_i32_i8_e32 v44, v40, v34
	v_lshrrev_b32_e32 v40, 4, v41
	v_and_b32_e32 v40, 0xf0f0f0f, v40
	v_dot4c_i32_i8_e32 v44, v40, v35
	v_and_b32_e32 v40, 0xf0f0f0f, v42
	v_dot4c_i32_i8_e32 v45, v40, v28
	v_lshrrev_b32_e32 v40, 4, v42
	v_and_b32_e32 v40, 0xf0f0f0f, v40
	v_dot4c_i32_i8_e32 v45, v40, v29
	v_and_b32_e32 v40, 0xf0f0f0f, v43
	v_dot4c_i32_i8_e32 v44, v40, v30
	v_lshrrev_b32_e32 v40, 4, v43
	v_and_b32_e32 v40, 0xf0f0f0f, v40
	v_dot4c_i32_i8_e32 v44, v40, v31
	v_and_b32_e32 v40, 0xf0f0f0f, v36
	v_mov_b32_e32 v41, 0
	v_dot4c_i32_i8_e32 v41, v40, v32
	v_lshrrev_b32_e32 v32, 4, v36
	v_and_b32_e32 v32, 0xf0f0f0f, v32
	v_dot4c_i32_i8_e32 v41, v32, v33
	v_and_b32_e32 v32, 0xf0f0f0f, v37
	v_mov_b32_e32 v33, 0
	v_dot4c_i32_i8_e32 v33, v32, v34
	v_lshrrev_b32_e32 v32, 4, v37
	v_and_b32_e32 v32, 0xf0f0f0f, v32
	v_dot4c_i32_i8_e32 v33, v32, v35
	v_and_b32_e32 v32, 0xf0f0f0f, v38
	v_dot4c_i32_i8_e32 v41, v32, v28
	v_lshrrev_b32_e32 v28, 4, v38
	v_and_b32_e32 v28, 0xf0f0f0f, v28
	v_dot4c_i32_i8_e32 v41, v28, v29
	v_and_b32_e32 v28, 0xf0f0f0f, v39
	v_dot4c_i32_i8_e32 v33, v28, v30
	v_lshrrev_b32_e32 v28, 4, v39
	v_and_b32_e32 v28, 0xf0f0f0f, v28
	v_dot4c_i32_i8_e32 v33, v28, v31
	v_sub_u32_e32 v30, v44, v169
	v_add_u32_e32 v30, v30, v45
	s_waitcnt vmcnt(16)
	v_lshlrev_b32_e32 v29, 16, v230
	v_sub_u32_e32 v31, v33, v169
	v_add_u32_e32 v32, v31, v41
	v_cvt_f32_i32_e32 v31, v30
	v_cvt_f32_i32_e32 v30, v32
	v_lshlrev_b32_e32 v28, 16, v231
	ds_read_b128 v[36:39], v166 offset:12288
	ds_read_b128 v[32:35], v166 offset:12304
	v_add_u32_e32 v166, 0x100, v166
	v_pk_fma_f32 v[112:113], v[28:29], v[30:31], v[112:113]
	ds_read_u16 v29, v93 offset:17280
	ds_read_u16 v30, v93 offset:17296
	ds_read_u16 v31, v93 offset:17312
	ds_read_u16 v40, v93 offset:17328
	v_mov_b32_e32 v28, 0
	s_waitcnt lgkmcnt(3)
	v_add_u32_e32 v29, s44, v29
	v_lshl_or_b32 v41, v29, 7, v165
	s_waitcnt lgkmcnt(2)
	v_add_u32_e32 v30, s44, v30
	global_load_dwordx4 v[68:71], v41, s[0:1]
	v_lshl_or_b32 v41, v30, 7, v165
	s_waitcnt lgkmcnt(1)
	v_add_u32_e32 v31, s44, v31
	global_load_dwordx4 v[64:67], v41, s[0:1]
	v_lshl_or_b32 v41, v31, 7, v165
	s_waitcnt lgkmcnt(0)
	v_add_u32_e32 v40, s44, v40
	global_load_dwordx4 v[60:63], v41, s[0:1]
	v_lshl_or_b32 v41, v40, 7, v165
	v_lshl_or_b32 v79, v40, 5, v248
	ds_read_u16 v40, v93 offset:17344
	global_load_dwordx4 v[56:59], v41, s[0:1]
	v_dot4c_i32_i8_e32 v28, 0x1010101, v36
	v_dot4c_i32_i8_e32 v28, 0x1010101, v37
	v_dot4c_i32_i8_e32 v28, 0x1010101, v38
	s_waitcnt lgkmcnt(0)
	v_add_u32_e32 v40, s44, v40
	v_lshl_or_b32 v41, v40, 7, v165
	v_lshl_or_b32 v80, v40, 5, v248
	ds_read_u16 v40, v93 offset:17360
	global_load_dwordx4 v[52:55], v41, s[0:1]
	v_dot4c_i32_i8_e32 v28, 0x1010101, v39
	v_dot4c_i32_i8_e32 v28, 0x1010101, v32
	v_dot4c_i32_i8_e32 v28, 0x1010101, v33
	s_waitcnt lgkmcnt(0)
	v_add_u32_e32 v40, s44, v40
	v_lshl_or_b32 v41, v40, 7, v165
	v_lshl_or_b32 v82, v40, 5, v248
	ds_read_u16 v40, v93 offset:17376
	global_load_dwordx4 v[48:51], v41, s[0:1]
	v_dot4c_i32_i8_e32 v28, 0x1010101, v34
	v_dot4c_i32_i8_e32 v28, 0x1010101, v35
	v_lshl_or_b32 v29, v29, 5, v248
	s_waitcnt lgkmcnt(0)
	v_add_u32_e32 v40, s44, v40
	v_lshl_or_b32 v41, v40, 7, v165
	v_lshl_or_b32 v87, v40, 5, v248
	ds_read_u16 v40, v93 offset:17392
	v_lshl_or_b32 v30, v30, 5, v248
	v_lshl_or_b32 v31, v31, 5, v248
	global_load_dwordx4 v[44:47], v41, s[0:1]
	s_waitcnt lgkmcnt(0)
; #define P12_ISSUE(c_, i_, h_, CW_, SC_) do { _Pragma("unroll") for (int bb = 0; bb < 8; ++bb) { const unsigned ro = (unsigned)(c_) * 16384u + (unsigned)EL[(i_) * 128 + ((h_) * 8 + bb) * 8 + g8]; \
;         CW_[bb] = *(const v4u*)(U4 + (size_t)(ro * 128u + 16u * (unsigned)k8)); SC_[bb] = USS[(size_t)(ro * 8u + (unsigned)k8)]; } } while (0)
; #define P12_COMP(i_, h_, CW_, SC_) do { _Pragma("unroll") for (int bb = 0; bb < 8; ++bb) { int a0 = 0, a1 = 0; P12_U4(CW_[bb].x, xa.x, xa.y, a0); P12_U4(CW_[bb].y, xa.z, xa.w, a1); P12_U4(CW_[bb].z, xb.x, xb.y, a0); P12_U4(CW_[bb].w, xb.z, xb.w, a1); \
;         psum[(i_)][(h_) * 8 + bb] += __uint_as_float(SC_[bb] << 16) * (float)((a0 + a1) - xo); } } while (0)
; #define P12_BAR() asm volatile("" ::: "memory")
; __device__ __forceinline__ void p12_peer(Frame& F) {
;     ...
;     { v4u cwA[8], cwB[8]; unsigned scA[8], scB[8]; v4u xa, xb; int xo;
;       P12_ISSUE(0, 0, 0, cwA, scA);
; _Pragma("nounroll")
;       for (int c = 0; c < 16; ++c) { const int cn = c + 1 < 16 ? c + 1 : 15;
;           P12_XQ(c, 0); P12_ISSUE(c, 0, 1, cwB, scB); P12_BAR(); P12_COMP(0, 0, cwA, scA); P12_ISSUE(c, 1, 0, cwA, scA); P12_BAR(); P12_COMP(0, 1, cwB, scB);
;           P12_XQ(c, 1); P12_ISSUE(c, 1, 1, cwB, scB); P12_BAR(); P12_COMP(1, 0, cwA, scA); P12_ISSUE(c, 2, 0, cwA, scA); P12_BAR(); P12_COMP(1, 1, cwB, scB);
;           P12_XQ(c, 2); P12_ISSUE(c, 2, 1, cwB, scB); P12_BAR(); P12_COMP(2, 0, cwA, scA); P12_ISSUE(c, 3, 0, cwA, scA); P12_BAR(); P12_COMP(2, 1, cwB, scB);
;           P12_XQ(c, 3); P12_ISSUE(c, 3, 1, cwB, scB); P12_BAR(); P12_COMP(3, 0, cwA, scA); P12_ISSUE(cn, 0, 0, cwA, scA); P12_BAR(); P12_COMP(3, 1, cwB, scB);
	v_add_u32_e32 v78, s44, v40
	v_lshl_or_b32 v40, v78, 7, v165
	global_load_dwordx4 v[40:43], v40, s[0:1]
	v_lshl_or_b32 v169, v78, 5, v248
	v_lshlrev_b32_e32 v78, 3, v28
	global_load_dword v240, v29, s[46:47]
	global_load_dword v241, v30, s[46:47]
	global_load_dword v242, v31, s[46:47]
	global_load_dword v243, v79, s[46:47]
	global_load_dword v244, v80, s[46:47]
	s_nop 0
	global_load_dword v245, v82, s[46:47]
	s_nop 0
	global_load_dword v246, v87, s[46:47]
	global_load_dword v247, v169, s[46:47]
	s_waitcnt vmcnt(31)
	v_and_b32_e32 v29, 0xf0f0f0f, v72
	v_mov_b32_e32 v28, 0
	v_dot4c_i32_i8_e32 v28, v29, v36
	v_lshrrev_b32_e32 v29, 4, v72
	v_and_b32_e32 v29, 0xf0f0f0f, v29
	v_dot4c_i32_i8_e32 v28, v29, v37
	v_and_b32_e32 v30, 0xf0f0f0f, v73
	v_mov_b32_e32 v29, 0
	v_dot4c_i32_i8_e32 v29, v30, v38
	v_lshrrev_b32_e32 v30, 4, v73
	v_and_b32_e32 v30, 0xf0f0f0f, v30
	v_dot4c_i32_i8_e32 v29, v30, v39
	v_and_b32_e32 v30, 0xf0f0f0f, v74
	v_dot4c_i32_i8_e32 v28, v30, v32
	v_lshrrev_b32_e32 v30, 4, v74
	v_and_b32_e32 v30, 0xf0f0f0f, v30
	v_dot4c_i32_i8_e32 v28, v30, v33
	v_and_b32_e32 v30, 0xf0f0f0f, v75
	v_dot4c_i32_i8_e32 v29, v30, v34
	v_lshrrev_b32_e32 v30, 4, v75
	v_and_b32_e32 v30, 0xf0f0f0f, v30
	v_dot4c_i32_i8_e32 v29, v30, v35
	s_waitcnt vmcnt(30)
	v_and_b32_e32 v31, 0xf0f0f0f, v24
	v_mov_b32_e32 v30, 0
	v_lshrrev_b32_e32 v24, 4, v24
	v_dot4c_i32_i8_e32 v30, v31, v36
	v_and_b32_e32 v24, 0xf0f0f0f, v24
	v_dot4c_i32_i8_e32 v30, v24, v37
	v_and_b32_e32 v24, 0xf0f0f0f, v25
	v_mov_b32_e32 v31, 0
	v_dot4c_i32_i8_e32 v31, v24, v38
	v_lshrrev_b32_e32 v24, 4, v25
	v_and_b32_e32 v24, 0xf0f0f0f, v24
	v_dot4c_i32_i8_e32 v31, v24, v39
	v_and_b32_e32 v24, 0xf0f0f0f, v26
	v_dot4c_i32_i8_e32 v30, v24, v32
	v_lshrrev_b32_e32 v24, 4, v26
	v_and_b32_e32 v24, 0xf0f0f0f, v24
	v_dot4c_i32_i8_e32 v30, v24, v33
	v_and_b32_e32 v24, 0xf0f0f0f, v27
	v_dot4c_i32_i8_e32 v31, v24, v34
	v_lshrrev_b32_e32 v24, 4, v27
	v_and_b32_e32 v24, 0xf0f0f0f, v24
	v_dot4c_i32_i8_e32 v31, v24, v35
	v_add_u32_e32 v26, v28, v29
	v_sub_u32_e32 v26, v26, v78
	s_waitcnt vmcnt(22)
	v_lshlrev_b32_e32 v25, 16, v232
	v_add_u32_e32 v27, v30, v31
	v_sub_u32_e32 v28, v27, v78
	v_cvt_f32_i32_e32 v27, v26
	v_cvt_f32_i32_e32 v26, v28
	v_lshlrev_b32_e32 v24, 16, v233
	s_cselect_b32 s44, s44, s45
	v_pk_fma_f32 v[110:111], v[24:25], v[26:27], v[110:111]
	v_and_b32_e32 v24, 0xf0f0f0f, v20
	v_mov_b32_e32 v25, 0
	v_lshrrev_b32_e32 v20, 4, v20
	v_dot4c_i32_i8_e32 v25, v24, v36
	v_and_b32_e32 v20, 0xf0f0f0f, v20
	v_dot4c_i32_i8_e32 v25, v20, v37
	v_and_b32_e32 v20, 0xf0f0f0f, v21
	v_mov_b32_e32 v24, 0
	v_dot4c_i32_i8_e32 v24, v20, v38
	v_lshrrev_b32_e32 v20, 4, v21
	v_and_b32_e32 v20, 0xf0f0f0f, v20
	v_dot4c_i32_i8_e32 v24, v20, v39
	v_and_b32_e32 v20, 0xf0f0f0f, v22
	v_dot4c_i32_i8_e32 v25, v20, v32
	v_lshrrev_b32_e32 v20, 4, v22
	v_and_b32_e32 v20, 0xf0f0f0f, v20
	v_dot4c_i32_i8_e32 v25, v20, v33
	v_and_b32_e32 v20, 0xf0f0f0f, v23
	v_dot4c_i32_i8_e32 v24, v20, v34
	v_lshrrev_b32_e32 v20, 4, v23
	v_and_b32_e32 v20, 0xf0f0f0f, v20
	v_dot4c_i32_i8_e32 v24, v20, v35
	v_and_b32_e32 v20, 0xf0f0f0f, v16
	v_mov_b32_e32 v21, 0
	v_lshrrev_b32_e32 v16, 4, v16
	v_dot4c_i32_i8_e32 v21, v20, v36
	v_and_b32_e32 v16, 0xf0f0f0f, v16
	v_dot4c_i32_i8_e32 v21, v16, v37
	v_and_b32_e32 v16, 0xf0f0f0f, v17
	v_mov_b32_e32 v20, 0
	v_dot4c_i32_i8_e32 v20, v16, v38
	v_lshrrev_b32_e32 v16, 4, v17
	v_and_b32_e32 v16, 0xf0f0f0f, v16
	v_dot4c_i32_i8_e32 v20, v16, v39
	v_and_b32_e32 v16, 0xf0f0f0f, v18
	v_dot4c_i32_i8_e32 v21, v16, v32
	v_lshrrev_b32_e32 v16, 4, v18
	v_and_b32_e32 v16, 0xf0f0f0f, v16
	v_dot4c_i32_i8_e32 v21, v16, v33
	v_and_b32_e32 v16, 0xf0f0f0f, v19
	v_dot4c_i32_i8_e32 v20, v16, v34
	v_lshrrev_b32_e32 v16, 4, v19
	v_and_b32_e32 v16, 0xf0f0f0f, v16
	v_dot4c_i32_i8_e32 v20, v16, v35
	v_add_u32_e32 v18, v25, v24
	v_sub_u32_e32 v18, v18, v78
	s_waitcnt vmcnt(20)
	v_lshlrev_b32_e32 v17, 16, v234
	v_add_u32_e32 v19, v21, v20
	v_sub_u32_e32 v20, v19, v78
	v_cvt_f32_i32_e32 v19, v18
	v_cvt_f32_i32_e32 v18, v20
	v_lshlrev_b32_e32 v16, 16, v235
	v_mov_b32_e32 v90, 0
	s_cmp_eq_u32 s45, 0x40000
	v_pk_fma_f32 v[108:109], v[16:17], v[18:19], v[108:109]
	v_and_b32_e32 v16, 0xf0f0f0f, v12
	v_mov_b32_e32 v17, 0
	v_lshrrev_b32_e32 v12, 4, v12
	v_dot4c_i32_i8_e32 v17, v16, v36
	v_and_b32_e32 v12, 0xf0f0f0f, v12
	v_dot4c_i32_i8_e32 v17, v12, v37
	v_and_b32_e32 v12, 0xf0f0f0f, v13
	v_mov_b32_e32 v16, 0
	v_dot4c_i32_i8_e32 v16, v12, v38
	v_lshrrev_b32_e32 v12, 4, v13
	v_and_b32_e32 v12, 0xf0f0f0f, v12
	v_dot4c_i32_i8_e32 v16, v12, v39
	v_and_b32_e32 v12, 0xf0f0f0f, v14
	v_dot4c_i32_i8_e32 v17, v12, v32
	v_lshrrev_b32_e32 v12, 4, v14
	v_and_b32_e32 v12, 0xf0f0f0f, v12
	v_dot4c_i32_i8_e32 v17, v12, v33
	v_and_b32_e32 v12, 0xf0f0f0f, v15
	v_dot4c_i32_i8_e32 v16, v12, v34
	v_lshrrev_b32_e32 v12, 4, v15
	v_and_b32_e32 v12, 0xf0f0f0f, v12
	v_dot4c_i32_i8_e32 v16, v12, v35
	v_and_b32_e32 v12, 0xf0f0f0f, v8
	v_mov_b32_e32 v13, 0
	v_lshrrev_b32_e32 v8, 4, v8
	v_dot4c_i32_i8_e32 v13, v12, v36
	v_and_b32_e32 v8, 0xf0f0f0f, v8
	v_dot4c_i32_i8_e32 v13, v8, v37
	v_and_b32_e32 v8, 0xf0f0f0f, v9
	v_mov_b32_e32 v12, 0
	v_dot4c_i32_i8_e32 v12, v8, v38
	v_lshrrev_b32_e32 v8, 4, v9
	v_and_b32_e32 v8, 0xf0f0f0f, v8
	v_dot4c_i32_i8_e32 v12, v8, v39
	v_and_b32_e32 v8, 0xf0f0f0f, v10
	v_dot4c_i32_i8_e32 v13, v8, v32
	v_lshrrev_b32_e32 v8, 4, v10
	v_and_b32_e32 v8, 0xf0f0f0f, v8
	v_dot4c_i32_i8_e32 v13, v8, v33
	v_and_b32_e32 v8, 0xf0f0f0f, v11
	v_dot4c_i32_i8_e32 v12, v8, v34
	v_lshrrev_b32_e32 v8, 4, v11
	v_and_b32_e32 v8, 0xf0f0f0f, v8
	v_dot4c_i32_i8_e32 v12, v8, v35
	v_add_u32_e32 v11, v17, v16
	s_waitcnt vmcnt(18)
; #define P12_ISSUE(c_, i_, h_, CW_, SC_) do { _Pragma("unroll") for (int bb = 0; bb < 8; ++bb) { const unsigned ro = (unsigned)(c_) * 16384u + (unsigned)EL[(i_) * 128 + ((h_) * 8 + bb) * 8 + g8]; \
;         CW_[bb] = *(const v4u*)(U4 + (size_t)(ro * 128u + 16u * (unsigned)k8)); SC_[bb] = USS[(size_t)(ro * 8u + (unsigned)k8)]; } } while (0)
; #define P12_COMP(i_, h_, CW_, SC_) do { _Pragma("unroll") for (int bb = 0; bb < 8; ++bb) { int a0 = 0, a1 = 0; P12_U4(CW_[bb].x, xa.x, xa.y, a0); P12_U4(CW_[bb].y, xa.z, xa.w, a1); P12_U4(CW_[bb].z, xb.x, xb.y, a0); P12_U4(CW_[bb].w, xb.z, xb.w, a1); \
;         psum[(i_)][(h_) * 8 + bb] += __uint_as_float(SC_[bb] << 16) * (float)((a0 + a1) - xo); } } while (0)
; #define P12_BAR() asm volatile("" ::: "memory")
; __device__ __forceinline__ void p12_peer(Frame& F) {
;     ...
;     { v4u cwA[8], cwB[8]; unsigned scA[8], scB[8]; v4u xa, xb; int xo;
;       P12_ISSUE(0, 0, 0, cwA, scA);
; _Pragma("nounroll")
;       for (int c = 0; c < 16; ++c) { const int cn = c + 1 < 16 ? c + 1 : 15;
;           P12_XQ(c, 0); P12_ISSUE(c, 0, 1, cwB, scB); P12_BAR(); P12_COMP(0, 0, cwA, scA); P12_ISSUE(c, 1, 0, cwA, scA); P12_BAR(); P12_COMP(0, 1, cwB, scB);
;           P12_XQ(c, 1); P12_ISSUE(c, 1, 1, cwB, scB); P12_BAR(); P12_COMP(1, 0, cwA, scA); P12_ISSUE(c, 2, 0, cwA, scA); P12_BAR(); P12_COMP(1, 1, cwB, scB);
;           P12_XQ(c, 2); P12_ISSUE(c, 2, 1, cwB, scB); P12_BAR(); P12_COMP(2, 0, cwA, scA); P12_ISSUE(c, 3, 0, cwA, scA); P12_BAR(); P12_COMP(2, 1, cwB, scB);
;           P12_XQ(c, 3); P12_ISSUE(c, 3, 1, cwB, scB); P12_BAR(); P12_COMP(3, 0, cwA, scA); P12_ISSUE(cn, 0, 0, cwA, scA); P12_BAR(); P12_COMP(3, 1, cwB, scB);
	v_lshlrev_b32_e32 v9, 16, v237
	v_lshlrev_b32_e32 v8, 16, v236
	v_add_u32_e32 v10, v13, v12
	v_sub_u32_e32 v12, v11, v78
	v_sub_u32_e32 v10, v10, v78
	v_cvt_f32_i32_e32 v11, v10
	v_cvt_f32_i32_e32 v10, v12
	s_waitcnt vmcnt(15)
	v_and_b32_e32 v89, 0xf0f0f0f, v68
	v_lshrrev_b32_e32 v68, 4, v68
	v_dot4c_i32_i8_e32 v90, v89, v36
	v_pk_fma_f32 v[106:107], v[8:9], v[10:11], v[106:107]
	v_and_b32_e32 v8, 0xf0f0f0f, v4
	v_mov_b32_e32 v9, 0
	v_lshrrev_b32_e32 v4, 4, v4
	v_dot4c_i32_i8_e32 v9, v8, v36
	v_and_b32_e32 v4, 0xf0f0f0f, v4
	v_dot4c_i32_i8_e32 v9, v4, v37
	v_and_b32_e32 v4, 0xf0f0f0f, v5
	v_mov_b32_e32 v8, 0
	v_dot4c_i32_i8_e32 v8, v4, v38
	v_lshrrev_b32_e32 v4, 4, v5
	v_and_b32_e32 v4, 0xf0f0f0f, v4
	v_dot4c_i32_i8_e32 v8, v4, v39
	v_and_b32_e32 v4, 0xf0f0f0f, v6
	v_dot4c_i32_i8_e32 v9, v4, v32
	v_lshrrev_b32_e32 v4, 4, v6
	v_and_b32_e32 v4, 0xf0f0f0f, v4
	v_dot4c_i32_i8_e32 v9, v4, v33
	v_and_b32_e32 v4, 0xf0f0f0f, v7
	v_dot4c_i32_i8_e32 v8, v4, v34
	v_lshrrev_b32_e32 v4, 4, v7
	v_and_b32_e32 v4, 0xf0f0f0f, v4
	v_dot4c_i32_i8_e32 v8, v4, v35
	v_and_b32_e32 v4, 0xf0f0f0f, v0
	v_mov_b32_e32 v5, 0
	v_lshrrev_b32_e32 v0, 4, v0
	v_dot4c_i32_i8_e32 v5, v4, v36
	v_and_b32_e32 v0, 0xf0f0f0f, v0
	v_dot4c_i32_i8_e32 v5, v0, v37
	v_and_b32_e32 v0, 0xf0f0f0f, v1
	v_mov_b32_e32 v4, 0
	v_dot4c_i32_i8_e32 v4, v0, v38
	v_lshrrev_b32_e32 v0, 4, v1
	v_and_b32_e32 v0, 0xf0f0f0f, v0
	v_dot4c_i32_i8_e32 v4, v0, v39
	v_and_b32_e32 v0, 0xf0f0f0f, v2
	v_dot4c_i32_i8_e32 v5, v0, v32
	v_lshrrev_b32_e32 v0, 4, v2
	v_and_b32_e32 v0, 0xf0f0f0f, v0
	v_dot4c_i32_i8_e32 v5, v0, v33
	v_and_b32_e32 v0, 0xf0f0f0f, v3
	v_dot4c_i32_i8_e32 v4, v0, v34
	v_lshrrev_b32_e32 v0, 4, v3
	v_and_b32_e32 v0, 0xf0f0f0f, v0
	v_dot4c_i32_i8_e32 v4, v0, v35
	v_add_u32_e32 v3, v9, v8
	v_lshlrev_b32_e32 v1, 16, v239
	v_lshlrev_b32_e32 v0, 16, v238
	v_add_u32_e32 v2, v5, v4
	v_sub_u32_e32 v4, v3, v78
	v_sub_u32_e32 v2, v2, v78
	v_cvt_f32_i32_e32 v3, v2
	v_cvt_f32_i32_e32 v2, v4
	v_and_b32_e32 v68, 0xf0f0f0f, v68
	v_dot4c_i32_i8_e32 v90, v68, v37
	v_and_b32_e32 v68, 0xf0f0f0f, v69
	v_pk_fma_f32 v[104:105], v[0:1], v[2:3], v[104:105]
	ds_read_u16 v0, v93 offset:16384
	ds_read_u16 v1, v93 offset:16400
	ds_read_u16 v2, v93 offset:16416
	ds_read_u16 v3, v93 offset:16432
	v_mov_b32_e32 v89, 0
	s_waitcnt lgkmcnt(3)
	v_add_u32_e32 v0, s44, v0
	v_lshl_or_b32 v4, v0, 7, v165
	v_lshl_or_b32 v0, v0, 4, v95
	global_load_dwordx4 v[28:31], v4, s[0:1]
	s_waitcnt lgkmcnt(2)
	v_add_u32_e32 v0, s44, v1
	v_dot4c_i32_i8_e32 v89, v68, v38
	v_lshrrev_b32_e32 v68, 4, v69
	v_lshl_or_b32 v1, v0, 7, v165
	v_lshl_or_b32 v0, v0, 4, v95
	v_and_b32_e32 v68, 0xf0f0f0f, v68
	global_load_dwordx4 v[24:27], v1, s[0:1]
	s_waitcnt lgkmcnt(1)
	v_add_u32_e32 v0, s44, v2
	v_dot4c_i32_i8_e32 v89, v68, v39
	v_and_b32_e32 v68, 0xf0f0f0f, v70
	v_lshl_or_b32 v1, v0, 7, v165
	v_lshl_or_b32 v0, v0, 4, v95
	v_dot4c_i32_i8_e32 v90, v68, v32
	v_lshrrev_b32_e32 v68, 4, v70
	global_load_dwordx4 v[20:23], v1, s[0:1]
	s_waitcnt lgkmcnt(0)
	v_add_u32_e32 v0, s44, v3
	v_and_b32_e32 v68, 0xf0f0f0f, v68
	v_lshl_or_b32 v1, v0, 7, v165
	v_lshl_or_b32 v0, v0, 4, v95
	v_dot4c_i32_i8_e32 v90, v68, v33
	v_and_b32_e32 v68, 0xf0f0f0f, v71
	global_load_dwordx4 v[16:19], v1, s[0:1]
	ds_read_u16 v0, v93 offset:16448
	v_dot4c_i32_i8_e32 v89, v68, v34
	v_lshrrev_b32_e32 v68, 4, v71
	v_and_b32_e32 v68, 0xf0f0f0f, v68
	v_dot4c_i32_i8_e32 v89, v68, v35
	s_waitcnt vmcnt(18)
	v_and_b32_e32 v68, 0xf0f0f0f, v64
	v_mov_b32_e32 v69, 0
	v_lshrrev_b32_e32 v64, 4, v64
	v_dot4c_i32_i8_e32 v69, v68, v36
	v_and_b32_e32 v64, 0xf0f0f0f, v64
	v_dot4c_i32_i8_e32 v69, v64, v37
	v_and_b32_e32 v64, 0xf0f0f0f, v65
	v_mov_b32_e32 v68, 0
	s_waitcnt lgkmcnt(0)
	v_add_u32_e32 v0, s44, v0
	v_dot4c_i32_i8_e32 v68, v64, v38
	v_lshrrev_b32_e32 v64, 4, v65
	v_lshl_or_b32 v1, v0, 7, v165
	v_lshl_or_b32 v0, v0, 4, v95
	v_and_b32_e32 v64, 0xf0f0f0f, v64
	global_load_dwordx4 v[12:15], v1, s[0:1]
	ds_read_u16 v0, v93 offset:16464
	v_dot4c_i32_i8_e32 v68, v64, v39
	v_and_b32_e32 v64, 0xf0f0f0f, v66
	v_dot4c_i32_i8_e32 v69, v64, v32
	v_lshrrev_b32_e32 v64, 4, v66
	v_and_b32_e32 v64, 0xf0f0f0f, v64
	v_dot4c_i32_i8_e32 v69, v64, v33
	v_and_b32_e32 v64, 0xf0f0f0f, v67
	v_dot4c_i32_i8_e32 v68, v64, v34
	v_lshrrev_b32_e32 v64, 4, v67
	s_waitcnt lgkmcnt(0)
	v_add_u32_e32 v0, s44, v0
	v_and_b32_e32 v64, 0xf0f0f0f, v64
	v_lshl_or_b32 v1, v0, 7, v165
	v_lshl_or_b32 v0, v0, 4, v95
	v_dot4c_i32_i8_e32 v68, v64, v35
	global_load_dwordx4 v[8:11], v1, s[0:1]
	ds_read_u16 v0, v93 offset:16480
	v_add_u32_e32 v66, v90, v89
	v_sub_u32_e32 v67, v68, v78
	v_add_u32_e32 v67, v67, v69
	v_sub_u32_e32 v66, v66, v78
	v_cvt_f32_i32_e32 v66, v66
	v_cvt_f32_i32_e32 v67, v67
	s_waitcnt lgkmcnt(0)
	v_add_u32_e32 v0, s44, v0
	s_waitcnt vmcnt(12)
	v_lshlrev_b32_e32 v65, 16, v241
	v_lshlrev_b32_e32 v64, 16, v240
	v_lshl_or_b32 v1, v0, 7, v165
	v_lshl_or_b32 v0, v0, 4, v95
	v_pk_fma_f32 v[102:103], v[64:65], v[66:67], v[102:103]
	v_and_b32_e32 v64, 0xf0f0f0f, v60
	v_mov_b32_e32 v65, 0
	v_lshrrev_b32_e32 v60, 4, v60
	global_load_dwordx4 v[4:7], v1, s[0:1]
	ds_read_u16 v0, v93 offset:16496
	v_dot4c_i32_i8_e32 v65, v64, v36
	v_and_b32_e32 v60, 0xf0f0f0f, v60
	v_dot4c_i32_i8_e32 v65, v60, v37
	v_and_b32_e32 v60, 0xf0f0f0f, v61
	v_mov_b32_e32 v64, 0
	v_dot4c_i32_i8_e32 v64, v60, v38
	v_lshrrev_b32_e32 v60, 4, v61
	v_and_b32_e32 v60, 0xf0f0f0f, v60
	v_dot4c_i32_i8_e32 v64, v60, v39
	v_and_b32_e32 v60, 0xf0f0f0f, v62
	s_waitcnt lgkmcnt(0)
; #define P12_ISSUE(c_, i_, h_, CW_, SC_) do { _Pragma("unroll") for (int bb = 0; bb < 8; ++bb) { const unsigned ro = (unsigned)(c_) * 16384u + (unsigned)EL[(i_) * 128 + ((h_) * 8 + bb) * 8 + g8]; \
;         CW_[bb] = *(const v4u*)(U4 + (size_t)(ro * 128u + 16u * (unsigned)k8)); SC_[bb] = USS[(size_t)(ro * 8u + (unsigned)k8)]; } } while (0)
; #define P12_COMP(i_, h_, CW_, SC_) do { _Pragma("unroll") for (int bb = 0; bb < 8; ++bb) { int a0 = 0, a1 = 0; P12_U4(CW_[bb].x, xa.x, xa.y, a0); P12_U4(CW_[bb].y, xa.z, xa.w, a1); P12_U4(CW_[bb].z, xb.x, xb.y, a0); P12_U4(CW_[bb].w, xb.z, xb.w, a1); \
;         psum[(i_)][(h_) * 8 + bb] += __uint_as_float(SC_[bb] << 16) * (float)((a0 + a1) - xo); } } while (0)
; #define P12_BAR() asm volatile("" ::: "memory")
; __device__ __forceinline__ void p12_peer(Frame& F) {
;     ...
;     { v4u cwA[8], cwB[8]; unsigned scA[8], scB[8]; v4u xa, xb; int xo;
;       P12_ISSUE(0, 0, 0, cwA, scA);
; _Pragma("nounroll")
;       for (int c = 0; c < 16; ++c) { const int cn = c + 1 < 16 ? c + 1 : 15;
;           P12_XQ(c, 0); P12_ISSUE(c, 0, 1, cwB, scB); P12_BAR(); P12_COMP(0, 0, cwA, scA); P12_ISSUE(c, 1, 0, cwA, scA); P12_BAR(); P12_COMP(0, 1, cwB, scB);
;           P12_XQ(c, 1); P12_ISSUE(c, 1, 1, cwB, scB); P12_BAR(); P12_COMP(1, 0, cwA, scA); P12_ISSUE(c, 2, 0, cwA, scA); P12_BAR(); P12_COMP(1, 1, cwB, scB);
;           P12_XQ(c, 2); P12_ISSUE(c, 2, 1, cwB, scB); P12_BAR(); P12_COMP(2, 0, cwA, scA); P12_ISSUE(c, 3, 0, cwA, scA); P12_BAR(); P12_COMP(2, 1, cwB, scB);
;           P12_XQ(c, 3); P12_ISSUE(c, 3, 1, cwB, scB); P12_BAR(); P12_COMP(3, 0, cwA, scA); P12_ISSUE(cn, 0, 0, cwA, scA); P12_BAR(); P12_COMP(3, 1, cwB, scB);
	v_add_u32_e32 v88, s44, v0
	v_dot4c_i32_i8_e32 v65, v60, v32
	v_lshrrev_b32_e32 v60, 4, v62
	v_lshl_or_b32 v0, v88, 7, v165
	v_lshl_or_b32 v88, v88, 4, v95
	v_and_b32_e32 v60, 0xf0f0f0f, v60
	global_load_dwordx4 v[0:3], v0, s[0:1]
	v_dot4c_i32_i8_e32 v65, v60, v33
	v_and_b32_e32 v60, 0xf0f0f0f, v63
	v_dot4c_i32_i8_e32 v64, v60, v34
	v_lshrrev_b32_e32 v60, 4, v63
	v_and_b32_e32 v60, 0xf0f0f0f, v60
	v_dot4c_i32_i8_e32 v64, v60, v35
	v_and_b32_e32 v60, 0xf0f0f0f, v56
	v_mov_b32_e32 v61, 0
	v_lshrrev_b32_e32 v56, 4, v56
	v_dot4c_i32_i8_e32 v61, v60, v36
	v_and_b32_e32 v56, 0xf0f0f0f, v56
	v_dot4c_i32_i8_e32 v61, v56, v37
	v_and_b32_e32 v56, 0xf0f0f0f, v57
	v_mov_b32_e32 v60, 0
	v_dot4c_i32_i8_e32 v60, v56, v38
	v_lshrrev_b32_e32 v56, 4, v57
	v_and_b32_e32 v56, 0xf0f0f0f, v56
	v_dot4c_i32_i8_e32 v60, v56, v39
	v_and_b32_e32 v56, 0xf0f0f0f, v58
	v_dot4c_i32_i8_e32 v61, v56, v32
	v_lshrrev_b32_e32 v56, 4, v58
	v_and_b32_e32 v56, 0xf0f0f0f, v56
	v_dot4c_i32_i8_e32 v61, v56, v33
	v_and_b32_e32 v56, 0xf0f0f0f, v59
	v_dot4c_i32_i8_e32 v60, v56, v34
	v_lshrrev_b32_e32 v56, 4, v59
	v_and_b32_e32 v56, 0xf0f0f0f, v56
	v_dot4c_i32_i8_e32 v60, v56, v35
	v_sub_u32_e32 v59, v64, v78
	s_waitcnt vmcnt(12)
	v_lshlrev_b32_e32 v57, 16, v243
	v_lshlrev_b32_e32 v56, 16, v242
	v_sub_u32_e32 v58, v60, v78
	v_add_u32_e32 v60, v59, v65
	v_add_u32_e32 v58, v58, v61
	v_cvt_f32_i32_e32 v59, v58
	v_cvt_f32_i32_e32 v58, v60
	s_mov_b32 s44, s45
	v_pk_fma_f32 v[100:101], v[56:57], v[58:59], v[100:101]
	v_and_b32_e32 v56, 0xf0f0f0f, v52
	v_mov_b32_e32 v57, 0
	v_lshrrev_b32_e32 v52, 4, v52
	v_dot4c_i32_i8_e32 v57, v56, v36
	v_and_b32_e32 v52, 0xf0f0f0f, v52
	v_dot4c_i32_i8_e32 v57, v52, v37
	v_and_b32_e32 v52, 0xf0f0f0f, v53
	v_mov_b32_e32 v56, 0
	v_dot4c_i32_i8_e32 v56, v52, v38
	v_lshrrev_b32_e32 v52, 4, v53
	v_and_b32_e32 v52, 0xf0f0f0f, v52
	v_dot4c_i32_i8_e32 v56, v52, v39
	v_and_b32_e32 v52, 0xf0f0f0f, v54
	v_dot4c_i32_i8_e32 v57, v52, v32
	v_lshrrev_b32_e32 v52, 4, v54
	v_and_b32_e32 v52, 0xf0f0f0f, v52
	v_dot4c_i32_i8_e32 v57, v52, v33
	v_and_b32_e32 v52, 0xf0f0f0f, v55
	v_dot4c_i32_i8_e32 v56, v52, v34
	v_lshrrev_b32_e32 v52, 4, v55
	v_and_b32_e32 v52, 0xf0f0f0f, v52
	v_dot4c_i32_i8_e32 v56, v52, v35
	v_and_b32_e32 v52, 0xf0f0f0f, v48
	v_mov_b32_e32 v53, 0
	v_lshrrev_b32_e32 v48, 4, v48
	v_dot4c_i32_i8_e32 v53, v52, v36
	v_and_b32_e32 v48, 0xf0f0f0f, v48
	v_dot4c_i32_i8_e32 v53, v48, v37
	v_and_b32_e32 v48, 0xf0f0f0f, v49
	v_mov_b32_e32 v52, 0
	v_dot4c_i32_i8_e32 v52, v48, v38
	v_lshrrev_b32_e32 v48, 4, v49
	v_and_b32_e32 v48, 0xf0f0f0f, v48
	v_dot4c_i32_i8_e32 v52, v48, v39
	v_and_b32_e32 v48, 0xf0f0f0f, v50
	v_dot4c_i32_i8_e32 v53, v48, v32
	v_lshrrev_b32_e32 v48, 4, v50
	v_and_b32_e32 v48, 0xf0f0f0f, v48
	v_dot4c_i32_i8_e32 v53, v48, v33
	v_and_b32_e32 v48, 0xf0f0f0f, v51
	v_dot4c_i32_i8_e32 v52, v48, v34
	v_lshrrev_b32_e32 v48, 4, v51
	v_and_b32_e32 v48, 0xf0f0f0f, v48
	v_dot4c_i32_i8_e32 v52, v48, v35
	v_sub_u32_e32 v51, v56, v78
	s_waitcnt vmcnt(10)
	v_lshlrev_b32_e32 v49, 16, v245
	v_lshlrev_b32_e32 v48, 16, v244
	v_sub_u32_e32 v50, v52, v78
	v_add_u32_e32 v52, v51, v57
	v_add_u32_e32 v50, v50, v53
	v_cvt_f32_i32_e32 v51, v50
	v_cvt_f32_i32_e32 v50, v52
	v_pk_fma_f32 v[98:99], v[48:49], v[50:51], v[98:99]
	v_and_b32_e32 v48, 0xf0f0f0f, v44
	v_mov_b32_e32 v49, 0
	v_lshrrev_b32_e32 v44, 4, v44
	v_dot4c_i32_i8_e32 v49, v48, v36
	v_and_b32_e32 v44, 0xf0f0f0f, v44
	v_dot4c_i32_i8_e32 v49, v44, v37
	v_and_b32_e32 v44, 0xf0f0f0f, v45
	v_mov_b32_e32 v48, 0
	v_dot4c_i32_i8_e32 v48, v44, v38
	v_lshrrev_b32_e32 v44, 4, v45
	v_and_b32_e32 v44, 0xf0f0f0f, v44
	v_dot4c_i32_i8_e32 v48, v44, v39
	v_and_b32_e32 v44, 0xf0f0f0f, v46
	v_dot4c_i32_i8_e32 v49, v44, v32
	v_lshrrev_b32_e32 v44, 4, v46
	v_and_b32_e32 v44, 0xf0f0f0f, v44
	v_dot4c_i32_i8_e32 v49, v44, v33
	v_and_b32_e32 v44, 0xf0f0f0f, v47
	v_dot4c_i32_i8_e32 v48, v44, v34
	v_lshrrev_b32_e32 v44, 4, v47
	v_and_b32_e32 v44, 0xf0f0f0f, v44
	v_dot4c_i32_i8_e32 v48, v44, v35
	v_and_b32_e32 v44, 0xf0f0f0f, v40
	v_mov_b32_e32 v45, 0
	v_dot4c_i32_i8_e32 v45, v44, v36
	v_lshrrev_b32_e32 v36, 4, v40
	v_and_b32_e32 v36, 0xf0f0f0f, v36
	v_dot4c_i32_i8_e32 v45, v36, v37
	v_and_b32_e32 v36, 0xf0f0f0f, v41
	v_mov_b32_e32 v37, 0
	v_dot4c_i32_i8_e32 v37, v36, v38
	v_lshrrev_b32_e32 v36, 4, v41
	v_and_b32_e32 v36, 0xf0f0f0f, v36
	v_dot4c_i32_i8_e32 v37, v36, v39
	v_and_b32_e32 v36, 0xf0f0f0f, v42
	v_dot4c_i32_i8_e32 v45, v36, v32
	v_lshrrev_b32_e32 v32, 4, v42
	v_and_b32_e32 v32, 0xf0f0f0f, v32
	v_dot4c_i32_i8_e32 v45, v32, v33
	v_and_b32_e32 v32, 0xf0f0f0f, v43
	v_dot4c_i32_i8_e32 v37, v32, v34
	v_lshrrev_b32_e32 v32, 4, v43
	v_and_b32_e32 v32, 0xf0f0f0f, v32
	v_dot4c_i32_i8_e32 v37, v32, v35
	v_sub_u32_e32 v35, v48, v78
	v_add_u32_e32 v36, v35, v49
	s_waitcnt vmcnt(8)
	v_lshlrev_b32_e32 v33, 16, v247
	v_sub_u32_e32 v34, v37, v78
	v_add_u32_e32 v34, v34, v45
	v_cvt_f32_i32_e32 v35, v34
	v_cvt_f32_i32_e32 v34, v36
	v_lshlrev_b32_e32 v32, 16, v246
	s_waitcnt vmcnt(0)
	v_perm_b32 v40, v190, v191, s48
	v_perm_b32 v41, v188, v189, s48
	v_pk_fma_f32 v[96:97], v[32:33], v[34:35], v[96:97]
	v_perm_b32 v42, v186, v187, s48
	v_perm_b32 v43, v184, v185, s48
	ds_read_b128 v[36:39], v166
	ds_read_b128 v[32:35], v166 offset:16
	ds_read_u16 v44, v93 offset:16512
	ds_read_u16 v45, v93 offset:16528
	ds_read_u16 v46, v93 offset:16544
	ds_read_u16 v47, v93 offset:16560
	v_mov_b32_e32 v48, 0
	s_waitcnt lgkmcnt(3)
	v_add_u32_e32 v44, s44, v44
	v_lshl_or_b32 v49, v44, 7, v165
	global_load_dwordx4 v[88:91], v49, s[0:1]
	v_lshl_or_b32 v49, v44, 4, v95
	s_waitcnt lgkmcnt(2)
	v_add_u32_e32 v44, s44, v45
	v_lshl_or_b32 v45, v44, 7, v165
	v_lshl_or_b32 v50, v44, 4, v95
	s_waitcnt lgkmcnt(1)
; #define P12_ISSUE(c_, i_, h_, CW_, SC_) do { _Pragma("unroll") for (int bb = 0; bb < 8; ++bb) { const unsigned ro = (unsigned)(c_) * 16384u + (unsigned)EL[(i_) * 128 + ((h_) * 8 + bb) * 8 + g8]; \
;         CW_[bb] = *(const v4u*)(U4 + (size_t)(ro * 128u + 16u * (unsigned)k8)); SC_[bb] = USS[(size_t)(ro * 8u + (unsigned)k8)]; } } while (0)
; #define P12_COMP(i_, h_, CW_, SC_) do { _Pragma("unroll") for (int bb = 0; bb < 8; ++bb) { int a0 = 0, a1 = 0; P12_U4(CW_[bb].x, xa.x, xa.y, a0); P12_U4(CW_[bb].y, xa.z, xa.w, a1); P12_U4(CW_[bb].z, xb.x, xb.y, a0); P12_U4(CW_[bb].w, xb.z, xb.w, a1); \
;         psum[(i_)][(h_) * 8 + bb] += __uint_as_float(SC_[bb] << 16) * (float)((a0 + a1) - xo); } } while (0)
; #define P12_BAR() asm volatile("" ::: "memory")
; __device__ __forceinline__ void p12_peer(Frame& F) {
;     ...
;     { v4u cwA[8], cwB[8]; unsigned scA[8], scB[8]; v4u xa, xb; int xo;
;       P12_ISSUE(0, 0, 0, cwA, scA);
; _Pragma("nounroll")
;       for (int c = 0; c < 16; ++c) { const int cn = c + 1 < 16 ? c + 1 : 15;
;           P12_XQ(c, 0); P12_ISSUE(c, 0, 1, cwB, scB); P12_BAR(); P12_COMP(0, 0, cwA, scA); P12_ISSUE(c, 1, 0, cwA, scA); P12_BAR(); P12_COMP(0, 1, cwB, scB);
;           P12_XQ(c, 1); P12_ISSUE(c, 1, 1, cwB, scB); P12_BAR(); P12_COMP(1, 0, cwA, scA); P12_ISSUE(c, 2, 0, cwA, scA); P12_BAR(); P12_COMP(1, 1, cwB, scB);
;           P12_XQ(c, 2); P12_ISSUE(c, 2, 1, cwB, scB); P12_BAR(); P12_COMP(2, 0, cwA, scA); P12_ISSUE(c, 3, 0, cwA, scA); P12_BAR(); P12_COMP(2, 1, cwB, scB);
;           P12_XQ(c, 3); P12_ISSUE(c, 3, 1, cwB, scB); P12_BAR(); P12_COMP(3, 0, cwA, scA); P12_ISSUE(cn, 0, 0, cwA, scA); P12_BAR(); P12_COMP(3, 1, cwB, scB);
	v_add_u32_e32 v44, s44, v46
	global_load_dwordx4 v[84:87], v45, s[0:1]
	v_lshl_or_b32 v45, v44, 7, v165
	v_lshl_or_b32 v51, v44, 4, v95
	s_waitcnt lgkmcnt(0)
	v_add_u32_e32 v44, s44, v47
	global_load_dwordx4 v[80:83], v45, s[0:1]
	v_lshl_or_b32 v45, v44, 7, v165
	v_lshl_or_b32 v56, v44, 4, v95
	ds_read_u16 v44, v93 offset:16576
	global_load_dwordx4 v[76:79], v45, s[0:1]
	v_dot4c_i32_i8_e32 v48, 0x1010101, v36
	v_dot4c_i32_i8_e32 v48, 0x1010101, v37
	v_dot4c_i32_i8_e32 v48, 0x1010101, v38
	s_waitcnt lgkmcnt(0)
	v_add_u32_e32 v44, s44, v44
	v_lshl_or_b32 v45, v44, 7, v165
	v_lshl_or_b32 v57, v44, 4, v95
	ds_read_u16 v44, v93 offset:16592
	global_load_dwordx4 v[68:71], v45, s[0:1]
	v_dot4c_i32_i8_e32 v48, 0x1010101, v39
	v_dot4c_i32_i8_e32 v48, 0x1010101, v32
	v_dot4c_i32_i8_e32 v48, 0x1010101, v33
	s_waitcnt lgkmcnt(0)
	v_add_u32_e32 v44, s44, v44
	v_lshl_or_b32 v45, v44, 7, v165
	v_lshl_or_b32 v58, v44, 4, v95
	ds_read_u16 v44, v93 offset:16608
	global_load_dwordx4 v[60:63], v45, s[0:1]
	v_dot4c_i32_i8_e32 v48, 0x1010101, v34
	v_dot4c_i32_i8_e32 v48, 0x1010101, v35
	s_add_i32 s45, s44, 0x4000
	s_waitcnt lgkmcnt(0)
	v_add_u32_e32 v44, s44, v44
	v_lshl_or_b32 v45, v44, 7, v165
	v_lshl_or_b32 v59, v44, 4, v95
	ds_read_u16 v44, v93 offset:16624
	global_load_dwordx4 v[52:55], v45, s[0:1]
	v_lshlrev_b32_e32 v171, 3, v48
	s_waitcnt vmcnt(10)
	v_and_b32_e32 v48, 0xf0f0f0f, v28
	v_lshrrev_b32_e32 v28, 4, v28
	s_waitcnt lgkmcnt(0)
	v_add_u32_e32 v64, s44, v44
	v_lshl_or_b32 v44, v64, 7, v165
	global_load_dwordx4 v[44:47], v44, s[0:1]
	v_lshl_or_b32 v64, v64, 4, v95
	v_mov_b32_e32 v49, 0
	v_dot4c_i32_i8_e32 v49, v48, v36
	v_and_b32_e32 v28, 0xf0f0f0f, v28
	v_dot4c_i32_i8_e32 v49, v28, v37
	v_and_b32_e32 v28, 0xf0f0f0f, v29
	v_mov_b32_e32 v48, 0
	v_dot4c_i32_i8_e32 v48, v28, v38
	v_lshrrev_b32_e32 v28, 4, v29
	v_and_b32_e32 v28, 0xf0f0f0f, v28
	v_dot4c_i32_i8_e32 v48, v28, v39
	v_and_b32_e32 v28, 0xf0f0f0f, v30
	v_dot4c_i32_i8_e32 v49, v28, v32
	v_lshrrev_b32_e32 v28, 4, v30
	v_and_b32_e32 v28, 0xf0f0f0f, v28
	v_dot4c_i32_i8_e32 v49, v28, v33
	v_and_b32_e32 v28, 0xf0f0f0f, v31
	v_dot4c_i32_i8_e32 v48, v28, v34
	v_lshrrev_b32_e32 v28, 4, v31
	v_and_b32_e32 v28, 0xf0f0f0f, v28
	v_dot4c_i32_i8_e32 v48, v28, v35
	s_waitcnt vmcnt(11)
	v_and_b32_e32 v28, 0xf0f0f0f, v24
	v_mov_b32_e32 v29, 0
	v_lshrrev_b32_e32 v24, 4, v24
	v_dot4c_i32_i8_e32 v29, v28, v36
	v_and_b32_e32 v24, 0xf0f0f0f, v24
	v_dot4c_i32_i8_e32 v29, v24, v37
	v_and_b32_e32 v24, 0xf0f0f0f, v25
	v_mov_b32_e32 v28, 0
	v_dot4c_i32_i8_e32 v28, v24, v38
	v_lshrrev_b32_e32 v24, 4, v25
	v_and_b32_e32 v24, 0xf0f0f0f, v24
	v_dot4c_i32_i8_e32 v28, v24, v39
	v_and_b32_e32 v24, 0xf0f0f0f, v26
	v_dot4c_i32_i8_e32 v29, v24, v32
	v_lshrrev_b32_e32 v24, 4, v26
	v_and_b32_e32 v24, 0xf0f0f0f, v24
	v_dot4c_i32_i8_e32 v29, v24, v33
	v_and_b32_e32 v24, 0xf0f0f0f, v27
	v_dot4c_i32_i8_e32 v28, v24, v34
	v_lshrrev_b32_e32 v24, 4, v27
	v_and_b32_e32 v24, 0xf0f0f0f, v24
	v_dot4c_i32_i8_e32 v28, v24, v35
	v_add_u32_e32 v26, v49, v48
	v_sub_u32_e32 v26, v26, v171
	v_and_b32_e32 v25, 0xffff0000, v43
	v_add_u32_e32 v27, v29, v28
	v_sub_u32_e32 v28, v27, v171
	v_cvt_f32_i32_e32 v27, v26
	v_cvt_f32_i32_e32 v26, v28
	v_lshlrev_b32_e32 v24, 16, v43
	s_cmp_eq_u32 s44, 0x3c000
	v_pk_fma_f32 v[158:159], v[24:25], v[26:27], v[158:159]
	s_waitcnt vmcnt(10)
	v_and_b32_e32 v24, 0xf0f0f0f, v20
	v_mov_b32_e32 v25, 0
	v_lshrrev_b32_e32 v20, 4, v20
	v_dot4c_i32_i8_e32 v25, v24, v36
	v_and_b32_e32 v20, 0xf0f0f0f, v20
	v_dot4c_i32_i8_e32 v25, v20, v37
	v_and_b32_e32 v20, 0xf0f0f0f, v21
	v_mov_b32_e32 v24, 0
	v_dot4c_i32_i8_e32 v24, v20, v38
	v_lshrrev_b32_e32 v20, 4, v21
	v_and_b32_e32 v20, 0xf0f0f0f, v20
	v_dot4c_i32_i8_e32 v24, v20, v39
	v_and_b32_e32 v20, 0xf0f0f0f, v22
	v_dot4c_i32_i8_e32 v25, v20, v32
	v_lshrrev_b32_e32 v20, 4, v22
	v_and_b32_e32 v20, 0xf0f0f0f, v20
	v_dot4c_i32_i8_e32 v25, v20, v33
	v_and_b32_e32 v20, 0xf0f0f0f, v23
	v_dot4c_i32_i8_e32 v24, v20, v34
	v_lshrrev_b32_e32 v20, 4, v23
	v_and_b32_e32 v20, 0xf0f0f0f, v20
	v_dot4c_i32_i8_e32 v24, v20, v35
	s_waitcnt vmcnt(10)
	v_and_b32_e32 v20, 0xf0f0f0f, v16
	v_mov_b32_e32 v21, 0
	v_lshrrev_b32_e32 v16, 4, v16
	v_dot4c_i32_i8_e32 v21, v20, v36
	v_and_b32_e32 v16, 0xf0f0f0f, v16
	v_dot4c_i32_i8_e32 v21, v16, v37
	v_and_b32_e32 v16, 0xf0f0f0f, v17
	v_mov_b32_e32 v20, 0
	v_dot4c_i32_i8_e32 v20, v16, v38
	v_lshrrev_b32_e32 v16, 4, v17
	v_and_b32_e32 v16, 0xf0f0f0f, v16
	v_dot4c_i32_i8_e32 v20, v16, v39
	v_and_b32_e32 v16, 0xf0f0f0f, v18
	v_dot4c_i32_i8_e32 v21, v16, v32
	v_lshrrev_b32_e32 v16, 4, v18
	v_and_b32_e32 v16, 0xf0f0f0f, v16
	v_dot4c_i32_i8_e32 v21, v16, v33
	v_and_b32_e32 v16, 0xf0f0f0f, v19
	v_dot4c_i32_i8_e32 v20, v16, v34
	v_lshrrev_b32_e32 v16, 4, v19
	v_and_b32_e32 v16, 0xf0f0f0f, v16
	v_dot4c_i32_i8_e32 v20, v16, v35
	v_add_u32_e32 v18, v25, v24
	v_sub_u32_e32 v18, v18, v171
	v_and_b32_e32 v17, 0xffff0000, v42
	v_add_u32_e32 v19, v21, v20
	v_sub_u32_e32 v20, v19, v171
	v_cvt_f32_i32_e32 v19, v18
	v_cvt_f32_i32_e32 v18, v20
	v_lshlrev_b32_e32 v16, 16, v42
	v_pk_fma_f32 v[156:157], v[16:17], v[18:19], v[156:157]
	s_waitcnt vmcnt(9)
	v_and_b32_e32 v16, 0xf0f0f0f, v12
	v_mov_b32_e32 v17, 0
	v_lshrrev_b32_e32 v12, 4, v12
	v_dot4c_i32_i8_e32 v17, v16, v36
	v_and_b32_e32 v12, 0xf0f0f0f, v12
	v_dot4c_i32_i8_e32 v17, v12, v37
	v_and_b32_e32 v12, 0xf0f0f0f, v13
	v_mov_b32_e32 v16, 0
	v_dot4c_i32_i8_e32 v16, v12, v38
	v_lshrrev_b32_e32 v12, 4, v13
	v_and_b32_e32 v12, 0xf0f0f0f, v12
	v_dot4c_i32_i8_e32 v16, v12, v39
	v_and_b32_e32 v12, 0xf0f0f0f, v14
	v_dot4c_i32_i8_e32 v17, v12, v32
	v_lshrrev_b32_e32 v12, 4, v14
	v_and_b32_e32 v12, 0xf0f0f0f, v12
	v_dot4c_i32_i8_e32 v17, v12, v33
	v_and_b32_e32 v12, 0xf0f0f0f, v15
	v_dot4c_i32_i8_e32 v16, v12, v34
	v_lshrrev_b32_e32 v12, 4, v15
	v_and_b32_e32 v12, 0xf0f0f0f, v12
	v_dot4c_i32_i8_e32 v16, v12, v35
	s_waitcnt vmcnt(9)
; #define P12_ISSUE(c_, i_, h_, CW_, SC_) do { _Pragma("unroll") for (int bb = 0; bb < 8; ++bb) { const unsigned ro = (unsigned)(c_) * 16384u + (unsigned)EL[(i_) * 128 + ((h_) * 8 + bb) * 8 + g8]; \
;         CW_[bb] = *(const v4u*)(U4 + (size_t)(ro * 128u + 16u * (unsigned)k8)); SC_[bb] = USS[(size_t)(ro * 8u + (unsigned)k8)]; } } while (0)
; #define P12_COMP(i_, h_, CW_, SC_) do { _Pragma("unroll") for (int bb = 0; bb < 8; ++bb) { int a0 = 0, a1 = 0; P12_U4(CW_[bb].x, xa.x, xa.y, a0); P12_U4(CW_[bb].y, xa.z, xa.w, a1); P12_U4(CW_[bb].z, xb.x, xb.y, a0); P12_U4(CW_[bb].w, xb.z, xb.w, a1); \
;         psum[(i_)][(h_) * 8 + bb] += __uint_as_float(SC_[bb] << 16) * (float)((a0 + a1) - xo); } } while (0)
; #define P12_BAR() asm volatile("" ::: "memory")
; __device__ __forceinline__ void p12_peer(Frame& F) {
;     ...
;     { v4u cwA[8], cwB[8]; unsigned scA[8], scB[8]; v4u xa, xb; int xo;
;       P12_ISSUE(0, 0, 0, cwA, scA);
; _Pragma("nounroll")
;       for (int c = 0; c < 16; ++c) { const int cn = c + 1 < 16 ? c + 1 : 15;
;           P12_XQ(c, 0); P12_ISSUE(c, 0, 1, cwB, scB); P12_BAR(); P12_COMP(0, 0, cwA, scA); P12_ISSUE(c, 1, 0, cwA, scA); P12_BAR(); P12_COMP(0, 1, cwB, scB);
;           P12_XQ(c, 1); P12_ISSUE(c, 1, 1, cwB, scB); P12_BAR(); P12_COMP(1, 0, cwA, scA); P12_ISSUE(c, 2, 0, cwA, scA); P12_BAR(); P12_COMP(1, 1, cwB, scB);
;           P12_XQ(c, 2); P12_ISSUE(c, 2, 1, cwB, scB); P12_BAR(); P12_COMP(2, 0, cwA, scA); P12_ISSUE(c, 3, 0, cwA, scA); P12_BAR(); P12_COMP(2, 1, cwB, scB);
;           P12_XQ(c, 3); P12_ISSUE(c, 3, 1, cwB, scB); P12_BAR(); P12_COMP(3, 0, cwA, scA); P12_ISSUE(cn, 0, 0, cwA, scA); P12_BAR(); P12_COMP(3, 1, cwB, scB);
	v_and_b32_e32 v12, 0xf0f0f0f, v8
	v_mov_b32_e32 v13, 0
	v_lshrrev_b32_e32 v8, 4, v8
	v_dot4c_i32_i8_e32 v13, v12, v36
	v_and_b32_e32 v8, 0xf0f0f0f, v8
	v_dot4c_i32_i8_e32 v13, v8, v37
	v_and_b32_e32 v8, 0xf0f0f0f, v9
	v_mov_b32_e32 v12, 0
	v_dot4c_i32_i8_e32 v12, v8, v38
	v_lshrrev_b32_e32 v8, 4, v9
	v_and_b32_e32 v8, 0xf0f0f0f, v8
	v_dot4c_i32_i8_e32 v12, v8, v39
	v_and_b32_e32 v8, 0xf0f0f0f, v10
	v_dot4c_i32_i8_e32 v13, v8, v32
	v_lshrrev_b32_e32 v8, 4, v10
	v_and_b32_e32 v8, 0xf0f0f0f, v8
	v_dot4c_i32_i8_e32 v13, v8, v33
	v_and_b32_e32 v8, 0xf0f0f0f, v11
	v_dot4c_i32_i8_e32 v12, v8, v34
	v_lshrrev_b32_e32 v8, 4, v11
	v_and_b32_e32 v8, 0xf0f0f0f, v8
	v_dot4c_i32_i8_e32 v12, v8, v35
	v_add_u32_e32 v10, v17, v16
	v_sub_u32_e32 v10, v10, v171
	v_and_b32_e32 v9, 0xffff0000, v41
	v_add_u32_e32 v11, v13, v12
	v_sub_u32_e32 v12, v11, v171
	v_cvt_f32_i32_e32 v11, v10
	v_cvt_f32_i32_e32 v10, v12
	v_lshlrev_b32_e32 v8, 16, v41
	v_pk_fma_f32 v[154:155], v[8:9], v[10:11], v[154:155]
	s_waitcnt vmcnt(8)
	v_and_b32_e32 v8, 0xf0f0f0f, v4
	v_mov_b32_e32 v9, 0
	v_lshrrev_b32_e32 v4, 4, v4
	v_dot4c_i32_i8_e32 v9, v8, v36
	v_and_b32_e32 v4, 0xf0f0f0f, v4
	v_dot4c_i32_i8_e32 v9, v4, v37
	v_and_b32_e32 v4, 0xf0f0f0f, v5
	v_mov_b32_e32 v8, 0
	v_dot4c_i32_i8_e32 v8, v4, v38
	v_lshrrev_b32_e32 v4, 4, v5
	v_and_b32_e32 v4, 0xf0f0f0f, v4
	v_dot4c_i32_i8_e32 v8, v4, v39
	v_and_b32_e32 v4, 0xf0f0f0f, v6
	v_dot4c_i32_i8_e32 v9, v4, v32
	v_lshrrev_b32_e32 v4, 4, v6
	v_and_b32_e32 v4, 0xf0f0f0f, v4
	v_dot4c_i32_i8_e32 v9, v4, v33
	v_and_b32_e32 v4, 0xf0f0f0f, v7
	v_dot4c_i32_i8_e32 v8, v4, v34
	v_lshrrev_b32_e32 v4, 4, v7
	v_and_b32_e32 v4, 0xf0f0f0f, v4
	v_dot4c_i32_i8_e32 v8, v4, v35
	s_waitcnt vmcnt(8)
	v_and_b32_e32 v4, 0xf0f0f0f, v0
	v_mov_b32_e32 v5, 0
	v_lshrrev_b32_e32 v0, 4, v0
	v_dot4c_i32_i8_e32 v5, v4, v36
	v_and_b32_e32 v0, 0xf0f0f0f, v0
	v_dot4c_i32_i8_e32 v5, v0, v37
	v_and_b32_e32 v0, 0xf0f0f0f, v1
	v_mov_b32_e32 v4, 0
	v_dot4c_i32_i8_e32 v4, v0, v38
	v_lshrrev_b32_e32 v0, 4, v1
	v_and_b32_e32 v0, 0xf0f0f0f, v0
	v_dot4c_i32_i8_e32 v4, v0, v39
	v_and_b32_e32 v0, 0xf0f0f0f, v2
	v_dot4c_i32_i8_e32 v5, v0, v32
	v_lshrrev_b32_e32 v0, 4, v2
	v_and_b32_e32 v0, 0xf0f0f0f, v0
	v_dot4c_i32_i8_e32 v5, v0, v33
	v_and_b32_e32 v0, 0xf0f0f0f, v3
	v_dot4c_i32_i8_e32 v4, v0, v34
	v_lshrrev_b32_e32 v0, 4, v3
	v_and_b32_e32 v0, 0xf0f0f0f, v0
	v_dot4c_i32_i8_e32 v4, v0, v35
	v_add_u32_e32 v2, v9, v8
	v_sub_u32_e32 v2, v2, v171
	v_and_b32_e32 v1, 0xffff0000, v40
	v_add_u32_e32 v3, v5, v4
	v_sub_u32_e32 v4, v3, v171
	v_cvt_f32_i32_e32 v3, v2
	v_cvt_f32_i32_e32 v2, v4
	v_lshlrev_b32_e32 v0, 16, v40
	v_pk_fma_f32 v[152:153], v[0:1], v[2:3], v[152:153]
	ds_read_u16 v0, v93 offset:16640
	ds_read_u16 v1, v93 offset:16656
	ds_read_u16 v2, v93 offset:16672
	ds_read_u16 v3, v93 offset:16688
	s_waitcnt lgkmcnt(3)
	v_add_u32_e32 v0, s44, v0
	v_lshl_or_b32 v4, v0, 7, v165
	s_waitcnt lgkmcnt(2)
	v_add_u32_e32 v1, s44, v1
	global_load_dwordx4 v[72:75], v4, s[0:1]
	v_lshl_or_b32 v4, v1, 7, v165
	s_waitcnt lgkmcnt(1)
	v_add_u32_e32 v2, s44, v2
	global_load_dwordx4 v[64:67], v4, s[0:1]
	v_lshl_or_b32 v4, v2, 7, v165
	s_waitcnt lgkmcnt(0)
	v_add_u32_e32 v3, s44, v3
	global_load_dwordx4 v[56:59], v4, s[0:1]
	v_lshl_or_b32 v4, v3, 7, v165
	global_load_dwordx4 v[48:51], v4, s[0:1]
	ds_read_u16 v4, v93 offset:16704
	v_lshl_or_b32 v0, v0, 4, v95
	v_lshl_or_b32 v1, v1, 4, v95
	v_lshl_or_b32 v2, v2, 4, v95
	v_lshl_or_b32 v3, v3, 4, v95
	s_waitcnt lgkmcnt(0)
	v_add_u32_e32 v4, s44, v4
	v_lshl_or_b32 v5, v4, 7, v165
	global_load_dwordx4 v[40:43], v5, s[0:1]
	ds_read_u16 v5, v93 offset:16720
	v_lshl_or_b32 v4, v4, 4, v95
	s_waitcnt lgkmcnt(0)
	v_add_u32_e32 v5, s44, v5
	v_lshl_or_b32 v6, v5, 7, v165
	global_load_dwordx4 v[24:27], v6, s[0:1]
	ds_read_u16 v6, v93 offset:16736
	v_lshl_or_b32 v5, v5, 4, v95
	s_waitcnt lgkmcnt(0)
	v_add_u32_e32 v6, s44, v6
	v_lshl_or_b32 v7, v6, 7, v165
	global_load_dwordx4 v[12:15], v7, s[0:1]
	ds_read_u16 v7, v93 offset:16752
	v_lshl_or_b32 v6, v6, 4, v95
	s_waitcnt lgkmcnt(0)
	v_add_u32_e32 v7, s44, v7
	v_lshl_or_b32 v8, v7, 7, v165
	global_load_dwordx4 v[8:11], v8, s[0:1]
	v_lshl_or_b32 v7, v7, 4, v95
	s_waitcnt vmcnt(15)
	v_and_b32_e32 v0, 0xf0f0f0f, v88
	v_mov_b32_e32 v2, 0
	v_dot4c_i32_i8_e32 v2, v0, v36
	v_lshrrev_b32_e32 v0, 4, v88
	v_and_b32_e32 v0, 0xf0f0f0f, v0
	v_dot4c_i32_i8_e32 v2, v0, v37
	v_and_b32_e32 v0, 0xf0f0f0f, v89
	v_mov_b32_e32 v3, 0
	v_dot4c_i32_i8_e32 v3, v0, v38
	v_lshrrev_b32_e32 v0, 4, v89
	v_and_b32_e32 v0, 0xf0f0f0f, v0
	v_dot4c_i32_i8_e32 v3, v0, v39
	v_and_b32_e32 v0, 0xf0f0f0f, v90
	v_dot4c_i32_i8_e32 v2, v0, v32
	v_lshrrev_b32_e32 v0, 4, v90
	v_and_b32_e32 v0, 0xf0f0f0f, v0
	v_dot4c_i32_i8_e32 v2, v0, v33
	v_and_b32_e32 v0, 0xf0f0f0f, v91
	v_dot4c_i32_i8_e32 v3, v0, v34
	v_lshrrev_b32_e32 v0, 4, v91
	v_and_b32_e32 v0, 0xf0f0f0f, v0
	v_dot4c_i32_i8_e32 v3, v0, v35
	s_waitcnt vmcnt(14)
	v_and_b32_e32 v0, 0xf0f0f0f, v84
	v_mov_b32_e32 v4, 0
	v_dot4c_i32_i8_e32 v4, v0, v36
	v_lshrrev_b32_e32 v0, 4, v84
	v_and_b32_e32 v0, 0xf0f0f0f, v0
	v_dot4c_i32_i8_e32 v4, v0, v37
	v_and_b32_e32 v0, 0xf0f0f0f, v85
	v_mov_b32_e32 v5, 0
	v_dot4c_i32_i8_e32 v5, v0, v38
	v_lshrrev_b32_e32 v0, 4, v85
	v_and_b32_e32 v0, 0xf0f0f0f, v0
	v_dot4c_i32_i8_e32 v5, v0, v39
	v_and_b32_e32 v0, 0xf0f0f0f, v86
	v_dot4c_i32_i8_e32 v4, v0, v32
	v_lshrrev_b32_e32 v0, 4, v86
	v_and_b32_e32 v0, 0xf0f0f0f, v0
	v_dot4c_i32_i8_e32 v4, v0, v33
	v_and_b32_e32 v0, 0xf0f0f0f, v87
	v_dot4c_i32_i8_e32 v5, v0, v34
	v_lshrrev_b32_e32 v0, 4, v87
	v_and_b32_e32 v0, 0xf0f0f0f, v0
	v_dot4c_i32_i8_e32 v5, v0, v35
	v_add_u32_e32 v2, v2, v3
	v_sub_u32_e32 v2, v2, v171
	s_waitcnt vmcnt(8)
; #define P12_ISSUE(c_, i_, h_, CW_, SC_) do { _Pragma("unroll") for (int bb = 0; bb < 8; ++bb) { const unsigned ro = (unsigned)(c_) * 16384u + (unsigned)EL[(i_) * 128 + ((h_) * 8 + bb) * 8 + g8]; \
;         CW_[bb] = *(const v4u*)(U4 + (size_t)(ro * 128u + 16u * (unsigned)k8)); SC_[bb] = USS[(size_t)(ro * 8u + (unsigned)k8)]; } } while (0)
; #define P12_COMP(i_, h_, CW_, SC_) do { _Pragma("unroll") for (int bb = 0; bb < 8; ++bb) { int a0 = 0, a1 = 0; P12_U4(CW_[bb].x, xa.x, xa.y, a0); P12_U4(CW_[bb].y, xa.z, xa.w, a1); P12_U4(CW_[bb].z, xb.x, xb.y, a0); P12_U4(CW_[bb].w, xb.z, xb.w, a1); \
;         psum[(i_)][(h_) * 8 + bb] += __uint_as_float(SC_[bb] << 16) * (float)((a0 + a1) - xo); } } while (0)
; #define P12_BAR() asm volatile("" ::: "memory")
; __device__ __forceinline__ void p12_peer(Frame& F) {
;     ...
;     { v4u cwA[8], cwB[8]; unsigned scA[8], scB[8]; v4u xa, xb; int xo;
;       P12_ISSUE(0, 0, 0, cwA, scA);
; _Pragma("nounroll")
;       for (int c = 0; c < 16; ++c) { const int cn = c + 1 < 16 ? c + 1 : 15;
;           P12_XQ(c, 0); P12_ISSUE(c, 0, 1, cwB, scB); P12_BAR(); P12_COMP(0, 0, cwA, scA); P12_ISSUE(c, 1, 0, cwA, scA); P12_BAR(); P12_COMP(0, 1, cwB, scB);
;           P12_XQ(c, 1); P12_ISSUE(c, 1, 1, cwB, scB); P12_BAR(); P12_COMP(1, 0, cwA, scA); P12_ISSUE(c, 2, 0, cwA, scA); P12_BAR(); P12_COMP(1, 1, cwB, scB);
;           P12_XQ(c, 2); P12_ISSUE(c, 2, 1, cwB, scB); P12_BAR(); P12_COMP(2, 0, cwA, scA); P12_ISSUE(c, 3, 0, cwA, scA); P12_BAR(); P12_COMP(2, 1, cwB, scB);
;           P12_XQ(c, 3); P12_ISSUE(c, 3, 1, cwB, scB); P12_BAR(); P12_COMP(3, 0, cwA, scA); P12_ISSUE(cn, 0, 0, cwA, scA); P12_BAR(); P12_COMP(3, 1, cwB, scB);
	v_and_b32_e32 v1, 0xffff0000, v192
	v_sub_u32_e32 v3, v5, v171
	v_add_u32_e32 v4, v3, v4
	v_cvt_f32_i32_e32 v3, v2
	v_cvt_f32_i32_e32 v2, v4
	v_and_b32_e32 v0, 0xffff0000, v193
	v_mov_b32_e32 v4, 0
	v_mov_b32_e32 v5, 0
	v_pk_fma_f32 v[150:151], v[0:1], v[2:3], v[150:151]
	v_and_b32_e32 v0, 0xf0f0f0f, v80
	v_mov_b32_e32 v2, 0
	v_dot4c_i32_i8_e32 v2, v0, v36
	v_lshrrev_b32_e32 v0, 4, v80
	v_and_b32_e32 v0, 0xf0f0f0f, v0
	v_dot4c_i32_i8_e32 v2, v0, v37
	v_and_b32_e32 v0, 0xf0f0f0f, v81
	v_mov_b32_e32 v3, 0
	v_dot4c_i32_i8_e32 v3, v0, v38
	v_lshrrev_b32_e32 v0, 4, v81
	v_and_b32_e32 v0, 0xf0f0f0f, v0
	v_dot4c_i32_i8_e32 v3, v0, v39
	v_and_b32_e32 v0, 0xf0f0f0f, v82
	v_dot4c_i32_i8_e32 v2, v0, v32
	v_lshrrev_b32_e32 v0, 4, v82
	v_and_b32_e32 v0, 0xf0f0f0f, v0
	v_dot4c_i32_i8_e32 v2, v0, v33
	v_and_b32_e32 v0, 0xf0f0f0f, v83
	v_dot4c_i32_i8_e32 v3, v0, v34
	v_lshrrev_b32_e32 v0, 4, v83
	v_and_b32_e32 v0, 0xf0f0f0f, v0
	v_dot4c_i32_i8_e32 v3, v0, v35
	v_and_b32_e32 v0, 0xf0f0f0f, v76
	v_dot4c_i32_i8_e32 v4, v0, v36
	v_lshrrev_b32_e32 v0, 4, v76
	v_and_b32_e32 v0, 0xf0f0f0f, v0
	v_dot4c_i32_i8_e32 v4, v0, v37
	v_and_b32_e32 v0, 0xf0f0f0f, v77
	v_dot4c_i32_i8_e32 v5, v0, v38
	v_lshrrev_b32_e32 v0, 4, v77
	v_and_b32_e32 v0, 0xf0f0f0f, v0
	v_dot4c_i32_i8_e32 v5, v0, v39
	v_and_b32_e32 v0, 0xf0f0f0f, v78
	v_dot4c_i32_i8_e32 v4, v0, v32
	v_lshrrev_b32_e32 v0, 4, v78
	v_and_b32_e32 v0, 0xf0f0f0f, v0
	v_dot4c_i32_i8_e32 v4, v0, v33
	v_and_b32_e32 v0, 0xf0f0f0f, v79
	v_dot4c_i32_i8_e32 v5, v0, v34
	v_lshrrev_b32_e32 v0, 4, v79
	v_and_b32_e32 v0, 0xf0f0f0f, v0
	v_dot4c_i32_i8_e32 v5, v0, v35
	v_sub_u32_e32 v3, v3, v171
	v_add_u32_e32 v2, v3, v2
	v_cvt_f32_i32_e32 v3, v2
	v_sub_u32_e32 v5, v5, v171
	v_add_u32_e32 v4, v5, v4
	v_cvt_f32_i32_e32 v2, v4
	s_waitcnt vmcnt(8)
	v_and_b32_e32 v1, 0xffff0000, v194
	v_and_b32_e32 v0, 0xffff0000, v195
	v_mov_b32_e32 v4, 0
	v_pk_fma_f32 v[148:149], v[0:1], v[2:3], v[148:149]
	v_and_b32_e32 v0, 0xf0f0f0f, v68
	v_mov_b32_e32 v2, 0
	v_dot4c_i32_i8_e32 v2, v0, v36
	v_lshrrev_b32_e32 v0, 4, v68
	v_and_b32_e32 v0, 0xf0f0f0f, v0
	v_dot4c_i32_i8_e32 v2, v0, v37
	v_and_b32_e32 v0, 0xf0f0f0f, v69
	v_mov_b32_e32 v3, 0
	v_dot4c_i32_i8_e32 v3, v0, v38
	v_lshrrev_b32_e32 v0, 4, v69
	v_and_b32_e32 v0, 0xf0f0f0f, v0
	v_dot4c_i32_i8_e32 v3, v0, v39
	v_and_b32_e32 v0, 0xf0f0f0f, v70
	v_dot4c_i32_i8_e32 v2, v0, v32
	v_lshrrev_b32_e32 v0, 4, v70
	v_and_b32_e32 v0, 0xf0f0f0f, v0
	v_dot4c_i32_i8_e32 v2, v0, v33
	v_and_b32_e32 v0, 0xf0f0f0f, v71
	v_dot4c_i32_i8_e32 v3, v0, v34
	v_lshrrev_b32_e32 v0, 4, v71
	v_and_b32_e32 v0, 0xf0f0f0f, v0
	v_dot4c_i32_i8_e32 v3, v0, v35
	v_and_b32_e32 v0, 0xf0f0f0f, v60
	v_dot4c_i32_i8_e32 v4, v0, v36
	v_lshrrev_b32_e32 v0, 4, v60
	v_and_b32_e32 v0, 0xf0f0f0f, v0
	v_dot4c_i32_i8_e32 v4, v0, v37
	v_and_b32_e32 v0, 0xf0f0f0f, v61
	v_mov_b32_e32 v5, 0
	v_dot4c_i32_i8_e32 v5, v0, v38
	v_lshrrev_b32_e32 v0, 4, v61
	v_and_b32_e32 v0, 0xf0f0f0f, v0
	v_dot4c_i32_i8_e32 v5, v0, v39
	v_and_b32_e32 v0, 0xf0f0f0f, v62
	v_dot4c_i32_i8_e32 v4, v0, v32
	v_lshrrev_b32_e32 v0, 4, v62
	v_and_b32_e32 v0, 0xf0f0f0f, v0
	v_dot4c_i32_i8_e32 v4, v0, v33
	v_and_b32_e32 v0, 0xf0f0f0f, v63
	v_dot4c_i32_i8_e32 v5, v0, v34
	v_lshrrev_b32_e32 v0, 4, v63
	v_and_b32_e32 v0, 0xf0f0f0f, v0
	v_dot4c_i32_i8_e32 v5, v0, v35
	v_sub_u32_e32 v3, v3, v171
	v_add_u32_e32 v2, v3, v2
	v_cvt_f32_i32_e32 v3, v2
	v_sub_u32_e32 v5, v5, v171
	v_add_u32_e32 v4, v5, v4
	v_cvt_f32_i32_e32 v2, v4
	s_waitcnt vmcnt(8)
	v_and_b32_e32 v1, 0xffff0000, v196
	v_and_b32_e32 v0, 0xffff0000, v197
	v_mov_b32_e32 v4, 0
	v_pk_fma_f32 v[146:147], v[0:1], v[2:3], v[146:147]
	v_and_b32_e32 v0, 0xf0f0f0f, v52
	v_mov_b32_e32 v2, 0
	v_dot4c_i32_i8_e32 v2, v0, v36
	v_lshrrev_b32_e32 v0, 4, v52
	v_and_b32_e32 v0, 0xf0f0f0f, v0
	v_dot4c_i32_i8_e32 v2, v0, v37
	v_and_b32_e32 v0, 0xf0f0f0f, v53
	v_mov_b32_e32 v3, 0
	v_dot4c_i32_i8_e32 v3, v0, v38
	v_lshrrev_b32_e32 v0, 4, v53
	v_and_b32_e32 v0, 0xf0f0f0f, v0
	v_dot4c_i32_i8_e32 v3, v0, v39
	v_and_b32_e32 v0, 0xf0f0f0f, v54
	v_dot4c_i32_i8_e32 v2, v0, v32
	v_lshrrev_b32_e32 v0, 4, v54
	v_and_b32_e32 v0, 0xf0f0f0f, v0
	v_dot4c_i32_i8_e32 v2, v0, v33
	v_and_b32_e32 v0, 0xf0f0f0f, v55
	v_dot4c_i32_i8_e32 v3, v0, v34
	v_lshrrev_b32_e32 v0, 4, v55
	v_and_b32_e32 v0, 0xf0f0f0f, v0
	v_dot4c_i32_i8_e32 v3, v0, v35
	v_and_b32_e32 v0, 0xf0f0f0f, v44
	v_dot4c_i32_i8_e32 v4, v0, v36
	v_lshrrev_b32_e32 v0, 4, v44
	v_and_b32_e32 v0, 0xf0f0f0f, v0
	v_dot4c_i32_i8_e32 v4, v0, v37
	v_and_b32_e32 v0, 0xf0f0f0f, v45
	v_mov_b32_e32 v5, 0
	v_dot4c_i32_i8_e32 v5, v0, v38
	v_lshrrev_b32_e32 v0, 4, v45
	v_and_b32_e32 v0, 0xf0f0f0f, v0
	v_dot4c_i32_i8_e32 v5, v0, v39
	v_and_b32_e32 v0, 0xf0f0f0f, v46
	v_dot4c_i32_i8_e32 v4, v0, v32
	v_lshrrev_b32_e32 v0, 4, v46
	v_and_b32_e32 v0, 0xf0f0f0f, v0
	v_dot4c_i32_i8_e32 v4, v0, v33
	v_and_b32_e32 v0, 0xf0f0f0f, v47
	v_dot4c_i32_i8_e32 v5, v0, v34
	v_lshrrev_b32_e32 v0, 4, v47
	v_and_b32_e32 v0, 0xf0f0f0f, v0
	v_dot4c_i32_i8_e32 v5, v0, v35
	v_sub_u32_e32 v3, v3, v171
	v_add_u32_e32 v2, v3, v2
	v_cvt_f32_i32_e32 v3, v2
	v_sub_u32_e32 v5, v5, v171
	v_add_u32_e32 v4, v5, v4
	v_cvt_f32_i32_e32 v2, v4
	s_waitcnt vmcnt(8)
	v_and_b32_e32 v1, 0xffff0000, v198
	v_and_b32_e32 v0, 0xffff0000, v199
	v_pk_fma_f32 v[144:145], v[0:1], v[2:3], v[144:145]
	ds_read_b128 v[4:7], v166 offset:4096
	ds_read_b128 v[0:3], v166 offset:4112
	ds_read_u16 v16, v93 offset:16768
	ds_read_u16 v17, v93 offset:16784
	ds_read_u16 v18, v93 offset:16800
	ds_read_u16 v19, v93 offset:16816
	v_mov_b32_e32 v44, 0
	s_waitcnt lgkmcnt(3)
	v_add_u32_e32 v16, s44, v16
	v_lshl_or_b32 v20, v16, 7, v165
	v_lshl_or_b32 v45, v16, 4, v95
	s_waitcnt lgkmcnt(2)
; #define P12_ISSUE(c_, i_, h_, CW_, SC_) do { _Pragma("unroll") for (int bb = 0; bb < 8; ++bb) { const unsigned ro = (unsigned)(c_) * 16384u + (unsigned)EL[(i_) * 128 + ((h_) * 8 + bb) * 8 + g8]; \
;         CW_[bb] = *(const v4u*)(U4 + (size_t)(ro * 128u + 16u * (unsigned)k8)); SC_[bb] = USS[(size_t)(ro * 8u + (unsigned)k8)]; } } while (0)
; #define P12_COMP(i_, h_, CW_, SC_) do { _Pragma("unroll") for (int bb = 0; bb < 8; ++bb) { int a0 = 0, a1 = 0; P12_U4(CW_[bb].x, xa.x, xa.y, a0); P12_U4(CW_[bb].y, xa.z, xa.w, a1); P12_U4(CW_[bb].z, xb.x, xb.y, a0); P12_U4(CW_[bb].w, xb.z, xb.w, a1); \
;         psum[(i_)][(h_) * 8 + bb] += __uint_as_float(SC_[bb] << 16) * (float)((a0 + a1) - xo); } } while (0)
; #define P12_BAR() asm volatile("" ::: "memory")
; __device__ __forceinline__ void p12_peer(Frame& F) {
;     ...
;     { v4u cwA[8], cwB[8]; unsigned scA[8], scB[8]; v4u xa, xb; int xo;
;       P12_ISSUE(0, 0, 0, cwA, scA);
; _Pragma("nounroll")
;       for (int c = 0; c < 16; ++c) { const int cn = c + 1 < 16 ? c + 1 : 15;
;           P12_XQ(c, 0); P12_ISSUE(c, 0, 1, cwB, scB); P12_BAR(); P12_COMP(0, 0, cwA, scA); P12_ISSUE(c, 1, 0, cwA, scA); P12_BAR(); P12_COMP(0, 1, cwB, scB);
;           P12_XQ(c, 1); P12_ISSUE(c, 1, 1, cwB, scB); P12_BAR(); P12_COMP(1, 0, cwA, scA); P12_ISSUE(c, 2, 0, cwA, scA); P12_BAR(); P12_COMP(1, 1, cwB, scB);
;           P12_XQ(c, 2); P12_ISSUE(c, 2, 1, cwB, scB); P12_BAR(); P12_COMP(2, 0, cwA, scA); P12_ISSUE(c, 3, 0, cwA, scA); P12_BAR(); P12_COMP(2, 1, cwB, scB);
;           P12_XQ(c, 3); P12_ISSUE(c, 3, 1, cwB, scB); P12_BAR(); P12_COMP(3, 0, cwA, scA); P12_ISSUE(cn, 0, 0, cwA, scA); P12_BAR(); P12_COMP(3, 1, cwB, scB);
	v_add_u32_e32 v16, s44, v17
	v_lshl_or_b32 v17, v16, 7, v165
	v_lshl_or_b32 v46, v16, 4, v95
	s_waitcnt lgkmcnt(1)
	v_add_u32_e32 v16, s44, v18
	global_load_dwordx4 v[80:83], v20, s[0:1]
	global_load_dwordx4 v[68:71], v17, s[0:1]
	v_lshl_or_b32 v17, v16, 7, v165
	v_lshl_or_b32 v47, v16, 4, v95
	s_waitcnt lgkmcnt(0)
	v_add_u32_e32 v16, s44, v19
	global_load_dwordx4 v[52:55], v17, s[0:1]
	v_lshl_or_b32 v17, v16, 7, v165
	v_lshl_or_b32 v60, v16, 4, v95
	ds_read_u16 v16, v93 offset:16832
	global_load_dwordx4 v[36:39], v17, s[0:1]
	v_dot4c_i32_i8_e32 v44, 0x1010101, v4
	v_dot4c_i32_i8_e32 v44, 0x1010101, v5
	v_dot4c_i32_i8_e32 v44, 0x1010101, v6
	s_waitcnt lgkmcnt(0)
	v_add_u32_e32 v16, s44, v16
	v_lshl_or_b32 v17, v16, 7, v165
	v_lshl_or_b32 v61, v16, 4, v95
	ds_read_u16 v16, v93 offset:16848
	global_load_dwordx4 v[32:35], v17, s[0:1]
	v_dot4c_i32_i8_e32 v44, 0x1010101, v7
	v_dot4c_i32_i8_e32 v44, 0x1010101, v0
	v_dot4c_i32_i8_e32 v44, 0x1010101, v1
	s_waitcnt lgkmcnt(0)
	v_add_u32_e32 v16, s44, v16
	v_lshl_or_b32 v17, v16, 7, v165
	v_lshl_or_b32 v62, v16, 4, v95
	ds_read_u16 v16, v93 offset:16864
	global_load_dwordx4 v[28:31], v17, s[0:1]
	v_dot4c_i32_i8_e32 v44, 0x1010101, v2
	v_dot4c_i32_i8_e32 v44, 0x1010101, v3
	s_waitcnt lgkmcnt(0)
	v_add_u32_e32 v16, s44, v16
	v_lshl_or_b32 v17, v16, 7, v165
	v_lshl_or_b32 v63, v16, 4, v95
	ds_read_u16 v16, v93 offset:16880
	global_load_dwordx4 v[20:23], v17, s[0:1]
	v_lshlrev_b32_e32 v84, 3, v44
	s_waitcnt vmcnt(14)
	v_and_b32_e32 v44, 0xf0f0f0f, v72
	s_waitcnt lgkmcnt(0)
	v_add_u32_e32 v76, s44, v16
	v_lshl_or_b32 v16, v76, 7, v165
	global_load_dwordx4 v[16:19], v16, s[0:1]
	v_lshl_or_b32 v76, v76, 4, v95
	v_mov_b32_e32 v46, 0
	v_dot4c_i32_i8_e32 v46, v44, v4
	v_lshrrev_b32_e32 v44, 4, v72
	v_and_b32_e32 v44, 0xf0f0f0f, v44
	v_dot4c_i32_i8_e32 v46, v44, v5
	v_and_b32_e32 v44, 0xf0f0f0f, v73
	v_mov_b32_e32 v47, 0
	v_dot4c_i32_i8_e32 v47, v44, v6
	v_lshrrev_b32_e32 v44, 4, v73
	v_and_b32_e32 v44, 0xf0f0f0f, v44
	v_dot4c_i32_i8_e32 v47, v44, v7
	v_and_b32_e32 v44, 0xf0f0f0f, v74
	v_dot4c_i32_i8_e32 v46, v44, v0
	v_lshrrev_b32_e32 v44, 4, v74
	v_and_b32_e32 v44, 0xf0f0f0f, v44
	v_dot4c_i32_i8_e32 v46, v44, v1
	v_and_b32_e32 v44, 0xf0f0f0f, v75
	v_dot4c_i32_i8_e32 v47, v44, v2
	v_lshrrev_b32_e32 v44, 4, v75
	v_and_b32_e32 v44, 0xf0f0f0f, v44
	v_dot4c_i32_i8_e32 v47, v44, v3
	s_waitcnt vmcnt(14)
	v_and_b32_e32 v44, 0xf0f0f0f, v64
	v_mov_b32_e32 v60, 0
	v_dot4c_i32_i8_e32 v60, v44, v4
	v_lshrrev_b32_e32 v44, 4, v64
	v_and_b32_e32 v44, 0xf0f0f0f, v44
	v_dot4c_i32_i8_e32 v60, v44, v5
	v_and_b32_e32 v44, 0xf0f0f0f, v65
	v_mov_b32_e32 v61, 0
	v_dot4c_i32_i8_e32 v61, v44, v6
	v_lshrrev_b32_e32 v44, 4, v65
	v_and_b32_e32 v44, 0xf0f0f0f, v44
	v_dot4c_i32_i8_e32 v61, v44, v7
	v_and_b32_e32 v44, 0xf0f0f0f, v66
	v_dot4c_i32_i8_e32 v60, v44, v0
	v_lshrrev_b32_e32 v44, 4, v66
	v_and_b32_e32 v44, 0xf0f0f0f, v44
	v_dot4c_i32_i8_e32 v60, v44, v1
	v_and_b32_e32 v44, 0xf0f0f0f, v67
	v_dot4c_i32_i8_e32 v61, v44, v2
	v_lshrrev_b32_e32 v44, 4, v67
	v_and_b32_e32 v44, 0xf0f0f0f, v44
	v_dot4c_i32_i8_e32 v61, v44, v3
	v_add_u32_e32 v46, v46, v47
	v_sub_u32_e32 v46, v46, v84
	s_waitcnt vmcnt(8)
	v_and_b32_e32 v45, 0xffff0000, v200
	v_add_u32_e32 v47, v60, v61
	v_sub_u32_e32 v60, v47, v84
	v_cvt_f32_i32_e32 v47, v46
	v_cvt_f32_i32_e32 v46, v60
	v_and_b32_e32 v44, 0xffff0000, v201
	v_pk_fma_f32 v[142:143], v[44:45], v[46:47], v[142:143]
	v_and_b32_e32 v44, 0xf0f0f0f, v56
	v_mov_b32_e32 v46, 0
	v_dot4c_i32_i8_e32 v46, v44, v4
	v_lshrrev_b32_e32 v44, 4, v56
	v_and_b32_e32 v44, 0xf0f0f0f, v44
	v_dot4c_i32_i8_e32 v46, v44, v5
	v_and_b32_e32 v44, 0xf0f0f0f, v57
	v_mov_b32_e32 v47, 0
	v_dot4c_i32_i8_e32 v47, v44, v6
	v_lshrrev_b32_e32 v44, 4, v57
	v_and_b32_e32 v44, 0xf0f0f0f, v44
	v_dot4c_i32_i8_e32 v47, v44, v7
	v_and_b32_e32 v44, 0xf0f0f0f, v58
	v_dot4c_i32_i8_e32 v46, v44, v0
	v_lshrrev_b32_e32 v44, 4, v58
	v_and_b32_e32 v44, 0xf0f0f0f, v44
	v_dot4c_i32_i8_e32 v46, v44, v1
	v_and_b32_e32 v44, 0xf0f0f0f, v59
	v_dot4c_i32_i8_e32 v47, v44, v2
	v_lshrrev_b32_e32 v44, 4, v59
	v_and_b32_e32 v44, 0xf0f0f0f, v44
	v_dot4c_i32_i8_e32 v47, v44, v3
	v_and_b32_e32 v44, 0xf0f0f0f, v48
	v_mov_b32_e32 v56, 0
	v_dot4c_i32_i8_e32 v56, v44, v4
	v_lshrrev_b32_e32 v44, 4, v48
	v_and_b32_e32 v44, 0xf0f0f0f, v44
	v_dot4c_i32_i8_e32 v56, v44, v5
	v_and_b32_e32 v44, 0xf0f0f0f, v49
	v_mov_b32_e32 v48, 0
	v_dot4c_i32_i8_e32 v48, v44, v6
	v_lshrrev_b32_e32 v44, 4, v49
	v_and_b32_e32 v44, 0xf0f0f0f, v44
	v_dot4c_i32_i8_e32 v48, v44, v7
	v_and_b32_e32 v44, 0xf0f0f0f, v50
	v_dot4c_i32_i8_e32 v56, v44, v0
	v_lshrrev_b32_e32 v44, 4, v50
	v_and_b32_e32 v44, 0xf0f0f0f, v44
	v_dot4c_i32_i8_e32 v56, v44, v1
	v_and_b32_e32 v44, 0xf0f0f0f, v51
	v_dot4c_i32_i8_e32 v48, v44, v2
	v_lshrrev_b32_e32 v44, 4, v51
	v_and_b32_e32 v44, 0xf0f0f0f, v44
	v_dot4c_i32_i8_e32 v48, v44, v3
	v_add_u32_e32 v46, v46, v47
	v_sub_u32_e32 v46, v46, v84
	s_waitcnt vmcnt(8)
; #define P12_ISSUE(c_, i_, h_, CW_, SC_) do { _Pragma("unroll") for (int bb = 0; bb < 8; ++bb) { const unsigned ro = (unsigned)(c_) * 16384u + (unsigned)EL[(i_) * 128 + ((h_) * 8 + bb) * 8 + g8]; \
;         CW_[bb] = *(const v4u*)(U4 + (size_t)(ro * 128u + 16u * (unsigned)k8)); SC_[bb] = USS[(size_t)(ro * 8u + (unsigned)k8)]; } } while (0)
; #define P12_COMP(i_, h_, CW_, SC_) do { _Pragma("unroll") for (int bb = 0; bb < 8; ++bb) { int a0 = 0, a1 = 0; P12_U4(CW_[bb].x, xa.x, xa.y, a0); P12_U4(CW_[bb].y, xa.z, xa.w, a1); P12_U4(CW_[bb].z, xb.x, xb.y, a0); P12_U4(CW_[bb].w, xb.z, xb.w, a1); \
;         psum[(i_)][(h_) * 8 + bb] += __uint_as_float(SC_[bb] << 16) * (float)((a0 + a1) - xo); } } while (0)
; #define P12_BAR() asm volatile("" ::: "memory")
; __device__ __forceinline__ void p12_peer(Frame& F) {
;     ...
;     { v4u cwA[8], cwB[8]; unsigned scA[8], scB[8]; v4u xa, xb; int xo;
;       P12_ISSUE(0, 0, 0, cwA, scA);
; _Pragma("nounroll")
;       for (int c = 0; c < 16; ++c) { const int cn = c + 1 < 16 ? c + 1 : 15;
;           P12_XQ(c, 0); P12_ISSUE(c, 0, 1, cwB, scB); P12_BAR(); P12_COMP(0, 0, cwA, scA); P12_ISSUE(c, 1, 0, cwA, scA); P12_BAR(); P12_COMP(0, 1, cwB, scB);
;           P12_XQ(c, 1); P12_ISSUE(c, 1, 1, cwB, scB); P12_BAR(); P12_COMP(1, 0, cwA, scA); P12_ISSUE(c, 2, 0, cwA, scA); P12_BAR(); P12_COMP(1, 1, cwB, scB);
;           P12_XQ(c, 2); P12_ISSUE(c, 2, 1, cwB, scB); P12_BAR(); P12_COMP(2, 0, cwA, scA); P12_ISSUE(c, 3, 0, cwA, scA); P12_BAR(); P12_COMP(2, 1, cwB, scB);
;           P12_XQ(c, 3); P12_ISSUE(c, 3, 1, cwB, scB); P12_BAR(); P12_COMP(3, 0, cwA, scA); P12_ISSUE(cn, 0, 0, cwA, scA); P12_BAR(); P12_COMP(3, 1, cwB, scB);
	v_and_b32_e32 v45, 0xffff0000, v202
	v_add_u32_e32 v47, v56, v48
	v_sub_u32_e32 v48, v47, v84
	v_cvt_f32_i32_e32 v47, v46
	v_cvt_f32_i32_e32 v46, v48
	v_and_b32_e32 v44, 0xffff0000, v203
	v_pk_fma_f32 v[140:141], v[44:45], v[46:47], v[140:141]
	v_and_b32_e32 v44, 0xf0f0f0f, v40
	v_mov_b32_e32 v45, 0
	v_lshrrev_b32_e32 v40, 4, v40
	v_dot4c_i32_i8_e32 v45, v44, v4
	v_and_b32_e32 v40, 0xf0f0f0f, v40
	v_dot4c_i32_i8_e32 v45, v40, v5
	v_and_b32_e32 v40, 0xf0f0f0f, v41
	v_mov_b32_e32 v44, 0
	v_dot4c_i32_i8_e32 v44, v40, v6
	v_lshrrev_b32_e32 v40, 4, v41
	v_and_b32_e32 v40, 0xf0f0f0f, v40
	v_dot4c_i32_i8_e32 v44, v40, v7
	v_and_b32_e32 v40, 0xf0f0f0f, v42
	v_dot4c_i32_i8_e32 v45, v40, v0
	v_lshrrev_b32_e32 v40, 4, v42
	v_and_b32_e32 v40, 0xf0f0f0f, v40
	v_dot4c_i32_i8_e32 v45, v40, v1
	v_and_b32_e32 v40, 0xf0f0f0f, v43
	v_dot4c_i32_i8_e32 v44, v40, v2
	v_lshrrev_b32_e32 v40, 4, v43
	v_and_b32_e32 v40, 0xf0f0f0f, v40
	v_dot4c_i32_i8_e32 v44, v40, v3
	v_and_b32_e32 v40, 0xf0f0f0f, v24
	v_mov_b32_e32 v41, 0
	v_lshrrev_b32_e32 v24, 4, v24
	v_dot4c_i32_i8_e32 v41, v40, v4
	v_and_b32_e32 v24, 0xf0f0f0f, v24
	v_dot4c_i32_i8_e32 v41, v24, v5
	v_and_b32_e32 v24, 0xf0f0f0f, v25
	v_mov_b32_e32 v40, 0
	v_dot4c_i32_i8_e32 v40, v24, v6
	v_lshrrev_b32_e32 v24, 4, v25
	v_and_b32_e32 v24, 0xf0f0f0f, v24
	v_dot4c_i32_i8_e32 v40, v24, v7
	v_and_b32_e32 v24, 0xf0f0f0f, v26
	v_dot4c_i32_i8_e32 v41, v24, v0
	v_lshrrev_b32_e32 v24, 4, v26
	v_and_b32_e32 v24, 0xf0f0f0f, v24
	v_dot4c_i32_i8_e32 v41, v24, v1
	v_and_b32_e32 v24, 0xf0f0f0f, v27
	v_dot4c_i32_i8_e32 v40, v24, v2
	v_lshrrev_b32_e32 v24, 4, v27
	v_and_b32_e32 v24, 0xf0f0f0f, v24
	v_dot4c_i32_i8_e32 v40, v24, v3
	v_add_u32_e32 v26, v45, v44
	v_sub_u32_e32 v26, v26, v84
	s_waitcnt vmcnt(8)
	v_and_b32_e32 v25, 0xffff0000, v204
	v_add_u32_e32 v27, v41, v40
	v_sub_u32_e32 v40, v27, v84
	v_cvt_f32_i32_e32 v27, v26
	v_cvt_f32_i32_e32 v26, v40
	v_and_b32_e32 v24, 0xffff0000, v205
	v_pk_fma_f32 v[138:139], v[24:25], v[26:27], v[138:139]
	v_and_b32_e32 v24, 0xf0f0f0f, v12
	v_mov_b32_e32 v25, 0
	v_lshrrev_b32_e32 v12, 4, v12
	v_dot4c_i32_i8_e32 v25, v24, v4
	v_and_b32_e32 v12, 0xf0f0f0f, v12
	v_dot4c_i32_i8_e32 v25, v12, v5
	v_and_b32_e32 v12, 0xf0f0f0f, v13
	v_mov_b32_e32 v24, 0
	v_dot4c_i32_i8_e32 v24, v12, v6
	v_lshrrev_b32_e32 v12, 4, v13
	v_and_b32_e32 v12, 0xf0f0f0f, v12
	v_dot4c_i32_i8_e32 v24, v12, v7
	v_and_b32_e32 v12, 0xf0f0f0f, v14
	v_dot4c_i32_i8_e32 v25, v12, v0
	v_lshrrev_b32_e32 v12, 4, v14
	v_and_b32_e32 v12, 0xf0f0f0f, v12
	v_dot4c_i32_i8_e32 v25, v12, v1
	v_and_b32_e32 v12, 0xf0f0f0f, v15
	v_dot4c_i32_i8_e32 v24, v12, v2
	v_lshrrev_b32_e32 v12, 4, v15
	v_and_b32_e32 v12, 0xf0f0f0f, v12
	v_dot4c_i32_i8_e32 v24, v12, v3
	v_and_b32_e32 v12, 0xf0f0f0f, v8
	v_mov_b32_e32 v13, 0
	v_lshrrev_b32_e32 v8, 4, v8
	v_dot4c_i32_i8_e32 v13, v12, v4
	v_and_b32_e32 v8, 0xf0f0f0f, v8
	v_dot4c_i32_i8_e32 v13, v8, v5
	v_and_b32_e32 v8, 0xf0f0f0f, v9
	v_mov_b32_e32 v12, 0
	v_dot4c_i32_i8_e32 v12, v8, v6
	v_lshrrev_b32_e32 v8, 4, v9
	v_and_b32_e32 v8, 0xf0f0f0f, v8
	v_dot4c_i32_i8_e32 v12, v8, v7
	v_and_b32_e32 v8, 0xf0f0f0f, v10
	v_dot4c_i32_i8_e32 v13, v8, v0
	v_lshrrev_b32_e32 v8, 4, v10
	v_and_b32_e32 v8, 0xf0f0f0f, v8
	v_dot4c_i32_i8_e32 v13, v8, v1
	v_and_b32_e32 v8, 0xf0f0f0f, v11
	v_dot4c_i32_i8_e32 v12, v8, v2
	v_lshrrev_b32_e32 v8, 4, v11
	v_and_b32_e32 v8, 0xf0f0f0f, v8
	v_dot4c_i32_i8_e32 v12, v8, v3
	v_add_u32_e32 v10, v25, v24
	v_sub_u32_e32 v10, v10, v84
	s_waitcnt vmcnt(8)
	v_and_b32_e32 v9, 0xffff0000, v206
	v_add_u32_e32 v11, v13, v12
	v_sub_u32_e32 v12, v11, v84
	v_cvt_f32_i32_e32 v11, v10
	v_cvt_f32_i32_e32 v10, v12
	v_and_b32_e32 v8, 0xffff0000, v207
	v_pk_fma_f32 v[136:137], v[8:9], v[10:11], v[136:137]
	ds_read_u16 v8, v93 offset:16896
	ds_read_u16 v9, v93 offset:16912
	ds_read_u16 v10, v93 offset:16928
	ds_read_u16 v11, v93 offset:16944
	s_waitcnt lgkmcnt(3)
	v_add_u32_e32 v8, s44, v8
	v_lshl_or_b32 v12, v8, 7, v165
	v_lshl_or_b32 v40, v8, 4, v95
	s_waitcnt lgkmcnt(2)
	v_add_u32_e32 v8, s44, v9
	v_lshl_or_b32 v9, v8, 7, v165
	v_lshl_or_b32 v41, v8, 4, v95
	s_waitcnt lgkmcnt(1)
	v_add_u32_e32 v8, s44, v10
	global_load_dwordx4 v[76:79], v12, s[0:1]
	global_load_dwordx4 v[72:75], v9, s[0:1]
	v_lshl_or_b32 v9, v8, 7, v165
	v_lshl_or_b32 v42, v8, 4, v95
	s_waitcnt lgkmcnt(0)
	v_add_u32_e32 v8, s44, v11
	global_load_dwordx4 v[60:63], v9, s[0:1]
	v_lshl_or_b32 v9, v8, 7, v165
	v_lshl_or_b32 v43, v8, 4, v95
	ds_read_u16 v8, v93 offset:16960
	global_load_dwordx4 v[56:59], v9, s[0:1]
	s_waitcnt lgkmcnt(0)
	v_add_u32_e32 v8, s44, v8
	v_lshl_or_b32 v9, v8, 7, v165
	v_lshl_or_b32 v48, v8, 4, v95
	ds_read_u16 v8, v93 offset:16976
	global_load_dwordx4 v[44:47], v9, s[0:1]
	s_waitcnt lgkmcnt(0)
	v_add_u32_e32 v8, s44, v8
	v_lshl_or_b32 v9, v8, 7, v165
	v_lshl_or_b32 v49, v8, 4, v95
	ds_read_u16 v8, v93 offset:16992
	global_load_dwordx4 v[24:27], v9, s[0:1]
	s_waitcnt lgkmcnt(0)
	v_add_u32_e32 v8, s44, v8
	v_lshl_or_b32 v9, v8, 7, v165
	v_lshl_or_b32 v50, v8, 4, v95
	ds_read_u16 v8, v93 offset:17008
	global_load_dwordx4 v[12:15], v9, s[0:1]
	s_waitcnt lgkmcnt(0)
	v_add_u32_e32 v51, s44, v8
	v_lshl_or_b32 v8, v51, 7, v165
	global_load_dwordx4 v[8:11], v8, s[0:1]
	v_lshl_or_b32 v51, v51, 4, v95
	s_waitcnt vmcnt(15)
	v_and_b32_e32 v40, 0xf0f0f0f, v80
	v_mov_b32_e32 v42, 0
	v_dot4c_i32_i8_e32 v42, v40, v4
	v_lshrrev_b32_e32 v40, 4, v80
	v_and_b32_e32 v40, 0xf0f0f0f, v40
	v_dot4c_i32_i8_e32 v42, v40, v5
	v_and_b32_e32 v40, 0xf0f0f0f, v81
	v_mov_b32_e32 v43, 0
	v_dot4c_i32_i8_e32 v43, v40, v6
	v_lshrrev_b32_e32 v40, 4, v81
	v_and_b32_e32 v40, 0xf0f0f0f, v40
	v_dot4c_i32_i8_e32 v43, v40, v7
	v_and_b32_e32 v40, 0xf0f0f0f, v82
	v_dot4c_i32_i8_e32 v42, v40, v0
	v_lshrrev_b32_e32 v40, 4, v82
	v_and_b32_e32 v40, 0xf0f0f0f, v40
	v_dot4c_i32_i8_e32 v42, v40, v1
	v_and_b32_e32 v40, 0xf0f0f0f, v83
	v_dot4c_i32_i8_e32 v43, v40, v2
	v_lshrrev_b32_e32 v40, 4, v83
	v_and_b32_e32 v40, 0xf0f0f0f, v40
	v_dot4c_i32_i8_e32 v43, v40, v3
	s_waitcnt vmcnt(14)
; #define P12_ISSUE(c_, i_, h_, CW_, SC_) do { _Pragma("unroll") for (int bb = 0; bb < 8; ++bb) { const unsigned ro = (unsigned)(c_) * 16384u + (unsigned)EL[(i_) * 128 + ((h_) * 8 + bb) * 8 + g8]; \
;         CW_[bb] = *(const v4u*)(U4 + (size_t)(ro * 128u + 16u * (unsigned)k8)); SC_[bb] = USS[(size_t)(ro * 8u + (unsigned)k8)]; } } while (0)
; #define P12_COMP(i_, h_, CW_, SC_) do { _Pragma("unroll") for (int bb = 0; bb < 8; ++bb) { int a0 = 0, a1 = 0; P12_U4(CW_[bb].x, xa.x, xa.y, a0); P12_U4(CW_[bb].y, xa.z, xa.w, a1); P12_U4(CW_[bb].z, xb.x, xb.y, a0); P12_U4(CW_[bb].w, xb.z, xb.w, a1); \
;         psum[(i_)][(h_) * 8 + bb] += __uint_as_float(SC_[bb] << 16) * (float)((a0 + a1) - xo); } } while (0)
; #define P12_BAR() asm volatile("" ::: "memory")
; __device__ __forceinline__ void p12_peer(Frame& F) {
;     ...
;     { v4u cwA[8], cwB[8]; unsigned scA[8], scB[8]; v4u xa, xb; int xo;
;       P12_ISSUE(0, 0, 0, cwA, scA);
; _Pragma("nounroll")
;       for (int c = 0; c < 16; ++c) { const int cn = c + 1 < 16 ? c + 1 : 15;
;           P12_XQ(c, 0); P12_ISSUE(c, 0, 1, cwB, scB); P12_BAR(); P12_COMP(0, 0, cwA, scA); P12_ISSUE(c, 1, 0, cwA, scA); P12_BAR(); P12_COMP(0, 1, cwB, scB);
;           P12_XQ(c, 1); P12_ISSUE(c, 1, 1, cwB, scB); P12_BAR(); P12_COMP(1, 0, cwA, scA); P12_ISSUE(c, 2, 0, cwA, scA); P12_BAR(); P12_COMP(1, 1, cwB, scB);
;           P12_XQ(c, 2); P12_ISSUE(c, 2, 1, cwB, scB); P12_BAR(); P12_COMP(2, 0, cwA, scA); P12_ISSUE(c, 3, 0, cwA, scA); P12_BAR(); P12_COMP(2, 1, cwB, scB);
;           P12_XQ(c, 3); P12_ISSUE(c, 3, 1, cwB, scB); P12_BAR(); P12_COMP(3, 0, cwA, scA); P12_ISSUE(cn, 0, 0, cwA, scA); P12_BAR(); P12_COMP(3, 1, cwB, scB);
	v_and_b32_e32 v40, 0xf0f0f0f, v68
	v_mov_b32_e32 v48, 0
	v_dot4c_i32_i8_e32 v48, v40, v4
	v_lshrrev_b32_e32 v40, 4, v68
	v_and_b32_e32 v40, 0xf0f0f0f, v40
	v_dot4c_i32_i8_e32 v48, v40, v5
	v_and_b32_e32 v40, 0xf0f0f0f, v69
	v_mov_b32_e32 v49, 0
	v_dot4c_i32_i8_e32 v49, v40, v6
	v_lshrrev_b32_e32 v40, 4, v69
	v_and_b32_e32 v40, 0xf0f0f0f, v40
	v_dot4c_i32_i8_e32 v49, v40, v7
	v_and_b32_e32 v40, 0xf0f0f0f, v70
	v_dot4c_i32_i8_e32 v48, v40, v0
	v_lshrrev_b32_e32 v40, 4, v70
	v_and_b32_e32 v40, 0xf0f0f0f, v40
	v_dot4c_i32_i8_e32 v48, v40, v1
	v_and_b32_e32 v40, 0xf0f0f0f, v71
	v_dot4c_i32_i8_e32 v49, v40, v2
	v_lshrrev_b32_e32 v40, 4, v71
	v_and_b32_e32 v40, 0xf0f0f0f, v40
	v_dot4c_i32_i8_e32 v49, v40, v3
	v_add_u32_e32 v42, v42, v43
	v_sub_u32_e32 v42, v42, v84
	s_waitcnt vmcnt(8)
	v_and_b32_e32 v41, 0xffff0000, v208
	v_sub_u32_e32 v43, v49, v84
	v_add_u32_e32 v48, v43, v48
	v_cvt_f32_i32_e32 v43, v42
	v_cvt_f32_i32_e32 v42, v48
	v_and_b32_e32 v40, 0xffff0000, v209
	v_pk_fma_f32 v[134:135], v[40:41], v[42:43], v[134:135]
	v_and_b32_e32 v40, 0xf0f0f0f, v52
	v_mov_b32_e32 v41, 0
	v_dot4c_i32_i8_e32 v41, v40, v4
	v_lshrrev_b32_e32 v40, 4, v52
	v_and_b32_e32 v40, 0xf0f0f0f, v40
	v_dot4c_i32_i8_e32 v41, v40, v5
	v_and_b32_e32 v40, 0xf0f0f0f, v53
	v_mov_b32_e32 v42, 0
	v_dot4c_i32_i8_e32 v42, v40, v6
	v_lshrrev_b32_e32 v40, 4, v53
	v_and_b32_e32 v40, 0xf0f0f0f, v40
	v_dot4c_i32_i8_e32 v42, v40, v7
	v_and_b32_e32 v40, 0xf0f0f0f, v54
	v_dot4c_i32_i8_e32 v41, v40, v0
	v_lshrrev_b32_e32 v40, 4, v54
	v_and_b32_e32 v40, 0xf0f0f0f, v40
	v_dot4c_i32_i8_e32 v41, v40, v1
	v_and_b32_e32 v40, 0xf0f0f0f, v55
	v_dot4c_i32_i8_e32 v42, v40, v2
	v_lshrrev_b32_e32 v40, 4, v55
	v_and_b32_e32 v40, 0xf0f0f0f, v40
	v_dot4c_i32_i8_e32 v42, v40, v3
	v_and_b32_e32 v40, 0xf0f0f0f, v36
	v_mov_b32_e32 v43, 0
	v_lshrrev_b32_e32 v36, 4, v36
	v_dot4c_i32_i8_e32 v43, v40, v4
	v_and_b32_e32 v36, 0xf0f0f0f, v36
	v_dot4c_i32_i8_e32 v43, v36, v5
	v_and_b32_e32 v36, 0xf0f0f0f, v37
	v_mov_b32_e32 v40, 0
	v_dot4c_i32_i8_e32 v40, v36, v6
	v_lshrrev_b32_e32 v36, 4, v37
	v_and_b32_e32 v36, 0xf0f0f0f, v36
	v_dot4c_i32_i8_e32 v40, v36, v7
	v_and_b32_e32 v36, 0xf0f0f0f, v38
	v_dot4c_i32_i8_e32 v43, v36, v0
	v_lshrrev_b32_e32 v36, 4, v38
	v_and_b32_e32 v36, 0xf0f0f0f, v36
	v_dot4c_i32_i8_e32 v43, v36, v1
	v_and_b32_e32 v36, 0xf0f0f0f, v39
	v_dot4c_i32_i8_e32 v40, v36, v2
	v_lshrrev_b32_e32 v36, 4, v39
	v_and_b32_e32 v36, 0xf0f0f0f, v36
	v_dot4c_i32_i8_e32 v40, v36, v3
	v_sub_u32_e32 v38, v42, v84
	v_add_u32_e32 v38, v38, v41
	s_waitcnt vmcnt(8)
	v_and_b32_e32 v37, 0xffff0000, v210
	v_sub_u32_e32 v39, v40, v84
	v_add_u32_e32 v40, v39, v43
	v_cvt_f32_i32_e32 v39, v38
	v_cvt_f32_i32_e32 v38, v40
	v_and_b32_e32 v36, 0xffff0000, v211
	v_pk_fma_f32 v[132:133], v[36:37], v[38:39], v[132:133]
	v_and_b32_e32 v36, 0xf0f0f0f, v32
	v_mov_b32_e32 v37, 0
	v_lshrrev_b32_e32 v32, 4, v32
	v_dot4c_i32_i8_e32 v37, v36, v4
	v_and_b32_e32 v32, 0xf0f0f0f, v32
	v_dot4c_i32_i8_e32 v37, v32, v5
	v_and_b32_e32 v32, 0xf0f0f0f, v33
	v_mov_b32_e32 v36, 0
	v_dot4c_i32_i8_e32 v36, v32, v6
	v_lshrrev_b32_e32 v32, 4, v33
	v_and_b32_e32 v32, 0xf0f0f0f, v32
	v_dot4c_i32_i8_e32 v36, v32, v7
	v_and_b32_e32 v32, 0xf0f0f0f, v34
	v_dot4c_i32_i8_e32 v37, v32, v0
	v_lshrrev_b32_e32 v32, 4, v34
	v_and_b32_e32 v32, 0xf0f0f0f, v32
	v_dot4c_i32_i8_e32 v37, v32, v1
	v_and_b32_e32 v32, 0xf0f0f0f, v35
	v_dot4c_i32_i8_e32 v36, v32, v2
	v_lshrrev_b32_e32 v32, 4, v35
	v_and_b32_e32 v32, 0xf0f0f0f, v32
	v_dot4c_i32_i8_e32 v36, v32, v3
	v_and_b32_e32 v32, 0xf0f0f0f, v28
	v_mov_b32_e32 v33, 0
	v_lshrrev_b32_e32 v28, 4, v28
	v_dot4c_i32_i8_e32 v33, v32, v4
	v_and_b32_e32 v28, 0xf0f0f0f, v28
	v_dot4c_i32_i8_e32 v33, v28, v5
	v_and_b32_e32 v28, 0xf0f0f0f, v29
	v_mov_b32_e32 v32, 0
	v_dot4c_i32_i8_e32 v32, v28, v6
	v_lshrrev_b32_e32 v28, 4, v29
	v_and_b32_e32 v28, 0xf0f0f0f, v28
	v_dot4c_i32_i8_e32 v32, v28, v7
	v_and_b32_e32 v28, 0xf0f0f0f, v30
	v_dot4c_i32_i8_e32 v33, v28, v0
	v_lshrrev_b32_e32 v28, 4, v30
	v_and_b32_e32 v28, 0xf0f0f0f, v28
	v_dot4c_i32_i8_e32 v33, v28, v1
	v_and_b32_e32 v28, 0xf0f0f0f, v31
	v_dot4c_i32_i8_e32 v32, v28, v2
	v_lshrrev_b32_e32 v28, 4, v31
	v_and_b32_e32 v28, 0xf0f0f0f, v28
	v_dot4c_i32_i8_e32 v32, v28, v3
	v_sub_u32_e32 v30, v36, v84
	v_add_u32_e32 v30, v30, v37
	s_waitcnt vmcnt(8)
	v_and_b32_e32 v29, 0xffff0000, v212
	v_sub_u32_e32 v31, v32, v84
	v_add_u32_e32 v32, v31, v33
	v_cvt_f32_i32_e32 v31, v30
	v_cvt_f32_i32_e32 v30, v32
	v_and_b32_e32 v28, 0xffff0000, v213
	v_pk_fma_f32 v[130:131], v[28:29], v[30:31], v[130:131]
	v_and_b32_e32 v28, 0xf0f0f0f, v20
	v_mov_b32_e32 v29, 0
	v_lshrrev_b32_e32 v20, 4, v20
	v_dot4c_i32_i8_e32 v29, v28, v4
	v_and_b32_e32 v20, 0xf0f0f0f, v20
	v_dot4c_i32_i8_e32 v29, v20, v5
	v_and_b32_e32 v20, 0xf0f0f0f, v21
	v_mov_b32_e32 v28, 0
	v_dot4c_i32_i8_e32 v28, v20, v6
	v_lshrrev_b32_e32 v20, 4, v21
	v_and_b32_e32 v20, 0xf0f0f0f, v20
	v_dot4c_i32_i8_e32 v28, v20, v7
	v_and_b32_e32 v20, 0xf0f0f0f, v22
	v_dot4c_i32_i8_e32 v29, v20, v0
	v_lshrrev_b32_e32 v20, 4, v22
	v_and_b32_e32 v20, 0xf0f0f0f, v20
	v_dot4c_i32_i8_e32 v29, v20, v1
	v_and_b32_e32 v20, 0xf0f0f0f, v23
	v_dot4c_i32_i8_e32 v28, v20, v2
	v_lshrrev_b32_e32 v20, 4, v23
	v_and_b32_e32 v20, 0xf0f0f0f, v20
	v_dot4c_i32_i8_e32 v28, v20, v3
	v_and_b32_e32 v20, 0xf0f0f0f, v16
	v_mov_b32_e32 v21, 0
	v_dot4c_i32_i8_e32 v21, v20, v4
	v_lshrrev_b32_e32 v4, 4, v16
	v_and_b32_e32 v4, 0xf0f0f0f, v4
	v_dot4c_i32_i8_e32 v21, v4, v5
	v_and_b32_e32 v4, 0xf0f0f0f, v17
	v_mov_b32_e32 v5, 0
	v_dot4c_i32_i8_e32 v5, v4, v6
	v_lshrrev_b32_e32 v4, 4, v17
	v_and_b32_e32 v4, 0xf0f0f0f, v4
	v_dot4c_i32_i8_e32 v5, v4, v7
	v_and_b32_e32 v4, 0xf0f0f0f, v18
	v_dot4c_i32_i8_e32 v21, v4, v0
	v_lshrrev_b32_e32 v0, 4, v18
	v_and_b32_e32 v0, 0xf0f0f0f, v0
	v_dot4c_i32_i8_e32 v21, v0, v1
	v_and_b32_e32 v0, 0xf0f0f0f, v19
	v_dot4c_i32_i8_e32 v5, v0, v2
	v_lshrrev_b32_e32 v0, 4, v19
	v_and_b32_e32 v0, 0xf0f0f0f, v0
	v_dot4c_i32_i8_e32 v5, v0, v3
	v_sub_u32_e32 v2, v28, v84
	v_add_u32_e32 v2, v2, v29
	s_waitcnt vmcnt(8)
; #define P12_ISSUE(c_, i_, h_, CW_, SC_) do { _Pragma("unroll") for (int bb = 0; bb < 8; ++bb) { const unsigned ro = (unsigned)(c_) * 16384u + (unsigned)EL[(i_) * 128 + ((h_) * 8 + bb) * 8 + g8]; \
;         CW_[bb] = *(const v4u*)(U4 + (size_t)(ro * 128u + 16u * (unsigned)k8)); SC_[bb] = USS[(size_t)(ro * 8u + (unsigned)k8)]; } } while (0)
; #define P12_COMP(i_, h_, CW_, SC_) do { _Pragma("unroll") for (int bb = 0; bb < 8; ++bb) { int a0 = 0, a1 = 0; P12_U4(CW_[bb].x, xa.x, xa.y, a0); P12_U4(CW_[bb].y, xa.z, xa.w, a1); P12_U4(CW_[bb].z, xb.x, xb.y, a0); P12_U4(CW_[bb].w, xb.z, xb.w, a1); \
;         psum[(i_)][(h_) * 8 + bb] += __uint_as_float(SC_[bb] << 16) * (float)((a0 + a1) - xo); } } while (0)
; #define P12_BAR() asm volatile("" ::: "memory")
; __device__ __forceinline__ void p12_peer(Frame& F) {
;     ...
;     { v4u cwA[8], cwB[8]; unsigned scA[8], scB[8]; v4u xa, xb; int xo;
;       P12_ISSUE(0, 0, 0, cwA, scA);
; _Pragma("nounroll")
;       for (int c = 0; c < 16; ++c) { const int cn = c + 1 < 16 ? c + 1 : 15;
;           P12_XQ(c, 0); P12_ISSUE(c, 0, 1, cwB, scB); P12_BAR(); P12_COMP(0, 0, cwA, scA); P12_ISSUE(c, 1, 0, cwA, scA); P12_BAR(); P12_COMP(0, 1, cwB, scB);
;           P12_XQ(c, 1); P12_ISSUE(c, 1, 1, cwB, scB); P12_BAR(); P12_COMP(1, 0, cwA, scA); P12_ISSUE(c, 2, 0, cwA, scA); P12_BAR(); P12_COMP(1, 1, cwB, scB);
;           P12_XQ(c, 2); P12_ISSUE(c, 2, 1, cwB, scB); P12_BAR(); P12_COMP(2, 0, cwA, scA); P12_ISSUE(c, 3, 0, cwA, scA); P12_BAR(); P12_COMP(2, 1, cwB, scB);
;           P12_XQ(c, 3); P12_ISSUE(c, 3, 1, cwB, scB); P12_BAR(); P12_COMP(3, 0, cwA, scA); P12_ISSUE(cn, 0, 0, cwA, scA); P12_BAR(); P12_COMP(3, 1, cwB, scB);
	v_and_b32_e32 v1, 0xffff0000, v214
	v_sub_u32_e32 v3, v5, v84
	v_add_u32_e32 v4, v3, v21
	v_cvt_f32_i32_e32 v3, v2
	v_cvt_f32_i32_e32 v2, v4
	v_and_b32_e32 v0, 0xffff0000, v215
	ds_read_b128 v[32:35], v166 offset:8192
	ds_read_b128 v[28:31], v166 offset:8208
	v_pk_fma_f32 v[128:129], v[0:1], v[2:3], v[128:129]
	ds_read_u16 v1, v93 offset:17024
	ds_read_u16 v2, v93 offset:17040
	ds_read_u16 v3, v93 offset:17056
	ds_read_u16 v4, v93 offset:17072
	v_mov_b32_e32 v0, 0
	s_waitcnt lgkmcnt(3)
	v_add_u32_e32 v1, s44, v1
	v_lshl_or_b32 v5, v1, 7, v165
	s_waitcnt lgkmcnt(2)
	v_add_u32_e32 v2, s44, v2
	global_load_dwordx4 v[84:87], v5, s[0:1]
	v_lshl_or_b32 v5, v2, 7, v165
	s_waitcnt lgkmcnt(1)
	v_add_u32_e32 v3, s44, v3
	global_load_dwordx4 v[80:83], v5, s[0:1]
	v_lshl_or_b32 v5, v3, 7, v165
	s_waitcnt lgkmcnt(0)
	v_add_u32_e32 v4, s44, v4
	global_load_dwordx4 v[68:71], v5, s[0:1]
	v_lshl_or_b32 v5, v4, 7, v165
	global_load_dwordx4 v[64:67], v5, s[0:1]
	ds_read_u16 v5, v93 offset:17088
	v_dot4c_i32_i8_e32 v0, 0x1010101, v32
	v_dot4c_i32_i8_e32 v0, 0x1010101, v33
	v_dot4c_i32_i8_e32 v0, 0x1010101, v34
	v_dot4c_i32_i8_e32 v0, 0x1010101, v35
	s_waitcnt lgkmcnt(0)
	v_add_u32_e32 v5, s44, v5
	v_lshl_or_b32 v6, v5, 7, v165
	global_load_dwordx4 v[52:55], v6, s[0:1]
	ds_read_u16 v6, v93 offset:17104
	v_dot4c_i32_i8_e32 v0, 0x1010101, v28
	v_dot4c_i32_i8_e32 v0, 0x1010101, v29
	v_dot4c_i32_i8_e32 v0, 0x1010101, v30
	v_dot4c_i32_i8_e32 v0, 0x1010101, v31
	s_waitcnt lgkmcnt(0)
	v_add_u32_e32 v6, s44, v6
	v_lshl_or_b32 v7, v6, 7, v165
	global_load_dwordx4 v[48:51], v7, s[0:1]
	ds_read_u16 v7, v93 offset:17120
	v_lshl_or_b32 v2, v2, 4, v95
	v_lshl_or_b32 v1, v1, 4, v95
	v_lshl_or_b32 v3, v3, 4, v95
	v_lshl_or_b32 v4, v4, 4, v95
	s_waitcnt lgkmcnt(0)
	v_add_u32_e32 v7, s44, v7
	v_lshl_or_b32 v16, v7, 7, v165
	global_load_dwordx4 v[40:43], v16, s[0:1]
	ds_read_u16 v16, v93 offset:17136
	v_lshl_or_b32 v5, v5, 4, v95
	v_lshl_or_b32 v6, v6, 4, v95
	v_lshl_or_b32 v7, v7, 4, v95
	v_lshlrev_b32_e32 v169, 3, v0
	s_waitcnt lgkmcnt(0)
	v_add_u32_e32 v16, s44, v16
	v_lshl_or_b32 v17, v16, 7, v165
	global_load_dwordx4 v[36:39], v17, s[0:1]
	v_lshl_or_b32 v16, v16, 4, v95
	s_waitcnt vmcnt(15)
	v_and_b32_e32 v0, 0xf0f0f0f, v76
	v_mov_b32_e32 v2, 0
	v_dot4c_i32_i8_e32 v2, v0, v32
	v_lshrrev_b32_e32 v0, 4, v76
	v_and_b32_e32 v0, 0xf0f0f0f, v0
	v_dot4c_i32_i8_e32 v2, v0, v33
	v_and_b32_e32 v0, 0xf0f0f0f, v77
	v_mov_b32_e32 v3, 0
	v_dot4c_i32_i8_e32 v3, v0, v34
	v_lshrrev_b32_e32 v0, 4, v77
	v_and_b32_e32 v0, 0xf0f0f0f, v0
	v_dot4c_i32_i8_e32 v3, v0, v35
	v_and_b32_e32 v0, 0xf0f0f0f, v78
	v_dot4c_i32_i8_e32 v2, v0, v28
	v_lshrrev_b32_e32 v0, 4, v78
	v_and_b32_e32 v0, 0xf0f0f0f, v0
	v_dot4c_i32_i8_e32 v2, v0, v29
	v_and_b32_e32 v0, 0xf0f0f0f, v79
	v_dot4c_i32_i8_e32 v3, v0, v30
	v_lshrrev_b32_e32 v0, 4, v79
	v_and_b32_e32 v0, 0xf0f0f0f, v0
	v_dot4c_i32_i8_e32 v3, v0, v31
	s_waitcnt vmcnt(14)
	v_and_b32_e32 v0, 0xf0f0f0f, v72
	v_mov_b32_e32 v4, 0
	v_dot4c_i32_i8_e32 v4, v0, v32
	v_lshrrev_b32_e32 v0, 4, v72
	v_and_b32_e32 v0, 0xf0f0f0f, v0
	v_dot4c_i32_i8_e32 v4, v0, v33
	v_and_b32_e32 v0, 0xf0f0f0f, v73
	v_mov_b32_e32 v5, 0
	v_dot4c_i32_i8_e32 v5, v0, v34
	v_lshrrev_b32_e32 v0, 4, v73
	v_and_b32_e32 v0, 0xf0f0f0f, v0
	v_dot4c_i32_i8_e32 v5, v0, v35
	v_and_b32_e32 v0, 0xf0f0f0f, v74
	v_dot4c_i32_i8_e32 v4, v0, v28
	v_lshrrev_b32_e32 v0, 4, v74
	v_and_b32_e32 v0, 0xf0f0f0f, v0
	v_dot4c_i32_i8_e32 v4, v0, v29
	v_and_b32_e32 v0, 0xf0f0f0f, v75
	v_dot4c_i32_i8_e32 v5, v0, v30
	v_lshrrev_b32_e32 v0, 4, v75
	v_and_b32_e32 v0, 0xf0f0f0f, v0
	v_dot4c_i32_i8_e32 v5, v0, v31
	v_add_u32_e32 v2, v2, v3
	v_sub_u32_e32 v2, v2, v169
	s_waitcnt vmcnt(8)
	v_and_b32_e32 v1, 0xffff0000, v216
	v_add_u32_e32 v3, v4, v5
	v_sub_u32_e32 v4, v3, v169
	v_cvt_f32_i32_e32 v3, v2
	v_cvt_f32_i32_e32 v2, v4
	v_and_b32_e32 v0, 0xffff0000, v217
	v_mov_b32_e32 v4, 0
	v_mov_b32_e32 v5, 0
	v_pk_fma_f32 v[126:127], v[0:1], v[2:3], v[126:127]
	v_and_b32_e32 v0, 0xf0f0f0f, v60
	v_mov_b32_e32 v2, 0
	v_dot4c_i32_i8_e32 v2, v0, v32
	v_lshrrev_b32_e32 v0, 4, v60
	v_and_b32_e32 v0, 0xf0f0f0f, v0
	v_dot4c_i32_i8_e32 v2, v0, v33
	v_and_b32_e32 v0, 0xf0f0f0f, v61
	v_mov_b32_e32 v3, 0
	v_dot4c_i32_i8_e32 v3, v0, v34
	v_lshrrev_b32_e32 v0, 4, v61
	v_and_b32_e32 v0, 0xf0f0f0f, v0
	v_dot4c_i32_i8_e32 v3, v0, v35
	v_and_b32_e32 v0, 0xf0f0f0f, v62
	v_dot4c_i32_i8_e32 v2, v0, v28
	v_lshrrev_b32_e32 v0, 4, v62
	v_and_b32_e32 v0, 0xf0f0f0f, v0
	v_dot4c_i32_i8_e32 v2, v0, v29
	v_and_b32_e32 v0, 0xf0f0f0f, v63
	v_dot4c_i32_i8_e32 v3, v0, v30
	v_lshrrev_b32_e32 v0, 4, v63
	v_and_b32_e32 v0, 0xf0f0f0f, v0
	v_dot4c_i32_i8_e32 v3, v0, v31
	v_and_b32_e32 v0, 0xf0f0f0f, v56
	v_dot4c_i32_i8_e32 v4, v0, v32
	v_lshrrev_b32_e32 v0, 4, v56
	v_and_b32_e32 v0, 0xf0f0f0f, v0
	v_dot4c_i32_i8_e32 v4, v0, v33
	v_and_b32_e32 v0, 0xf0f0f0f, v57
	v_dot4c_i32_i8_e32 v5, v0, v34
	v_lshrrev_b32_e32 v0, 4, v57
	v_and_b32_e32 v0, 0xf0f0f0f, v0
	v_dot4c_i32_i8_e32 v5, v0, v35
	v_and_b32_e32 v0, 0xf0f0f0f, v58
	v_dot4c_i32_i8_e32 v4, v0, v28
	v_lshrrev_b32_e32 v0, 4, v58
	v_and_b32_e32 v0, 0xf0f0f0f, v0
	v_dot4c_i32_i8_e32 v4, v0, v29
	v_and_b32_e32 v0, 0xf0f0f0f, v59
	v_dot4c_i32_i8_e32 v5, v0, v30
	v_lshrrev_b32_e32 v0, 4, v59
	v_and_b32_e32 v0, 0xf0f0f0f, v0
	v_dot4c_i32_i8_e32 v5, v0, v31
	v_add_u32_e32 v2, v2, v3
	v_sub_u32_e32 v2, v2, v169
	s_waitcnt vmcnt(8)
; #define P12_ISSUE(c_, i_, h_, CW_, SC_) do { _Pragma("unroll") for (int bb = 0; bb < 8; ++bb) { const unsigned ro = (unsigned)(c_) * 16384u + (unsigned)EL[(i_) * 128 + ((h_) * 8 + bb) * 8 + g8]; \
;         CW_[bb] = *(const v4u*)(U4 + (size_t)(ro * 128u + 16u * (unsigned)k8)); SC_[bb] = USS[(size_t)(ro * 8u + (unsigned)k8)]; } } while (0)
; #define P12_COMP(i_, h_, CW_, SC_) do { _Pragma("unroll") for (int bb = 0; bb < 8; ++bb) { int a0 = 0, a1 = 0; P12_U4(CW_[bb].x, xa.x, xa.y, a0); P12_U4(CW_[bb].y, xa.z, xa.w, a1); P12_U4(CW_[bb].z, xb.x, xb.y, a0); P12_U4(CW_[bb].w, xb.z, xb.w, a1); \
;         psum[(i_)][(h_) * 8 + bb] += __uint_as_float(SC_[bb] << 16) * (float)((a0 + a1) - xo); } } while (0)
; #define P12_BAR() asm volatile("" ::: "memory")
; __device__ __forceinline__ void p12_peer(Frame& F) {
;     ...
;     { v4u cwA[8], cwB[8]; unsigned scA[8], scB[8]; v4u xa, xb; int xo;
;       P12_ISSUE(0, 0, 0, cwA, scA);
; _Pragma("nounroll")
;       for (int c = 0; c < 16; ++c) { const int cn = c + 1 < 16 ? c + 1 : 15;
;           P12_XQ(c, 0); P12_ISSUE(c, 0, 1, cwB, scB); P12_BAR(); P12_COMP(0, 0, cwA, scA); P12_ISSUE(c, 1, 0, cwA, scA); P12_BAR(); P12_COMP(0, 1, cwB, scB);
;           P12_XQ(c, 1); P12_ISSUE(c, 1, 1, cwB, scB); P12_BAR(); P12_COMP(1, 0, cwA, scA); P12_ISSUE(c, 2, 0, cwA, scA); P12_BAR(); P12_COMP(1, 1, cwB, scB);
;           P12_XQ(c, 2); P12_ISSUE(c, 2, 1, cwB, scB); P12_BAR(); P12_COMP(2, 0, cwA, scA); P12_ISSUE(c, 3, 0, cwA, scA); P12_BAR(); P12_COMP(2, 1, cwB, scB);
;           P12_XQ(c, 3); P12_ISSUE(c, 3, 1, cwB, scB); P12_BAR(); P12_COMP(3, 0, cwA, scA); P12_ISSUE(cn, 0, 0, cwA, scA); P12_BAR(); P12_COMP(3, 1, cwB, scB);
	v_and_b32_e32 v1, 0xffff0000, v218
	v_add_u32_e32 v3, v4, v5
	v_sub_u32_e32 v4, v3, v169
	v_cvt_f32_i32_e32 v3, v2
	v_cvt_f32_i32_e32 v2, v4
	v_and_b32_e32 v0, 0xffff0000, v219
	v_mov_b32_e32 v4, 0
	v_mov_b32_e32 v5, 0
	v_pk_fma_f32 v[124:125], v[0:1], v[2:3], v[124:125]
	v_and_b32_e32 v0, 0xf0f0f0f, v44
	v_mov_b32_e32 v2, 0
	v_dot4c_i32_i8_e32 v2, v0, v32
	v_lshrrev_b32_e32 v0, 4, v44
	v_and_b32_e32 v0, 0xf0f0f0f, v0
	v_dot4c_i32_i8_e32 v2, v0, v33
	v_and_b32_e32 v0, 0xf0f0f0f, v45
	v_mov_b32_e32 v3, 0
	v_dot4c_i32_i8_e32 v3, v0, v34
	v_lshrrev_b32_e32 v0, 4, v45
	v_and_b32_e32 v0, 0xf0f0f0f, v0
	v_dot4c_i32_i8_e32 v3, v0, v35
	v_and_b32_e32 v0, 0xf0f0f0f, v46
	v_dot4c_i32_i8_e32 v2, v0, v28
	v_lshrrev_b32_e32 v0, 4, v46
	v_and_b32_e32 v0, 0xf0f0f0f, v0
	v_dot4c_i32_i8_e32 v2, v0, v29
	v_and_b32_e32 v0, 0xf0f0f0f, v47
	v_dot4c_i32_i8_e32 v3, v0, v30
	v_lshrrev_b32_e32 v0, 4, v47
	v_and_b32_e32 v0, 0xf0f0f0f, v0
	v_dot4c_i32_i8_e32 v3, v0, v31
	v_and_b32_e32 v0, 0xf0f0f0f, v24
	v_dot4c_i32_i8_e32 v4, v0, v32
	v_lshrrev_b32_e32 v0, 4, v24
	v_and_b32_e32 v0, 0xf0f0f0f, v0
	v_dot4c_i32_i8_e32 v4, v0, v33
	v_and_b32_e32 v0, 0xf0f0f0f, v25
	v_dot4c_i32_i8_e32 v5, v0, v34
	v_lshrrev_b32_e32 v0, 4, v25
	v_and_b32_e32 v0, 0xf0f0f0f, v0
	v_dot4c_i32_i8_e32 v5, v0, v35
	v_and_b32_e32 v0, 0xf0f0f0f, v26
	v_dot4c_i32_i8_e32 v4, v0, v28
	v_lshrrev_b32_e32 v0, 4, v26
	v_and_b32_e32 v0, 0xf0f0f0f, v0
	v_dot4c_i32_i8_e32 v4, v0, v29
	v_and_b32_e32 v0, 0xf0f0f0f, v27
	v_dot4c_i32_i8_e32 v5, v0, v30
	v_lshrrev_b32_e32 v0, 4, v27
	v_and_b32_e32 v0, 0xf0f0f0f, v0
	v_dot4c_i32_i8_e32 v5, v0, v31
	v_add_u32_e32 v2, v2, v3
	v_sub_u32_e32 v2, v2, v169
	s_waitcnt vmcnt(8)
	v_and_b32_e32 v1, 0xffff0000, v220
	v_add_u32_e32 v3, v4, v5
	v_sub_u32_e32 v4, v3, v169
	v_cvt_f32_i32_e32 v3, v2
	v_cvt_f32_i32_e32 v2, v4
	v_and_b32_e32 v0, 0xffff0000, v221
	v_mov_b32_e32 v4, 0
	v_mov_b32_e32 v5, 0
	v_pk_fma_f32 v[122:123], v[0:1], v[2:3], v[122:123]
	v_and_b32_e32 v0, 0xf0f0f0f, v12
	v_mov_b32_e32 v2, 0
	v_dot4c_i32_i8_e32 v2, v0, v32
	v_lshrrev_b32_e32 v0, 4, v12
	v_and_b32_e32 v0, 0xf0f0f0f, v0
	v_dot4c_i32_i8_e32 v2, v0, v33
	v_and_b32_e32 v0, 0xf0f0f0f, v13
	v_mov_b32_e32 v3, 0
	v_dot4c_i32_i8_e32 v3, v0, v34
	v_lshrrev_b32_e32 v0, 4, v13
	v_and_b32_e32 v0, 0xf0f0f0f, v0
	v_dot4c_i32_i8_e32 v3, v0, v35
	v_and_b32_e32 v0, 0xf0f0f0f, v14
	v_dot4c_i32_i8_e32 v2, v0, v28
	v_lshrrev_b32_e32 v0, 4, v14
	v_and_b32_e32 v0, 0xf0f0f0f, v0
	v_dot4c_i32_i8_e32 v2, v0, v29
	v_and_b32_e32 v0, 0xf0f0f0f, v15
	v_dot4c_i32_i8_e32 v3, v0, v30
	v_lshrrev_b32_e32 v0, 4, v15
	v_and_b32_e32 v0, 0xf0f0f0f, v0
	v_dot4c_i32_i8_e32 v3, v0, v31
	v_and_b32_e32 v0, 0xf0f0f0f, v8
	v_dot4c_i32_i8_e32 v4, v0, v32
	v_lshrrev_b32_e32 v0, 4, v8
	v_and_b32_e32 v0, 0xf0f0f0f, v0
	v_dot4c_i32_i8_e32 v4, v0, v33
	v_and_b32_e32 v0, 0xf0f0f0f, v9
	v_dot4c_i32_i8_e32 v5, v0, v34
	v_lshrrev_b32_e32 v0, 4, v9
	v_and_b32_e32 v0, 0xf0f0f0f, v0
	v_dot4c_i32_i8_e32 v5, v0, v35
	v_and_b32_e32 v0, 0xf0f0f0f, v10
	v_dot4c_i32_i8_e32 v4, v0, v28
	v_lshrrev_b32_e32 v0, 4, v10
	v_and_b32_e32 v0, 0xf0f0f0f, v0
	v_dot4c_i32_i8_e32 v4, v0, v29
	v_and_b32_e32 v0, 0xf0f0f0f, v11
	v_dot4c_i32_i8_e32 v5, v0, v30
	v_lshrrev_b32_e32 v0, 4, v11
	v_and_b32_e32 v0, 0xf0f0f0f, v0
	v_dot4c_i32_i8_e32 v5, v0, v31
	v_add_u32_e32 v2, v2, v3
	v_sub_u32_e32 v2, v2, v169
	s_waitcnt vmcnt(8)
	v_and_b32_e32 v1, 0xffff0000, v222
	v_add_u32_e32 v3, v4, v5
	v_sub_u32_e32 v4, v3, v169
	v_cvt_f32_i32_e32 v3, v2
	v_cvt_f32_i32_e32 v2, v4
	v_and_b32_e32 v0, 0xffff0000, v223
	v_pk_fma_f32 v[120:121], v[0:1], v[2:3], v[120:121]
	ds_read_u16 v0, v93 offset:17152
	ds_read_u16 v1, v93 offset:17168
	ds_read_u16 v2, v93 offset:17184
	ds_read_u16 v3, v93 offset:17200
	s_waitcnt lgkmcnt(3)
	v_add_u32_e32 v0, s44, v0
	v_lshl_or_b32 v4, v0, 7, v165
	v_lshl_or_b32 v44, v0, 4, v95
	s_waitcnt lgkmcnt(2)
	v_add_u32_e32 v0, s44, v1
	v_lshl_or_b32 v1, v0, 7, v165
	v_lshl_or_b32 v45, v0, 4, v95
	s_waitcnt lgkmcnt(1)
	v_add_u32_e32 v0, s44, v2
	global_load_dwordx4 v[72:75], v4, s[0:1]
	global_load_dwordx4 v[24:27], v1, s[0:1]
	v_lshl_or_b32 v1, v0, 7, v165
	v_lshl_or_b32 v46, v0, 4, v95
	s_waitcnt lgkmcnt(0)
	v_add_u32_e32 v0, s44, v3
	global_load_dwordx4 v[20:23], v1, s[0:1]
	v_lshl_or_b32 v1, v0, 7, v165
	v_lshl_or_b32 v47, v0, 4, v95
	ds_read_u16 v0, v93 offset:17216
	global_load_dwordx4 v[16:19], v1, s[0:1]
	s_waitcnt lgkmcnt(0)
	v_add_u32_e32 v0, s44, v0
	v_lshl_or_b32 v1, v0, 7, v165
	v_lshl_or_b32 v56, v0, 4, v95
	ds_read_u16 v0, v93 offset:17232
	global_load_dwordx4 v[12:15], v1, s[0:1]
	s_waitcnt lgkmcnt(0)
	v_add_u32_e32 v0, s44, v0
	v_lshl_or_b32 v1, v0, 7, v165
	v_lshl_or_b32 v57, v0, 4, v95
	ds_read_u16 v0, v93 offset:17248
	global_load_dwordx4 v[8:11], v1, s[0:1]
	s_waitcnt lgkmcnt(0)
	v_add_u32_e32 v0, s44, v0
	v_lshl_or_b32 v1, v0, 7, v165
	v_lshl_or_b32 v58, v0, 4, v95
	ds_read_u16 v0, v93 offset:17264
	global_load_dwordx4 v[4:7], v1, s[0:1]
	s_waitcnt lgkmcnt(0)
	v_add_u32_e32 v59, s44, v0
	v_lshl_or_b32 v0, v59, 7, v165
	global_load_dwordx4 v[0:3], v0, s[0:1]
	v_lshl_or_b32 v59, v59, 4, v95
	s_waitcnt vmcnt(15)
	v_and_b32_e32 v44, 0xf0f0f0f, v84
	v_mov_b32_e32 v46, 0
	v_dot4c_i32_i8_e32 v46, v44, v32
	v_lshrrev_b32_e32 v44, 4, v84
	v_and_b32_e32 v44, 0xf0f0f0f, v44
	v_dot4c_i32_i8_e32 v46, v44, v33
	v_and_b32_e32 v44, 0xf0f0f0f, v85
	v_mov_b32_e32 v47, 0
	v_dot4c_i32_i8_e32 v47, v44, v34
	v_lshrrev_b32_e32 v44, 4, v85
	v_and_b32_e32 v44, 0xf0f0f0f, v44
	v_dot4c_i32_i8_e32 v47, v44, v35
	v_and_b32_e32 v44, 0xf0f0f0f, v86
	v_dot4c_i32_i8_e32 v46, v44, v28
	v_lshrrev_b32_e32 v44, 4, v86
	v_and_b32_e32 v44, 0xf0f0f0f, v44
	v_dot4c_i32_i8_e32 v46, v44, v29
	v_and_b32_e32 v44, 0xf0f0f0f, v87
	v_dot4c_i32_i8_e32 v47, v44, v30
	v_lshrrev_b32_e32 v44, 4, v87
	v_and_b32_e32 v44, 0xf0f0f0f, v44
	v_dot4c_i32_i8_e32 v47, v44, v31
	s_waitcnt vmcnt(14)
; #define P12_ISSUE(c_, i_, h_, CW_, SC_) do { _Pragma("unroll") for (int bb = 0; bb < 8; ++bb) { const unsigned ro = (unsigned)(c_) * 16384u + (unsigned)EL[(i_) * 128 + ((h_) * 8 + bb) * 8 + g8]; \
;         CW_[bb] = *(const v4u*)(U4 + (size_t)(ro * 128u + 16u * (unsigned)k8)); SC_[bb] = USS[(size_t)(ro * 8u + (unsigned)k8)]; } } while (0)
; #define P12_COMP(i_, h_, CW_, SC_) do { _Pragma("unroll") for (int bb = 0; bb < 8; ++bb) { int a0 = 0, a1 = 0; P12_U4(CW_[bb].x, xa.x, xa.y, a0); P12_U4(CW_[bb].y, xa.z, xa.w, a1); P12_U4(CW_[bb].z, xb.x, xb.y, a0); P12_U4(CW_[bb].w, xb.z, xb.w, a1); \
;         psum[(i_)][(h_) * 8 + bb] += __uint_as_float(SC_[bb] << 16) * (float)((a0 + a1) - xo); } } while (0)
; #define P12_BAR() asm volatile("" ::: "memory")
; __device__ __forceinline__ void p12_peer(Frame& F) {
;     ...
;     { v4u cwA[8], cwB[8]; unsigned scA[8], scB[8]; v4u xa, xb; int xo;
;       P12_ISSUE(0, 0, 0, cwA, scA);
; _Pragma("nounroll")
;       for (int c = 0; c < 16; ++c) { const int cn = c + 1 < 16 ? c + 1 : 15;
;           P12_XQ(c, 0); P12_ISSUE(c, 0, 1, cwB, scB); P12_BAR(); P12_COMP(0, 0, cwA, scA); P12_ISSUE(c, 1, 0, cwA, scA); P12_BAR(); P12_COMP(0, 1, cwB, scB);
;           P12_XQ(c, 1); P12_ISSUE(c, 1, 1, cwB, scB); P12_BAR(); P12_COMP(1, 0, cwA, scA); P12_ISSUE(c, 2, 0, cwA, scA); P12_BAR(); P12_COMP(1, 1, cwB, scB);
;           P12_XQ(c, 2); P12_ISSUE(c, 2, 1, cwB, scB); P12_BAR(); P12_COMP(2, 0, cwA, scA); P12_ISSUE(c, 3, 0, cwA, scA); P12_BAR(); P12_COMP(2, 1, cwB, scB);
;           P12_XQ(c, 3); P12_ISSUE(c, 3, 1, cwB, scB); P12_BAR(); P12_COMP(3, 0, cwA, scA); P12_ISSUE(cn, 0, 0, cwA, scA); P12_BAR(); P12_COMP(3, 1, cwB, scB);
	v_and_b32_e32 v44, 0xf0f0f0f, v80
	v_mov_b32_e32 v56, 0
	v_dot4c_i32_i8_e32 v56, v44, v32
	v_lshrrev_b32_e32 v44, 4, v80
	v_and_b32_e32 v44, 0xf0f0f0f, v44
	v_dot4c_i32_i8_e32 v56, v44, v33
	v_and_b32_e32 v44, 0xf0f0f0f, v81
	v_mov_b32_e32 v57, 0
	v_dot4c_i32_i8_e32 v57, v44, v34
	v_lshrrev_b32_e32 v44, 4, v81
	v_and_b32_e32 v44, 0xf0f0f0f, v44
	v_dot4c_i32_i8_e32 v57, v44, v35
	v_and_b32_e32 v44, 0xf0f0f0f, v82
	v_dot4c_i32_i8_e32 v56, v44, v28
	v_lshrrev_b32_e32 v44, 4, v82
	v_and_b32_e32 v44, 0xf0f0f0f, v44
	v_dot4c_i32_i8_e32 v56, v44, v29
	v_and_b32_e32 v44, 0xf0f0f0f, v83
	v_dot4c_i32_i8_e32 v57, v44, v30
	v_lshrrev_b32_e32 v44, 4, v83
	v_and_b32_e32 v44, 0xf0f0f0f, v44
	v_dot4c_i32_i8_e32 v57, v44, v31
	v_add_u32_e32 v46, v46, v47
	v_sub_u32_e32 v46, v46, v169
	s_waitcnt vmcnt(8)
	v_and_b32_e32 v45, 0xffff0000, v224
	v_sub_u32_e32 v47, v57, v169
	v_add_u32_e32 v56, v47, v56
	v_cvt_f32_i32_e32 v47, v46
	v_cvt_f32_i32_e32 v46, v56
	v_and_b32_e32 v44, 0xffff0000, v225
	v_mov_b32_e32 v56, 0
	v_mov_b32_e32 v57, 0
	v_pk_fma_f32 v[118:119], v[44:45], v[46:47], v[118:119]
	v_and_b32_e32 v44, 0xf0f0f0f, v68
	v_mov_b32_e32 v46, 0
	v_dot4c_i32_i8_e32 v46, v44, v32
	v_lshrrev_b32_e32 v44, 4, v68
	v_and_b32_e32 v44, 0xf0f0f0f, v44
	v_dot4c_i32_i8_e32 v46, v44, v33
	v_and_b32_e32 v44, 0xf0f0f0f, v69
	v_mov_b32_e32 v47, 0
	v_dot4c_i32_i8_e32 v47, v44, v34
	v_lshrrev_b32_e32 v44, 4, v69
	v_and_b32_e32 v44, 0xf0f0f0f, v44
	v_dot4c_i32_i8_e32 v47, v44, v35
	v_and_b32_e32 v44, 0xf0f0f0f, v70
	v_dot4c_i32_i8_e32 v46, v44, v28
	v_lshrrev_b32_e32 v44, 4, v70
	v_and_b32_e32 v44, 0xf0f0f0f, v44
	v_dot4c_i32_i8_e32 v46, v44, v29
	v_and_b32_e32 v44, 0xf0f0f0f, v71
	v_dot4c_i32_i8_e32 v47, v44, v30
	v_lshrrev_b32_e32 v44, 4, v71
	v_and_b32_e32 v44, 0xf0f0f0f, v44
	v_dot4c_i32_i8_e32 v47, v44, v31
	v_and_b32_e32 v44, 0xf0f0f0f, v64
	v_dot4c_i32_i8_e32 v56, v44, v32
	v_lshrrev_b32_e32 v44, 4, v64
	v_and_b32_e32 v44, 0xf0f0f0f, v44
	v_dot4c_i32_i8_e32 v56, v44, v33
	v_and_b32_e32 v44, 0xf0f0f0f, v65
	v_dot4c_i32_i8_e32 v57, v44, v34
	v_lshrrev_b32_e32 v44, 4, v65
	v_and_b32_e32 v44, 0xf0f0f0f, v44
	v_dot4c_i32_i8_e32 v57, v44, v35
	v_and_b32_e32 v44, 0xf0f0f0f, v66
	v_dot4c_i32_i8_e32 v56, v44, v28
	v_lshrrev_b32_e32 v44, 4, v66
	v_and_b32_e32 v44, 0xf0f0f0f, v44
	v_dot4c_i32_i8_e32 v56, v44, v29
	v_and_b32_e32 v44, 0xf0f0f0f, v67
	v_dot4c_i32_i8_e32 v57, v44, v30
	v_lshrrev_b32_e32 v44, 4, v67
	v_and_b32_e32 v44, 0xf0f0f0f, v44
	v_dot4c_i32_i8_e32 v57, v44, v31
	v_sub_u32_e32 v47, v47, v169
	v_add_u32_e32 v46, v47, v46
	v_cvt_f32_i32_e32 v47, v46
	v_sub_u32_e32 v57, v57, v169
	v_add_u32_e32 v56, v57, v56
	v_cvt_f32_i32_e32 v46, v56
	s_waitcnt vmcnt(8)
	v_and_b32_e32 v45, 0xffff0000, v226
	v_and_b32_e32 v44, 0xffff0000, v227
	v_pk_fma_f32 v[116:117], v[44:45], v[46:47], v[116:117]
	v_and_b32_e32 v44, 0xf0f0f0f, v52
	v_mov_b32_e32 v46, 0
	v_dot4c_i32_i8_e32 v46, v44, v32
	v_lshrrev_b32_e32 v44, 4, v52
	v_and_b32_e32 v44, 0xf0f0f0f, v44
	v_dot4c_i32_i8_e32 v46, v44, v33
	v_and_b32_e32 v44, 0xf0f0f0f, v53
	v_mov_b32_e32 v47, 0
	v_dot4c_i32_i8_e32 v47, v44, v34
	v_lshrrev_b32_e32 v44, 4, v53
	v_and_b32_e32 v44, 0xf0f0f0f, v44
	v_dot4c_i32_i8_e32 v47, v44, v35
	v_and_b32_e32 v44, 0xf0f0f0f, v54
	v_dot4c_i32_i8_e32 v46, v44, v28
	v_lshrrev_b32_e32 v44, 4, v54
	v_and_b32_e32 v44, 0xf0f0f0f, v44
	v_dot4c_i32_i8_e32 v46, v44, v29
	v_and_b32_e32 v44, 0xf0f0f0f, v55
	v_dot4c_i32_i8_e32 v47, v44, v30
	v_lshrrev_b32_e32 v44, 4, v55
	v_and_b32_e32 v44, 0xf0f0f0f, v44
	v_dot4c_i32_i8_e32 v47, v44, v31
	v_and_b32_e32 v44, 0xf0f0f0f, v48
	v_mov_b32_e32 v52, 0
	v_dot4c_i32_i8_e32 v52, v44, v32
	v_lshrrev_b32_e32 v44, 4, v48
	v_and_b32_e32 v44, 0xf0f0f0f, v44
	v_dot4c_i32_i8_e32 v52, v44, v33
	v_and_b32_e32 v44, 0xf0f0f0f, v49
	v_mov_b32_e32 v48, 0
	v_dot4c_i32_i8_e32 v48, v44, v34
	v_lshrrev_b32_e32 v44, 4, v49
	v_and_b32_e32 v44, 0xf0f0f0f, v44
	v_dot4c_i32_i8_e32 v48, v44, v35
	v_and_b32_e32 v44, 0xf0f0f0f, v50
	v_dot4c_i32_i8_e32 v52, v44, v28
	v_lshrrev_b32_e32 v44, 4, v50
	v_and_b32_e32 v44, 0xf0f0f0f, v44
	v_dot4c_i32_i8_e32 v52, v44, v29
	v_and_b32_e32 v44, 0xf0f0f0f, v51
	v_dot4c_i32_i8_e32 v48, v44, v30
	v_lshrrev_b32_e32 v44, 4, v51
	v_and_b32_e32 v44, 0xf0f0f0f, v44
	v_dot4c_i32_i8_e32 v48, v44, v31
	v_sub_u32_e32 v47, v47, v169
	v_add_u32_e32 v46, v47, v46
	v_cvt_f32_i32_e32 v47, v46
	v_sub_u32_e32 v48, v48, v169
	v_add_u32_e32 v48, v48, v52
	v_cvt_f32_i32_e32 v46, v48
	s_waitcnt vmcnt(8)
	v_and_b32_e32 v45, 0xffff0000, v228
	v_and_b32_e32 v44, 0xffff0000, v229
	v_pk_fma_f32 v[114:115], v[44:45], v[46:47], v[114:115]
	v_and_b32_e32 v44, 0xf0f0f0f, v40
	v_mov_b32_e32 v45, 0
	v_lshrrev_b32_e32 v40, 4, v40
	v_dot4c_i32_i8_e32 v45, v44, v32
	v_and_b32_e32 v40, 0xf0f0f0f, v40
	v_dot4c_i32_i8_e32 v45, v40, v33
	v_and_b32_e32 v40, 0xf0f0f0f, v41
	v_mov_b32_e32 v44, 0
	v_dot4c_i32_i8_e32 v44, v40, v34
	v_lshrrev_b32_e32 v40, 4, v41
	v_and_b32_e32 v40, 0xf0f0f0f, v40
	v_dot4c_i32_i8_e32 v44, v40, v35
	v_and_b32_e32 v40, 0xf0f0f0f, v42
	v_dot4c_i32_i8_e32 v45, v40, v28
	v_lshrrev_b32_e32 v40, 4, v42
	v_and_b32_e32 v40, 0xf0f0f0f, v40
	v_dot4c_i32_i8_e32 v45, v40, v29
	v_and_b32_e32 v40, 0xf0f0f0f, v43
	v_dot4c_i32_i8_e32 v44, v40, v30
	v_lshrrev_b32_e32 v40, 4, v43
	v_and_b32_e32 v40, 0xf0f0f0f, v40
	v_dot4c_i32_i8_e32 v44, v40, v31
	v_and_b32_e32 v40, 0xf0f0f0f, v36
	v_mov_b32_e32 v41, 0
	v_dot4c_i32_i8_e32 v41, v40, v32
	v_lshrrev_b32_e32 v32, 4, v36
	v_and_b32_e32 v32, 0xf0f0f0f, v32
	v_dot4c_i32_i8_e32 v41, v32, v33
	v_and_b32_e32 v32, 0xf0f0f0f, v37
	v_mov_b32_e32 v33, 0
	v_dot4c_i32_i8_e32 v33, v32, v34
	v_lshrrev_b32_e32 v32, 4, v37
	v_and_b32_e32 v32, 0xf0f0f0f, v32
	v_dot4c_i32_i8_e32 v33, v32, v35
	v_and_b32_e32 v32, 0xf0f0f0f, v38
	v_dot4c_i32_i8_e32 v41, v32, v28
	v_lshrrev_b32_e32 v28, 4, v38
	v_and_b32_e32 v28, 0xf0f0f0f, v28
	v_dot4c_i32_i8_e32 v41, v28, v29
	v_and_b32_e32 v28, 0xf0f0f0f, v39
	v_dot4c_i32_i8_e32 v33, v28, v30
	v_lshrrev_b32_e32 v28, 4, v39
	v_and_b32_e32 v28, 0xf0f0f0f, v28
	v_dot4c_i32_i8_e32 v33, v28, v31
	v_sub_u32_e32 v30, v44, v169
	v_add_u32_e32 v30, v30, v45
	s_waitcnt vmcnt(8)
; #define P12_ISSUE(c_, i_, h_, CW_, SC_) do { _Pragma("unroll") for (int bb = 0; bb < 8; ++bb) { const unsigned ro = (unsigned)(c_) * 16384u + (unsigned)EL[(i_) * 128 + ((h_) * 8 + bb) * 8 + g8]; \
;         CW_[bb] = *(const v4u*)(U4 + (size_t)(ro * 128u + 16u * (unsigned)k8)); SC_[bb] = USS[(size_t)(ro * 8u + (unsigned)k8)]; } } while (0)
; #define P12_COMP(i_, h_, CW_, SC_) do { _Pragma("unroll") for (int bb = 0; bb < 8; ++bb) { int a0 = 0, a1 = 0; P12_U4(CW_[bb].x, xa.x, xa.y, a0); P12_U4(CW_[bb].y, xa.z, xa.w, a1); P12_U4(CW_[bb].z, xb.x, xb.y, a0); P12_U4(CW_[bb].w, xb.z, xb.w, a1); \
;         psum[(i_)][(h_) * 8 + bb] += __uint_as_float(SC_[bb] << 16) * (float)((a0 + a1) - xo); } } while (0)
; #define P12_BAR() asm volatile("" ::: "memory")
; __device__ __forceinline__ void p12_peer(Frame& F) {
;     ...
;     { v4u cwA[8], cwB[8]; unsigned scA[8], scB[8]; v4u xa, xb; int xo;
;       P12_ISSUE(0, 0, 0, cwA, scA);
; _Pragma("nounroll")
;       for (int c = 0; c < 16; ++c) { const int cn = c + 1 < 16 ? c + 1 : 15;
;           P12_XQ(c, 0); P12_ISSUE(c, 0, 1, cwB, scB); P12_BAR(); P12_COMP(0, 0, cwA, scA); P12_ISSUE(c, 1, 0, cwA, scA); P12_BAR(); P12_COMP(0, 1, cwB, scB);
;           P12_XQ(c, 1); P12_ISSUE(c, 1, 1, cwB, scB); P12_BAR(); P12_COMP(1, 0, cwA, scA); P12_ISSUE(c, 2, 0, cwA, scA); P12_BAR(); P12_COMP(1, 1, cwB, scB);
;           P12_XQ(c, 2); P12_ISSUE(c, 2, 1, cwB, scB); P12_BAR(); P12_COMP(2, 0, cwA, scA); P12_ISSUE(c, 3, 0, cwA, scA); P12_BAR(); P12_COMP(2, 1, cwB, scB);
;           P12_XQ(c, 3); P12_ISSUE(c, 3, 1, cwB, scB); P12_BAR(); P12_COMP(3, 0, cwA, scA); P12_ISSUE(cn, 0, 0, cwA, scA); P12_BAR(); P12_COMP(3, 1, cwB, scB);
	v_and_b32_e32 v29, 0xffff0000, v230
	v_sub_u32_e32 v31, v33, v169
	v_add_u32_e32 v32, v31, v41
	v_cvt_f32_i32_e32 v31, v30
	v_cvt_f32_i32_e32 v30, v32
	v_and_b32_e32 v28, 0xffff0000, v231
	ds_read_b128 v[36:39], v166 offset:12288
	ds_read_b128 v[32:35], v166 offset:12304
	v_add_u32_e32 v166, 0x100, v166
	v_pk_fma_f32 v[112:113], v[28:29], v[30:31], v[112:113]
	ds_read_u16 v29, v93 offset:17280
	ds_read_u16 v30, v93 offset:17296
	ds_read_u16 v31, v93 offset:17312
	ds_read_u16 v40, v93 offset:17328
	v_mov_b32_e32 v28, 0
	s_waitcnt lgkmcnt(3)
	v_add_u32_e32 v29, s44, v29
	v_lshl_or_b32 v41, v29, 7, v165
	s_waitcnt lgkmcnt(2)
	v_add_u32_e32 v30, s44, v30
	global_load_dwordx4 v[68:71], v41, s[0:1]
	v_lshl_or_b32 v41, v30, 7, v165
	s_waitcnt lgkmcnt(1)
	v_add_u32_e32 v31, s44, v31
	global_load_dwordx4 v[64:67], v41, s[0:1]
	v_lshl_or_b32 v41, v31, 7, v165
	s_waitcnt lgkmcnt(0)
	v_add_u32_e32 v40, s44, v40
	global_load_dwordx4 v[60:63], v41, s[0:1]
	v_lshl_or_b32 v41, v40, 7, v165
	v_lshl_or_b32 v79, v40, 4, v95
	ds_read_u16 v40, v93 offset:17344
	global_load_dwordx4 v[56:59], v41, s[0:1]
	v_dot4c_i32_i8_e32 v28, 0x1010101, v36
	v_dot4c_i32_i8_e32 v28, 0x1010101, v37
	v_dot4c_i32_i8_e32 v28, 0x1010101, v38
	s_waitcnt lgkmcnt(0)
	v_add_u32_e32 v40, s44, v40
	v_lshl_or_b32 v41, v40, 7, v165
	v_lshl_or_b32 v80, v40, 4, v95
	ds_read_u16 v40, v93 offset:17360
	global_load_dwordx4 v[52:55], v41, s[0:1]
	v_dot4c_i32_i8_e32 v28, 0x1010101, v39
	v_dot4c_i32_i8_e32 v28, 0x1010101, v32
	v_dot4c_i32_i8_e32 v28, 0x1010101, v33
	s_waitcnt lgkmcnt(0)
	v_add_u32_e32 v40, s44, v40
	v_lshl_or_b32 v41, v40, 7, v165
	v_lshl_or_b32 v82, v40, 4, v95
	ds_read_u16 v40, v93 offset:17376
	global_load_dwordx4 v[48:51], v41, s[0:1]
	v_dot4c_i32_i8_e32 v28, 0x1010101, v34
	v_dot4c_i32_i8_e32 v28, 0x1010101, v35
	v_lshl_or_b32 v29, v29, 4, v95
	s_waitcnt lgkmcnt(0)
	v_add_u32_e32 v40, s44, v40
	v_lshl_or_b32 v41, v40, 7, v165
	v_lshl_or_b32 v87, v40, 4, v95
	ds_read_u16 v40, v93 offset:17392
	v_lshl_or_b32 v30, v30, 4, v95
	v_lshl_or_b32 v31, v31, 4, v95
	global_load_dwordx4 v[44:47], v41, s[0:1]
	s_waitcnt lgkmcnt(0)
	v_add_u32_e32 v78, s44, v40
	v_lshl_or_b32 v40, v78, 7, v165
	global_load_dwordx4 v[40:43], v40, s[0:1]
	v_lshl_or_b32 v169, v78, 4, v95
	v_lshlrev_b32_e32 v78, 3, v28
	s_nop 0
	s_nop 0
	s_waitcnt vmcnt(15)
	v_and_b32_e32 v29, 0xf0f0f0f, v72
	v_mov_b32_e32 v28, 0
	v_dot4c_i32_i8_e32 v28, v29, v36
	v_lshrrev_b32_e32 v29, 4, v72
	v_and_b32_e32 v29, 0xf0f0f0f, v29
	v_dot4c_i32_i8_e32 v28, v29, v37
	v_and_b32_e32 v30, 0xf0f0f0f, v73
	v_mov_b32_e32 v29, 0
	v_dot4c_i32_i8_e32 v29, v30, v38
	v_lshrrev_b32_e32 v30, 4, v73
	v_and_b32_e32 v30, 0xf0f0f0f, v30
	v_dot4c_i32_i8_e32 v29, v30, v39
	v_and_b32_e32 v30, 0xf0f0f0f, v74
	v_dot4c_i32_i8_e32 v28, v30, v32
	v_lshrrev_b32_e32 v30, 4, v74
	v_and_b32_e32 v30, 0xf0f0f0f, v30
	v_dot4c_i32_i8_e32 v28, v30, v33
	v_and_b32_e32 v30, 0xf0f0f0f, v75
	v_dot4c_i32_i8_e32 v29, v30, v34
	v_lshrrev_b32_e32 v30, 4, v75
	v_and_b32_e32 v30, 0xf0f0f0f, v30
	v_dot4c_i32_i8_e32 v29, v30, v35
	s_waitcnt vmcnt(14)
	v_and_b32_e32 v31, 0xf0f0f0f, v24
	v_mov_b32_e32 v30, 0
	v_lshrrev_b32_e32 v24, 4, v24
	v_dot4c_i32_i8_e32 v30, v31, v36
	v_and_b32_e32 v24, 0xf0f0f0f, v24
	v_dot4c_i32_i8_e32 v30, v24, v37
	v_and_b32_e32 v24, 0xf0f0f0f, v25
	v_mov_b32_e32 v31, 0
	v_dot4c_i32_i8_e32 v31, v24, v38
	v_lshrrev_b32_e32 v24, 4, v25
	v_and_b32_e32 v24, 0xf0f0f0f, v24
	v_dot4c_i32_i8_e32 v31, v24, v39
	v_and_b32_e32 v24, 0xf0f0f0f, v26
	v_dot4c_i32_i8_e32 v30, v24, v32
	v_lshrrev_b32_e32 v24, 4, v26
	v_and_b32_e32 v24, 0xf0f0f0f, v24
	v_dot4c_i32_i8_e32 v30, v24, v33
	v_and_b32_e32 v24, 0xf0f0f0f, v27
	v_dot4c_i32_i8_e32 v31, v24, v34
	v_lshrrev_b32_e32 v24, 4, v27
	v_and_b32_e32 v24, 0xf0f0f0f, v24
	v_dot4c_i32_i8_e32 v31, v24, v35
	v_add_u32_e32 v26, v28, v29
	v_sub_u32_e32 v26, v26, v78
	s_waitcnt vmcnt(8)
	v_and_b32_e32 v25, 0xffff0000, v232
	v_add_u32_e32 v27, v30, v31
	v_sub_u32_e32 v28, v27, v78
	v_cvt_f32_i32_e32 v27, v26
	v_cvt_f32_i32_e32 v26, v28
	v_and_b32_e32 v24, 0xffff0000, v233
	s_cselect_b32 s44, s44, s45
	s_lshl_b32 s49, s44, 4
	s_sub_u32 s46, s18, s49
	s_subb_u32 s47, s19, 0
	s_cmp_eq_u32 s45, 0x40000
	v_pk_fma_f32 v[110:111], v[24:25], v[26:27], v[110:111]
	v_and_b32_e32 v24, 0xf0f0f0f, v20
	v_mov_b32_e32 v25, 0
	v_lshrrev_b32_e32 v20, 4, v20
	v_dot4c_i32_i8_e32 v25, v24, v36
	v_and_b32_e32 v20, 0xf0f0f0f, v20
	v_dot4c_i32_i8_e32 v25, v20, v37
	v_and_b32_e32 v20, 0xf0f0f0f, v21
	v_mov_b32_e32 v24, 0
	v_dot4c_i32_i8_e32 v24, v20, v38
	v_lshrrev_b32_e32 v20, 4, v21
	v_and_b32_e32 v20, 0xf0f0f0f, v20
	v_dot4c_i32_i8_e32 v24, v20, v39
	v_and_b32_e32 v20, 0xf0f0f0f, v22
	v_dot4c_i32_i8_e32 v25, v20, v32
	v_lshrrev_b32_e32 v20, 4, v22
	v_and_b32_e32 v20, 0xf0f0f0f, v20
	v_dot4c_i32_i8_e32 v25, v20, v33
	v_and_b32_e32 v20, 0xf0f0f0f, v23
	v_dot4c_i32_i8_e32 v24, v20, v34
	v_lshrrev_b32_e32 v20, 4, v23
	v_and_b32_e32 v20, 0xf0f0f0f, v20
	v_dot4c_i32_i8_e32 v24, v20, v35
	v_and_b32_e32 v20, 0xf0f0f0f, v16
	v_mov_b32_e32 v21, 0
	v_lshrrev_b32_e32 v16, 4, v16
	v_dot4c_i32_i8_e32 v21, v20, v36
	v_and_b32_e32 v16, 0xf0f0f0f, v16
	v_dot4c_i32_i8_e32 v21, v16, v37
	v_and_b32_e32 v16, 0xf0f0f0f, v17
	v_mov_b32_e32 v20, 0
	v_dot4c_i32_i8_e32 v20, v16, v38
	v_lshrrev_b32_e32 v16, 4, v17
	v_and_b32_e32 v16, 0xf0f0f0f, v16
	v_dot4c_i32_i8_e32 v20, v16, v39
	v_and_b32_e32 v16, 0xf0f0f0f, v18
	v_dot4c_i32_i8_e32 v21, v16, v32
	v_lshrrev_b32_e32 v16, 4, v18
	v_and_b32_e32 v16, 0xf0f0f0f, v16
	v_dot4c_i32_i8_e32 v21, v16, v33
	v_and_b32_e32 v16, 0xf0f0f0f, v19
	v_dot4c_i32_i8_e32 v20, v16, v34
	v_lshrrev_b32_e32 v16, 4, v19
	v_and_b32_e32 v16, 0xf0f0f0f, v16
	v_dot4c_i32_i8_e32 v20, v16, v35
	v_add_u32_e32 v18, v25, v24
	v_sub_u32_e32 v18, v18, v78
	s_waitcnt vmcnt(8)
; #define P12_ISSUE(c_, i_, h_, CW_, SC_) do { _Pragma("unroll") for (int bb = 0; bb < 8; ++bb) { const unsigned ro = (unsigned)(c_) * 16384u + (unsigned)EL[(i_) * 128 + ((h_) * 8 + bb) * 8 + g8]; \
;         CW_[bb] = *(const v4u*)(U4 + (size_t)(ro * 128u + 16u * (unsigned)k8)); SC_[bb] = USS[(size_t)(ro * 8u + (unsigned)k8)]; } } while (0)
; #define P12_COMP(i_, h_, CW_, SC_) do { _Pragma("unroll") for (int bb = 0; bb < 8; ++bb) { int a0 = 0, a1 = 0; P12_U4(CW_[bb].x, xa.x, xa.y, a0); P12_U4(CW_[bb].y, xa.z, xa.w, a1); P12_U4(CW_[bb].z, xb.x, xb.y, a0); P12_U4(CW_[bb].w, xb.z, xb.w, a1); \
;         psum[(i_)][(h_) * 8 + bb] += __uint_as_float(SC_[bb] << 16) * (float)((a0 + a1) - xo); } } while (0)
; #define P12_BAR() asm volatile("" ::: "memory")
; __device__ __forceinline__ void p12_peer(Frame& F) {
;     ...
;     { v4u cwA[8], cwB[8]; unsigned scA[8], scB[8]; v4u xa, xb; int xo;
;       P12_ISSUE(0, 0, 0, cwA, scA);
; _Pragma("nounroll")
;       for (int c = 0; c < 16; ++c) { const int cn = c + 1 < 16 ? c + 1 : 15;
;           P12_XQ(c, 0); P12_ISSUE(c, 0, 1, cwB, scB); P12_BAR(); P12_COMP(0, 0, cwA, scA); P12_ISSUE(c, 1, 0, cwA, scA); P12_BAR(); P12_COMP(0, 1, cwB, scB);
;           P12_XQ(c, 1); P12_ISSUE(c, 1, 1, cwB, scB); P12_BAR(); P12_COMP(1, 0, cwA, scA); P12_ISSUE(c, 2, 0, cwA, scA); P12_BAR(); P12_COMP(1, 1, cwB, scB);
;           P12_XQ(c, 2); P12_ISSUE(c, 2, 1, cwB, scB); P12_BAR(); P12_COMP(2, 0, cwA, scA); P12_ISSUE(c, 3, 0, cwA, scA); P12_BAR(); P12_COMP(2, 1, cwB, scB);
;           P12_XQ(c, 3); P12_ISSUE(c, 3, 1, cwB, scB); P12_BAR(); P12_COMP(3, 0, cwA, scA); P12_ISSUE(cn, 0, 0, cwA, scA); P12_BAR(); P12_COMP(3, 1, cwB, scB);
	v_and_b32_e32 v17, 0xffff0000, v234
	v_add_u32_e32 v19, v21, v20
	v_sub_u32_e32 v20, v19, v78
	v_cvt_f32_i32_e32 v19, v18
	v_cvt_f32_i32_e32 v18, v20
	v_and_b32_e32 v16, 0xffff0000, v235
	v_mov_b32_e32 v90, 0
	s_cmp_eq_u32 s45, 0x40000
	v_pk_fma_f32 v[108:109], v[16:17], v[18:19], v[108:109]
	v_and_b32_e32 v16, 0xf0f0f0f, v12
	v_mov_b32_e32 v17, 0
	v_lshrrev_b32_e32 v12, 4, v12
	v_dot4c_i32_i8_e32 v17, v16, v36
	v_and_b32_e32 v12, 0xf0f0f0f, v12
	v_dot4c_i32_i8_e32 v17, v12, v37
	v_and_b32_e32 v12, 0xf0f0f0f, v13
	v_mov_b32_e32 v16, 0
	v_dot4c_i32_i8_e32 v16, v12, v38
	v_lshrrev_b32_e32 v12, 4, v13
	v_and_b32_e32 v12, 0xf0f0f0f, v12
	v_dot4c_i32_i8_e32 v16, v12, v39
	v_and_b32_e32 v12, 0xf0f0f0f, v14
	v_dot4c_i32_i8_e32 v17, v12, v32
	v_lshrrev_b32_e32 v12, 4, v14
	v_and_b32_e32 v12, 0xf0f0f0f, v12
	v_dot4c_i32_i8_e32 v17, v12, v33
	v_and_b32_e32 v12, 0xf0f0f0f, v15
	v_dot4c_i32_i8_e32 v16, v12, v34
	v_lshrrev_b32_e32 v12, 4, v15
	v_and_b32_e32 v12, 0xf0f0f0f, v12
	v_dot4c_i32_i8_e32 v16, v12, v35
	v_and_b32_e32 v12, 0xf0f0f0f, v8
	v_mov_b32_e32 v13, 0
	v_lshrrev_b32_e32 v8, 4, v8
	v_dot4c_i32_i8_e32 v13, v12, v36
	v_and_b32_e32 v8, 0xf0f0f0f, v8
	v_dot4c_i32_i8_e32 v13, v8, v37
	v_and_b32_e32 v8, 0xf0f0f0f, v9
	v_mov_b32_e32 v12, 0
	v_dot4c_i32_i8_e32 v12, v8, v38
	v_lshrrev_b32_e32 v8, 4, v9
	v_and_b32_e32 v8, 0xf0f0f0f, v8
	v_dot4c_i32_i8_e32 v12, v8, v39
	v_and_b32_e32 v8, 0xf0f0f0f, v10
	v_dot4c_i32_i8_e32 v13, v8, v32
	v_lshrrev_b32_e32 v8, 4, v10
	v_and_b32_e32 v8, 0xf0f0f0f, v8
	v_dot4c_i32_i8_e32 v13, v8, v33
	v_and_b32_e32 v8, 0xf0f0f0f, v11
	v_dot4c_i32_i8_e32 v12, v8, v34
	v_lshrrev_b32_e32 v8, 4, v11
	v_and_b32_e32 v8, 0xf0f0f0f, v8
	v_dot4c_i32_i8_e32 v12, v8, v35
	v_add_u32_e32 v11, v17, v16
	s_waitcnt vmcnt(8)
	v_and_b32_e32 v9, 0xffff0000, v237
	v_and_b32_e32 v8, 0xffff0000, v236
	v_add_u32_e32 v10, v13, v12
	v_sub_u32_e32 v12, v11, v78
	v_sub_u32_e32 v10, v10, v78
	v_cvt_f32_i32_e32 v11, v10
	v_cvt_f32_i32_e32 v10, v12
	s_waitcnt vmcnt(7)
	v_and_b32_e32 v89, 0xf0f0f0f, v68
	v_lshrrev_b32_e32 v68, 4, v68
	v_dot4c_i32_i8_e32 v90, v89, v36
	v_pk_fma_f32 v[106:107], v[8:9], v[10:11], v[106:107]
	v_and_b32_e32 v8, 0xf0f0f0f, v4
	v_mov_b32_e32 v9, 0
	v_lshrrev_b32_e32 v4, 4, v4
	v_dot4c_i32_i8_e32 v9, v8, v36
	v_and_b32_e32 v4, 0xf0f0f0f, v4
	v_dot4c_i32_i8_e32 v9, v4, v37
	v_and_b32_e32 v4, 0xf0f0f0f, v5
	v_mov_b32_e32 v8, 0
	v_dot4c_i32_i8_e32 v8, v4, v38
	v_lshrrev_b32_e32 v4, 4, v5
	v_and_b32_e32 v4, 0xf0f0f0f, v4
	v_dot4c_i32_i8_e32 v8, v4, v39
	v_and_b32_e32 v4, 0xf0f0f0f, v6
	v_dot4c_i32_i8_e32 v9, v4, v32
	v_lshrrev_b32_e32 v4, 4, v6
	v_and_b32_e32 v4, 0xf0f0f0f, v4
	v_dot4c_i32_i8_e32 v9, v4, v33
	v_and_b32_e32 v4, 0xf0f0f0f, v7
	v_dot4c_i32_i8_e32 v8, v4, v34
	v_lshrrev_b32_e32 v4, 4, v7
	v_and_b32_e32 v4, 0xf0f0f0f, v4
	v_dot4c_i32_i8_e32 v8, v4, v35
	v_and_b32_e32 v4, 0xf0f0f0f, v0
	v_mov_b32_e32 v5, 0
	v_lshrrev_b32_e32 v0, 4, v0
	v_dot4c_i32_i8_e32 v5, v4, v36
	v_and_b32_e32 v0, 0xf0f0f0f, v0
	v_dot4c_i32_i8_e32 v5, v0, v37
	v_and_b32_e32 v0, 0xf0f0f0f, v1
	v_mov_b32_e32 v4, 0
	v_dot4c_i32_i8_e32 v4, v0, v38
	v_lshrrev_b32_e32 v0, 4, v1
	v_and_b32_e32 v0, 0xf0f0f0f, v0
	v_dot4c_i32_i8_e32 v4, v0, v39
	v_and_b32_e32 v0, 0xf0f0f0f, v2
	v_dot4c_i32_i8_e32 v5, v0, v32
	v_lshrrev_b32_e32 v0, 4, v2
	v_and_b32_e32 v0, 0xf0f0f0f, v0
	v_dot4c_i32_i8_e32 v5, v0, v33
	v_and_b32_e32 v0, 0xf0f0f0f, v3
	v_dot4c_i32_i8_e32 v4, v0, v34
	v_lshrrev_b32_e32 v0, 4, v3
	v_and_b32_e32 v0, 0xf0f0f0f, v0
	v_dot4c_i32_i8_e32 v4, v0, v35
	v_add_u32_e32 v3, v9, v8
	v_and_b32_e32 v1, 0xffff0000, v239
	v_and_b32_e32 v0, 0xffff0000, v238
	v_add_u32_e32 v2, v5, v4
	v_sub_u32_e32 v4, v3, v78
	v_sub_u32_e32 v2, v2, v78
	v_cvt_f32_i32_e32 v3, v2
	v_cvt_f32_i32_e32 v2, v4
	v_and_b32_e32 v68, 0xf0f0f0f, v68
	v_dot4c_i32_i8_e32 v90, v68, v37
	v_and_b32_e32 v68, 0xf0f0f0f, v69
	v_pk_fma_f32 v[104:105], v[0:1], v[2:3], v[104:105]
	ds_read_u16 v0, v93 offset:16384
	ds_read_u16 v1, v93 offset:16400
	ds_read_u16 v2, v93 offset:16416
	ds_read_u16 v3, v93 offset:16432
	v_mov_b32_e32 v89, 0
	s_waitcnt lgkmcnt(3)
	v_add_u32_e32 v0, s44, v0
	v_lshl_or_b32 v4, v0, 7, v165
	v_lshl_or_b32 v0, v0, 5, v248
	global_load_dwordx4 v[28:31], v4, s[0:1]
	global_load_dword v184, v0, s[46:47]
	s_waitcnt lgkmcnt(2)
	v_add_u32_e32 v0, s44, v1
	v_dot4c_i32_i8_e32 v89, v68, v38
	v_lshrrev_b32_e32 v68, 4, v69
	v_lshl_or_b32 v1, v0, 7, v165
	v_lshl_or_b32 v0, v0, 5, v248
	v_and_b32_e32 v68, 0xf0f0f0f, v68
	global_load_dwordx4 v[24:27], v1, s[0:1]
	global_load_dword v185, v0, s[46:47]
	s_waitcnt lgkmcnt(1)
	v_add_u32_e32 v0, s44, v2
	v_dot4c_i32_i8_e32 v89, v68, v39
	v_and_b32_e32 v68, 0xf0f0f0f, v70
	v_lshl_or_b32 v1, v0, 7, v165
	v_lshl_or_b32 v0, v0, 5, v248
	v_dot4c_i32_i8_e32 v90, v68, v32
	v_lshrrev_b32_e32 v68, 4, v70
	global_load_dwordx4 v[20:23], v1, s[0:1]
	global_load_dword v186, v0, s[46:47]
	s_waitcnt lgkmcnt(0)
	v_add_u32_e32 v0, s44, v3
	v_and_b32_e32 v68, 0xf0f0f0f, v68
	v_lshl_or_b32 v1, v0, 7, v165
	v_lshl_or_b32 v0, v0, 5, v248
	v_dot4c_i32_i8_e32 v90, v68, v33
	v_and_b32_e32 v68, 0xf0f0f0f, v71
	global_load_dwordx4 v[16:19], v1, s[0:1]
	global_load_dword v187, v0, s[46:47]
	ds_read_u16 v0, v93 offset:16448
	v_dot4c_i32_i8_e32 v89, v68, v34
	v_lshrrev_b32_e32 v68, 4, v71
	v_and_b32_e32 v68, 0xf0f0f0f, v68
	v_dot4c_i32_i8_e32 v89, v68, v35
	s_waitcnt vmcnt(14)
	v_and_b32_e32 v68, 0xf0f0f0f, v64
	v_mov_b32_e32 v69, 0
	v_lshrrev_b32_e32 v64, 4, v64
	v_dot4c_i32_i8_e32 v69, v68, v36
	v_and_b32_e32 v64, 0xf0f0f0f, v64
	v_dot4c_i32_i8_e32 v69, v64, v37
	v_and_b32_e32 v64, 0xf0f0f0f, v65
	v_mov_b32_e32 v68, 0
	s_waitcnt lgkmcnt(0)
; #define P12_ISSUE(c_, i_, h_, CW_, SC_) do { _Pragma("unroll") for (int bb = 0; bb < 8; ++bb) { const unsigned ro = (unsigned)(c_) * 16384u + (unsigned)EL[(i_) * 128 + ((h_) * 8 + bb) * 8 + g8]; \
;         CW_[bb] = *(const v4u*)(U4 + (size_t)(ro * 128u + 16u * (unsigned)k8)); SC_[bb] = USS[(size_t)(ro * 8u + (unsigned)k8)]; } } while (0)
; #define P12_COMP(i_, h_, CW_, SC_) do { _Pragma("unroll") for (int bb = 0; bb < 8; ++bb) { int a0 = 0, a1 = 0; P12_U4(CW_[bb].x, xa.x, xa.y, a0); P12_U4(CW_[bb].y, xa.z, xa.w, a1); P12_U4(CW_[bb].z, xb.x, xb.y, a0); P12_U4(CW_[bb].w, xb.z, xb.w, a1); \
;         psum[(i_)][(h_) * 8 + bb] += __uint_as_float(SC_[bb] << 16) * (float)((a0 + a1) - xo); } } while (0)
; #define P12_BAR() asm volatile("" ::: "memory")
; __device__ __forceinline__ void p12_peer(Frame& F) {
;     ...
;     { v4u cwA[8], cwB[8]; unsigned scA[8], scB[8]; v4u xa, xb; int xo;
;       P12_ISSUE(0, 0, 0, cwA, scA);
; _Pragma("nounroll")
;       for (int c = 0; c < 16; ++c) { const int cn = c + 1 < 16 ? c + 1 : 15;
;           P12_XQ(c, 0); P12_ISSUE(c, 0, 1, cwB, scB); P12_BAR(); P12_COMP(0, 0, cwA, scA); P12_ISSUE(c, 1, 0, cwA, scA); P12_BAR(); P12_COMP(0, 1, cwB, scB);
;           P12_XQ(c, 1); P12_ISSUE(c, 1, 1, cwB, scB); P12_BAR(); P12_COMP(1, 0, cwA, scA); P12_ISSUE(c, 2, 0, cwA, scA); P12_BAR(); P12_COMP(1, 1, cwB, scB);
;           P12_XQ(c, 2); P12_ISSUE(c, 2, 1, cwB, scB); P12_BAR(); P12_COMP(2, 0, cwA, scA); P12_ISSUE(c, 3, 0, cwA, scA); P12_BAR(); P12_COMP(2, 1, cwB, scB);
;           P12_XQ(c, 3); P12_ISSUE(c, 3, 1, cwB, scB); P12_BAR(); P12_COMP(3, 0, cwA, scA); P12_ISSUE(cn, 0, 0, cwA, scA); P12_BAR(); P12_COMP(3, 1, cwB, scB);
	v_add_u32_e32 v0, s44, v0
	v_dot4c_i32_i8_e32 v68, v64, v38
	v_lshrrev_b32_e32 v64, 4, v65
	v_lshl_or_b32 v1, v0, 7, v165
	v_lshl_or_b32 v0, v0, 5, v248
	v_and_b32_e32 v64, 0xf0f0f0f, v64
	global_load_dwordx4 v[12:15], v1, s[0:1]
	global_load_dword v188, v0, s[46:47]
	ds_read_u16 v0, v93 offset:16464
	v_dot4c_i32_i8_e32 v68, v64, v39
	v_and_b32_e32 v64, 0xf0f0f0f, v66
	v_dot4c_i32_i8_e32 v69, v64, v32
	v_lshrrev_b32_e32 v64, 4, v66
	v_and_b32_e32 v64, 0xf0f0f0f, v64
	v_dot4c_i32_i8_e32 v69, v64, v33
	v_and_b32_e32 v64, 0xf0f0f0f, v67
	v_dot4c_i32_i8_e32 v68, v64, v34
	v_lshrrev_b32_e32 v64, 4, v67
	s_waitcnt lgkmcnt(0)
	v_add_u32_e32 v0, s44, v0
	v_and_b32_e32 v64, 0xf0f0f0f, v64
	v_lshl_or_b32 v1, v0, 7, v165
	v_lshl_or_b32 v0, v0, 5, v248
	v_dot4c_i32_i8_e32 v68, v64, v35
	global_load_dwordx4 v[8:11], v1, s[0:1]
	global_load_dword v189, v0, s[46:47]
	ds_read_u16 v0, v93 offset:16480
	v_add_u32_e32 v66, v90, v89
	v_sub_u32_e32 v67, v68, v78
	v_add_u32_e32 v67, v67, v69
	v_sub_u32_e32 v66, v66, v78
	v_cvt_f32_i32_e32 v66, v66
	v_cvt_f32_i32_e32 v67, v67
	s_waitcnt lgkmcnt(0)
	v_add_u32_e32 v0, s44, v0
	s_waitcnt vmcnt(12)
	v_and_b32_e32 v65, 0xffff0000, v241
	v_and_b32_e32 v64, 0xffff0000, v240
	v_lshl_or_b32 v1, v0, 7, v165
	v_lshl_or_b32 v0, v0, 5, v248
	v_pk_fma_f32 v[102:103], v[64:65], v[66:67], v[102:103]
	v_and_b32_e32 v64, 0xf0f0f0f, v60
	v_mov_b32_e32 v65, 0
	v_lshrrev_b32_e32 v60, 4, v60
	global_load_dwordx4 v[4:7], v1, s[0:1]
	global_load_dword v190, v0, s[46:47]
	ds_read_u16 v0, v93 offset:16496
	v_dot4c_i32_i8_e32 v65, v64, v36
	v_and_b32_e32 v60, 0xf0f0f0f, v60
	v_dot4c_i32_i8_e32 v65, v60, v37
	v_and_b32_e32 v60, 0xf0f0f0f, v61
	v_mov_b32_e32 v64, 0
	v_dot4c_i32_i8_e32 v64, v60, v38
	v_lshrrev_b32_e32 v60, 4, v61
	v_and_b32_e32 v60, 0xf0f0f0f, v60
	v_dot4c_i32_i8_e32 v64, v60, v39
	v_and_b32_e32 v60, 0xf0f0f0f, v62
	s_waitcnt lgkmcnt(0)
	v_add_u32_e32 v88, s44, v0
	v_dot4c_i32_i8_e32 v65, v60, v32
	v_lshrrev_b32_e32 v60, 4, v62
	v_lshl_or_b32 v0, v88, 7, v165
	v_lshl_or_b32 v88, v88, 5, v248
	v_and_b32_e32 v60, 0xf0f0f0f, v60
	global_load_dwordx4 v[0:3], v0, s[0:1]
	v_dot4c_i32_i8_e32 v65, v60, v33
	global_load_dword v191, v88, s[46:47]
	v_and_b32_e32 v60, 0xf0f0f0f, v63
	v_dot4c_i32_i8_e32 v64, v60, v34
	v_lshrrev_b32_e32 v60, 4, v63
	v_and_b32_e32 v60, 0xf0f0f0f, v60
	v_dot4c_i32_i8_e32 v64, v60, v35
	v_and_b32_e32 v60, 0xf0f0f0f, v56
	v_mov_b32_e32 v61, 0
	v_lshrrev_b32_e32 v56, 4, v56
	v_dot4c_i32_i8_e32 v61, v60, v36
	v_and_b32_e32 v56, 0xf0f0f0f, v56
	v_dot4c_i32_i8_e32 v61, v56, v37
	v_and_b32_e32 v56, 0xf0f0f0f, v57
	v_mov_b32_e32 v60, 0
	v_dot4c_i32_i8_e32 v60, v56, v38
	v_lshrrev_b32_e32 v56, 4, v57
	v_and_b32_e32 v56, 0xf0f0f0f, v56
	v_dot4c_i32_i8_e32 v60, v56, v39
	v_and_b32_e32 v56, 0xf0f0f0f, v58
	v_dot4c_i32_i8_e32 v61, v56, v32
	v_lshrrev_b32_e32 v56, 4, v58
	v_and_b32_e32 v56, 0xf0f0f0f, v56
	v_dot4c_i32_i8_e32 v61, v56, v33
	v_and_b32_e32 v56, 0xf0f0f0f, v59
	v_dot4c_i32_i8_e32 v60, v56, v34
	v_lshrrev_b32_e32 v56, 4, v59
	v_and_b32_e32 v56, 0xf0f0f0f, v56
	v_dot4c_i32_i8_e32 v60, v56, v35
	v_sub_u32_e32 v59, v64, v78
	s_waitcnt vmcnt(16)
	v_and_b32_e32 v57, 0xffff0000, v243
	v_and_b32_e32 v56, 0xffff0000, v242
	v_sub_u32_e32 v58, v60, v78
	v_add_u32_e32 v60, v59, v65
	v_add_u32_e32 v58, v58, v61
	v_cvt_f32_i32_e32 v59, v58
	v_cvt_f32_i32_e32 v58, v60
	s_mov_b32 s44, s45
	v_pk_fma_f32 v[100:101], v[56:57], v[58:59], v[100:101]
	v_and_b32_e32 v56, 0xf0f0f0f, v52
	v_mov_b32_e32 v57, 0
	v_lshrrev_b32_e32 v52, 4, v52
	v_dot4c_i32_i8_e32 v57, v56, v36
	v_and_b32_e32 v52, 0xf0f0f0f, v52
	v_dot4c_i32_i8_e32 v57, v52, v37
	v_and_b32_e32 v52, 0xf0f0f0f, v53
	v_mov_b32_e32 v56, 0
	v_dot4c_i32_i8_e32 v56, v52, v38
	v_lshrrev_b32_e32 v52, 4, v53
	v_and_b32_e32 v52, 0xf0f0f0f, v52
	v_dot4c_i32_i8_e32 v56, v52, v39
	v_and_b32_e32 v52, 0xf0f0f0f, v54
	v_dot4c_i32_i8_e32 v57, v52, v32
	v_lshrrev_b32_e32 v52, 4, v54
	v_and_b32_e32 v52, 0xf0f0f0f, v52
	v_dot4c_i32_i8_e32 v57, v52, v33
	v_and_b32_e32 v52, 0xf0f0f0f, v55
	v_dot4c_i32_i8_e32 v56, v52, v34
	v_lshrrev_b32_e32 v52, 4, v55
	v_and_b32_e32 v52, 0xf0f0f0f, v52
	v_dot4c_i32_i8_e32 v56, v52, v35
	v_and_b32_e32 v52, 0xf0f0f0f, v48
	v_mov_b32_e32 v53, 0
	v_lshrrev_b32_e32 v48, 4, v48
	v_dot4c_i32_i8_e32 v53, v52, v36
	v_and_b32_e32 v48, 0xf0f0f0f, v48
	v_dot4c_i32_i8_e32 v53, v48, v37
	v_and_b32_e32 v48, 0xf0f0f0f, v49
	v_mov_b32_e32 v52, 0
	v_dot4c_i32_i8_e32 v52, v48, v38
	v_lshrrev_b32_e32 v48, 4, v49
	v_and_b32_e32 v48, 0xf0f0f0f, v48
	v_dot4c_i32_i8_e32 v52, v48, v39
	v_and_b32_e32 v48, 0xf0f0f0f, v50
	v_dot4c_i32_i8_e32 v53, v48, v32
	v_lshrrev_b32_e32 v48, 4, v50
	v_and_b32_e32 v48, 0xf0f0f0f, v48
	v_dot4c_i32_i8_e32 v53, v48, v33
	v_and_b32_e32 v48, 0xf0f0f0f, v51
	v_dot4c_i32_i8_e32 v52, v48, v34
	v_lshrrev_b32_e32 v48, 4, v51
	v_and_b32_e32 v48, 0xf0f0f0f, v48
	v_dot4c_i32_i8_e32 v52, v48, v35
	v_sub_u32_e32 v51, v56, v78
	s_waitcnt vmcnt(16)
; #define P12_ISSUE(c_, i_, h_, CW_, SC_) do { _Pragma("unroll") for (int bb = 0; bb < 8; ++bb) { const unsigned ro = (unsigned)(c_) * 16384u + (unsigned)EL[(i_) * 128 + ((h_) * 8 + bb) * 8 + g8]; \
;         CW_[bb] = *(const v4u*)(U4 + (size_t)(ro * 128u + 16u * (unsigned)k8)); SC_[bb] = USS[(size_t)(ro * 8u + (unsigned)k8)]; } } while (0)
; #define P12_COMP(i_, h_, CW_, SC_) do { _Pragma("unroll") for (int bb = 0; bb < 8; ++bb) { int a0 = 0, a1 = 0; P12_U4(CW_[bb].x, xa.x, xa.y, a0); P12_U4(CW_[bb].y, xa.z, xa.w, a1); P12_U4(CW_[bb].z, xb.x, xb.y, a0); P12_U4(CW_[bb].w, xb.z, xb.w, a1); \
;         psum[(i_)][(h_) * 8 + bb] += __uint_as_float(SC_[bb] << 16) * (float)((a0 + a1) - xo); } } while (0)
; #define P12_BAR() asm volatile("" ::: "memory")
; __device__ __forceinline__ void p12_peer(Frame& F) {
;     ...
;     { v4u cwA[8], cwB[8]; unsigned scA[8], scB[8]; v4u xa, xb; int xo;
;       P12_ISSUE(0, 0, 0, cwA, scA);
; _Pragma("nounroll")
;       for (int c = 0; c < 16; ++c) { const int cn = c + 1 < 16 ? c + 1 : 15;
;           P12_XQ(c, 0); P12_ISSUE(c, 0, 1, cwB, scB); P12_BAR(); P12_COMP(0, 0, cwA, scA); P12_ISSUE(c, 1, 0, cwA, scA); P12_BAR(); P12_COMP(0, 1, cwB, scB);
;           P12_XQ(c, 1); P12_ISSUE(c, 1, 1, cwB, scB); P12_BAR(); P12_COMP(1, 0, cwA, scA); P12_ISSUE(c, 2, 0, cwA, scA); P12_BAR(); P12_COMP(1, 1, cwB, scB);
;           P12_XQ(c, 2); P12_ISSUE(c, 2, 1, cwB, scB); P12_BAR(); P12_COMP(2, 0, cwA, scA); P12_ISSUE(c, 3, 0, cwA, scA); P12_BAR(); P12_COMP(2, 1, cwB, scB);
;           P12_XQ(c, 3); P12_ISSUE(c, 3, 1, cwB, scB); P12_BAR(); P12_COMP(3, 0, cwA, scA); P12_ISSUE(cn, 0, 0, cwA, scA); P12_BAR(); P12_COMP(3, 1, cwB, scB);
	v_and_b32_e32 v49, 0xffff0000, v245
	v_and_b32_e32 v48, 0xffff0000, v244
	v_sub_u32_e32 v50, v52, v78
	v_add_u32_e32 v52, v51, v57
	v_add_u32_e32 v50, v50, v53
	v_cvt_f32_i32_e32 v51, v50
	v_cvt_f32_i32_e32 v50, v52
	v_pk_fma_f32 v[98:99], v[48:49], v[50:51], v[98:99]
	v_and_b32_e32 v48, 0xf0f0f0f, v44
	v_mov_b32_e32 v49, 0
	v_lshrrev_b32_e32 v44, 4, v44
	v_dot4c_i32_i8_e32 v49, v48, v36
	v_and_b32_e32 v44, 0xf0f0f0f, v44
	v_dot4c_i32_i8_e32 v49, v44, v37
	v_and_b32_e32 v44, 0xf0f0f0f, v45
	v_mov_b32_e32 v48, 0
	v_dot4c_i32_i8_e32 v48, v44, v38
	v_lshrrev_b32_e32 v44, 4, v45
	v_and_b32_e32 v44, 0xf0f0f0f, v44
	v_dot4c_i32_i8_e32 v48, v44, v39
	v_and_b32_e32 v44, 0xf0f0f0f, v46
	v_dot4c_i32_i8_e32 v49, v44, v32
	v_lshrrev_b32_e32 v44, 4, v46
	v_and_b32_e32 v44, 0xf0f0f0f, v44
	v_dot4c_i32_i8_e32 v49, v44, v33
	v_and_b32_e32 v44, 0xf0f0f0f, v47
	v_dot4c_i32_i8_e32 v48, v44, v34
	v_lshrrev_b32_e32 v44, 4, v47
	v_and_b32_e32 v44, 0xf0f0f0f, v44
	v_dot4c_i32_i8_e32 v48, v44, v35
	v_and_b32_e32 v44, 0xf0f0f0f, v40
	v_mov_b32_e32 v45, 0
	v_dot4c_i32_i8_e32 v45, v44, v36
	v_lshrrev_b32_e32 v36, 4, v40
	v_and_b32_e32 v36, 0xf0f0f0f, v36
	v_dot4c_i32_i8_e32 v45, v36, v37
	v_and_b32_e32 v36, 0xf0f0f0f, v41
	v_mov_b32_e32 v37, 0
	v_dot4c_i32_i8_e32 v37, v36, v38
	v_lshrrev_b32_e32 v36, 4, v41
	v_and_b32_e32 v36, 0xf0f0f0f, v36
	v_dot4c_i32_i8_e32 v37, v36, v39
	v_and_b32_e32 v36, 0xf0f0f0f, v42
	v_dot4c_i32_i8_e32 v45, v36, v32
	v_lshrrev_b32_e32 v32, 4, v42
	v_and_b32_e32 v32, 0xf0f0f0f, v32
	v_dot4c_i32_i8_e32 v45, v32, v33
	v_and_b32_e32 v32, 0xf0f0f0f, v43
	v_dot4c_i32_i8_e32 v37, v32, v34
	v_lshrrev_b32_e32 v32, 4, v43
	v_and_b32_e32 v32, 0xf0f0f0f, v32
	v_dot4c_i32_i8_e32 v37, v32, v35
	v_sub_u32_e32 v35, v48, v78
	v_add_u32_e32 v36, v35, v49
	s_waitcnt vmcnt(16)
	v_and_b32_e32 v33, 0xffff0000, v247
	v_sub_u32_e32 v34, v37, v78
	v_add_u32_e32 v34, v34, v45
	v_cvt_f32_i32_e32 v35, v34
	v_cvt_f32_i32_e32 v34, v36
	v_and_b32_e32 v32, 0xffff0000, v246
	s_waitcnt vmcnt(0)
	v_perm_b32 v40, v190, v191, s43
	v_perm_b32 v41, v188, v189, s43
	v_pk_fma_f32 v[96:97], v[32:33], v[34:35], v[96:97]
	v_perm_b32 v42, v186, v187, s43
	v_perm_b32 v43, v184, v185, s43
	s_cbranch_scc0 .LBB0_3272
; #define LDS_WAIT() asm volatile("s_waitcnt lgkmcnt(0)" ::: "memory")
; __device__ __forceinline__ float wave_sum(float v) { v = dpp_add16(v); return (rdlane(v, 0) + rdlane(v, 16)) + (rdlane(v, 32) + rdlane(v, 48)); }
; __device__ __forceinline__ float wave_max(float v) { v = dpp_max16(v); return fmaxf(fmaxf(rdlane(v, 0), rdlane(v, 16)), fmaxf(rdlane(v, 32), rdlane(v, 48))); }
; __device__ __forceinline__ void p12_peer(Frame& F) {
;     ...
;         mxa = wave_max(mxa); const float inv = mxa > 0.f ? 127.0f / mxa : 0.f;
;         const float rsn = 1.0f / sqrtf(wave_sum(PSQ[(size_t)t * 64 + F.lane]) * (1.f / D_) + 1e-6f);
;         sx[i] = mxa * rsn * (1.0f / 127.0f);
;     ...
;     asm volatile("" ::: "memory"); LDS_WAIT();
; #pragma unroll
;     for (int i = 0; i < 4; ++i) { const int t = F.gw + i * F.NGW;
; #pragma unroll
;         for (int b = 0; b < 16; ++b) { float d = psum[i][b];
;             d += __builtin_bit_cast(float, __builtin_amdgcn_update_dpp(0, __builtin_bit_cast(int, d), 0xB1, 0xF, 0xF, false));
;             d += __builtin_bit_cast(float, __builtin_amdgcn_update_dpp(0, __builtin_bit_cast(int, d), 0x4E, 0xF, 0xF, false));
;             d += __builtin_bit_cast(float, __builtin_amdgcn_update_dpp(0, __builtin_bit_cast(int, d), 0x141, 0xF, 0xF, false));
;             const int idx = b * 8 + g8; const float w = PGT[(size_t)t * 128 + idx] * gelu_erf(sx[i] * d) * VSC[EL[i * 128 + idx]];
;             if (k8 == 0) WL[i * 128 + idx] = w; } }
	v_mov_b32_e32 v0, s41
	v_mov_b32_e32 v1, s42
	v_add_f32_e32 v0, s39, v0
	v_add_f32_e32 v1, s40, v1
	v_add_f32_e32 v0, v0, v1
	v_mov_b32_e32 v1, 0x358637bd
	v_fmac_f32_e32 v1, 0x39800000, v0
	s_mov_b32 s0, 0xf800000
	v_mul_f32_e32 v0, 0x4f800000, v1
	v_cmp_gt_f32_e32 vcc, s0, v1
	s_add_u32 s43, s68, 0x1200000
	s_addc_u32 s44, s69, 0
	v_cndmask_b32_e32 v0, v1, v0, vcc
	v_sqrt_f32_e32 v1, v0
	s_add_u32 s18, s68, 0xf000000
	s_addc_u32 s19, s69, 0
	v_add_u32_e32 v2, -1, v1
	v_fma_f32 v3, -v2, v1, v0
	v_cmp_ge_f32_e64 s[0:1], 0, v3
	v_add_u32_e32 v3, 1, v1
	s_add_u32 s2, s43, s2
	v_cndmask_b32_e64 v2, v1, v2, s[0:1]
	v_fma_f32 v1, -v3, v1, v0
	v_cmp_lt_f32_e64 s[0:1], 0, v1
	s_waitcnt lgkmcnt(0)
	s_addc_u32 s3, s44, s3
	v_ashrrev_i32_e32 v95, 31, v94
	v_cndmask_b32_e64 v1, v2, v3, s[0:1]
	v_mul_f32_e32 v2, 0x37800000, v1
	v_cndmask_b32_e32 v1, v1, v2, vcc
	v_mov_b32_e32 v2, 0x260
	v_cmp_class_f32_e32 vcc, v0, v2
	s_nop 1
	v_cndmask_b32_e32 v2, v1, v0, vcc
	v_div_scale_f32 v3, s[0:1], v2, v2, 1.0
	v_rcp_f32_e32 v4, v3
	v_lshl_add_u64 v[0:1], v[94:95], 2, s[2:3]
	ds_read_u16 v20, v93 offset:16384
	ds_read_u16 v21, v93 offset:16400
	ds_read_u16 v22, v93 offset:16416
	ds_read_u16 v23, v93 offset:16432
	ds_read_u16 v24, v93 offset:16448
	ds_read_u16 v25, v93 offset:16464
	ds_read_u16 v26, v93 offset:16480
	ds_read_u16 v27, v93 offset:16496
	s_waitcnt lgkmcnt(0)
	ds_read_u16 v28, v93 offset:16512
	ds_read_u16 v29, v93 offset:16528
	ds_read_u16 v30, v93 offset:16544
	ds_read_u16 v31, v93 offset:16560
	ds_read_u16 v32, v93 offset:16576
	ds_read_u16 v33, v93 offset:16592
	ds_read_u16 v34, v93 offset:16608
	ds_read_u16 v35, v93 offset:16624
	s_waitcnt lgkmcnt(0)
	v_lshlrev_b32_e32 v20, 2, v20
	v_lshlrev_b32_e32 v21, 2, v21
	v_lshlrev_b32_e32 v22, 2, v22
	v_lshlrev_b32_e32 v23, 2, v23
	v_lshlrev_b32_e32 v24, 2, v24
	v_lshlrev_b32_e32 v25, 2, v25
	v_lshlrev_b32_e32 v26, 2, v26
	v_lshlrev_b32_e32 v27, 2, v27
	v_lshlrev_b32_e32 v28, 2, v28
	v_lshlrev_b32_e32 v29, 2, v29
	v_lshlrev_b32_e32 v30, 2, v30
	v_lshlrev_b32_e32 v31, 2, v31
	v_lshlrev_b32_e32 v32, 2, v32
	v_lshlrev_b32_e32 v33, 2, v33
	v_lshlrev_b32_e32 v34, 2, v34
	v_lshlrev_b32_e32 v35, 2, v35
	global_load_dword v40, v[0:1], off offset:0
	global_load_dword v60, v20, s[18:19]
	global_load_dword v41, v[0:1], off offset:32
	global_load_dword v61, v21, s[18:19]
	global_load_dword v42, v[0:1], off offset:64
	global_load_dword v62, v22, s[18:19]
	global_load_dword v43, v[0:1], off offset:96
	global_load_dword v63, v23, s[18:19]
	global_load_dword v44, v[0:1], off offset:128
	global_load_dword v64, v24, s[18:19]
	global_load_dword v45, v[0:1], off offset:160
	global_load_dword v65, v25, s[18:19]
	global_load_dword v46, v[0:1], off offset:192
	global_load_dword v66, v26, s[18:19]
	global_load_dword v47, v[0:1], off offset:224
	global_load_dword v67, v27, s[18:19]
	global_load_dword v48, v[0:1], off offset:256
	global_load_dword v68, v28, s[18:19]
	global_load_dword v49, v[0:1], off offset:288
	global_load_dword v69, v29, s[18:19]
	global_load_dword v50, v[0:1], off offset:320
	global_load_dword v70, v30, s[18:19]
	global_load_dword v51, v[0:1], off offset:352
	global_load_dword v71, v31, s[18:19]
	global_load_dword v52, v[0:1], off offset:384
	global_load_dword v72, v32, s[18:19]
	global_load_dword v53, v[0:1], off offset:416
	global_load_dword v73, v33, s[18:19]
	global_load_dword v54, v[0:1], off offset:448
	global_load_dword v74, v34, s[18:19]
	global_load_dword v55, v[0:1], off offset:480
	global_load_dword v75, v35, s[18:19]
	s_waitcnt vmcnt(0)
	v_cmp_eq_u32_e64 s[0:1], 0, v164
	v_fma_f32 v5, -v3, v4, 1.0
	v_fmac_f32_e32 v4, v5, v4
	v_div_scale_f32 v5, vcc, 1.0, v2, 1.0
	v_mul_f32_e32 v6, v5, v4
	v_fma_f32 v7, -v3, v6, v5
	v_fmac_f32_e32 v6, v7, v4
	v_fma_f32 v3, -v3, v6, v5
	v_div_fmas_f32 v3, v3, v4, v6
	v_div_fixup_f32 v2, v3, v2, 1.0
	v_add_f32_dpp v5, v159, v159 quad_perm:[1,0,3,2] row_mask:0xf bank_mask:0xf bound_ctrl:1
	v_mul_f32_e32 v3, v163, v2
	v_mov_b32_e32 v6, 0
	v_add_f32_dpp v5, v5, v5 quad_perm:[2,3,0,1] row_mask:0xf bank_mask:0xf bound_ctrl:1
	v_mov_b32_e32 v4, 0
	v_lshl_add_u32 v2, v94, 2, s20
	v_mul_f32_e32 v3, 0x3c010204, v3
	v_mov_b32_dpp v6, v5 row_half_mirror row_mask:0xf bank_mask:0xf
	s_and_saveexec_b64 s[2:3], s[0:1]
	s_cbranch_execz .LBB0_3275
	v_add_f32_e32 v5, v5, v6
	v_mul_f32_e32 v5, v3, v5
	s_mov_b32 s39, 0x3e6d3388
	v_mul_f32_e32 v6, v5, v5
	s_waitcnt lgkmcnt(0)
	v_fma_f32 v7, |v5|, s39, 1.0
	v_rcp_f32_e32 v7, v7
	v_mov_b32_e32 v10, 0xbf3a00e3
	v_mul_f32_e32 v6, 0xbf38aa3b, v6
	v_exp_f32_e32 v6, v6
	v_fmac_f32_e32 v10, 0x3f07dc22, v7
	v_fmaak_f32 v10, v7, v10, 0x3f35f0e3
	v_fmaak_f32 v10, v7, v10, 0xbe11a98e
	v_fmaak_f32 v10, v7, v10, 0x3e027906
	v_mul_f32_e32 v7, v7, v10
	v_mul_f32_e32 v6, v6, v7
	v_mul_f32_e32 v7, v5, v6
	v_fma_f32 v6, -v5, v6, v5
	v_cmp_gt_f32_e32 vcc, 0, v5
	s_nop 1
	v_cndmask_b32_e32 v5, v6, v7, vcc
	s_waitcnt vmcnt(1)
	v_mul_f32_e32 v5, v5, v40
	s_waitcnt vmcnt(0)
	v_mul_f32_e32 v5, v5, v60
	ds_write_b32 v2, v5
